# baseline (speedup 1.0000x reference)
.LBB7_6:
	s_andn2_b64 vcc, exec, s[4:5]
	s_cbranch_vccnz .LBB7_70
	s_load_dwordx4 s[4:7], s[0:1], 0x0
	s_load_dwordx2 s[8:9], s[0:1], 0x10
	v_lshrrev_b32_e32 v80, 3, v0
	v_and_b32_e32 v81, 24, v80
	s_lshl_b32 s24, s2, 5
	v_and_b32_e32 v82, 63, v0
	v_or_b32_e32 v72, s24, v81
	v_lshlrev_b32_e32 v2, 5, v82
	v_mov_b32_e32 v3, 0
	v_ashrrev_i32_e32 v73, 31, v72
	s_waitcnt lgkmcnt(0)
	v_lshl_add_u64 v[70:71], s[4:5], 0, v[2:3]
	v_lshlrev_b64 v[2:3], 11, v[72:73]
	v_lshl_add_u64 v[2:3], v[70:71], 0, v[2:3]
	v_lshlrev_b32_e32 v74, 8, v82
	global_load_dwordx4 v[84:87], v[2:3], off
	global_load_dwordx4 v[62:65], v74, s[6:7]
	global_load_dwordx4 v[58:61], v74, s[6:7] offset:16
	global_load_dwordx4 v[54:57], v74, s[6:7] offset:32
	global_load_dwordx4 v[50:53], v74, s[6:7] offset:48
	global_load_dwordx4 v[66:69], v[2:3], off offset:16
	global_load_dwordx4 v[46:49], v74, s[6:7] offset:64
	global_load_dwordx4 v[42:45], v74, s[6:7] offset:80
	global_load_dwordx4 v[26:29], v74, s[6:7] offset:112
	global_load_dwordx4 v[38:41], v74, s[6:7] offset:96
	v_lshrrev_b32_e32 v1, 1, v0
	v_mbcnt_lo_u32_b32 v2, -1, 0
	v_and_b32_e32 v91, 28, v1
	v_mbcnt_hi_u32_b32 v1, -1, v2
	v_and_b32_e32 v2, 64, v1
	v_xor_b32_e32 v3, 32, v1
	v_add_u32_e32 v2, 64, v2
	v_xor_b32_e32 v4, 16, v1
	v_cmp_lt_i32_e32 vcc, v3, v2
	v_xor_b32_e32 v5, 8, v1
	v_xor_b32_e32 v6, 4, v1
	v_cndmask_b32_e32 v75, v1, v3, vcc
	v_cmp_lt_i32_e32 vcc, v4, v2
	global_load_dwordx4 v[18:21], v74, s[6:7] offset:144
	global_load_dwordx4 v[30:33], v74, s[6:7] offset:128
	v_cndmask_b32_e32 v76, v1, v4, vcc
	v_cmp_lt_i32_e32 vcc, v5, v2
	v_xor_b32_e32 v7, 2, v1
	v_xor_b32_e32 v8, 1, v1
	v_cndmask_b32_e32 v77, v1, v5, vcc
	v_cmp_lt_i32_e32 vcc, v6, v2
	v_lshlrev_b32_e32 v78, 2, v76
	v_lshlrev_b32_e32 v79, 2, v75
	v_cndmask_b32_e32 v83, v1, v6, vcc
	v_cmp_lt_i32_e32 vcc, v7, v2
	v_lshlrev_b32_e32 v76, 2, v83
	v_lshlrev_b32_e32 v77, 2, v77
	v_cndmask_b32_e32 v92, v1, v7, vcc
	v_cmp_lt_i32_e32 vcc, v8, v2
	v_lshlrev_b32_e32 v75, 2, v92
	v_and_b32_e32 v88, 32, v0
	v_cndmask_b32_e32 v93, v1, v8, vcc
	global_load_dwordx4 v[22:25], v74, s[6:7] offset:176
	global_load_dwordx4 v[34:37], v74, s[6:7] offset:160
	global_load_dwordx4 v[2:5], v74, s[6:7] offset:240
	global_load_dwordx4 v[6:9], v74, s[6:7] offset:224
	global_load_dwordx4 v[10:13], v74, s[6:7] offset:208
	global_load_dwordx4 v[14:17], v74, s[6:7] offset:192
	global_load_dword v73, v91, s[8:9]
	v_lshlrev_b32_e32 v74, 2, v93
	v_cmp_eq_u32_e64 s[8:9], 0, v88
	v_and_b32_e32 v89, 16, v0
	v_cmp_eq_u32_e64 s[2:3], 0, v89
	v_and_b32_e32 v90, 8, v0
	v_cmp_eq_u32_e64 s[4:5], 0, v90
	s_load_dwordx2 s[14:15], s[0:1], 0x28
	s_waitcnt vmcnt(18)
	v_add_f32_e32 v83, 0, v84
	v_add_f32_e32 v83, v83, v85
	v_add_f32_e32 v83, v83, v86
	v_add_f32_e32 v83, v83, v87
	s_waitcnt vmcnt(17)
	v_fma_f32 v92, v62, v84, 0
	s_waitcnt vmcnt(13)
	v_add_f32_e32 v83, v83, v66
	v_add_f32_e32 v83, v83, v67
	v_add_f32_e32 v83, v83, v68
	v_add_f32_e32 v83, v83, v69
	ds_bpermute_b32 v100, v79, v83
	v_fma_f32 v93, v63, v84, 0
	v_fma_f32 v94, v64, v84, 0
	v_fma_f32 v95, v65, v84, 0
	v_fma_f32 v96, v58, v84, 0
	s_waitcnt lgkmcnt(0)
	v_add_f32_e32 v83, v83, v100
	ds_bpermute_b32 v100, v78, v83
	v_fma_f32 v97, v59, v84, 0
	v_fma_f32 v98, v60, v84, 0
	v_fma_f32 v99, v61, v84, 0
	v_fmac_f32_e32 v92, v54, v85
	s_waitcnt lgkmcnt(0)
	v_add_f32_e32 v83, v83, v100
	s_nop 1
	v_mov_b32_dpp v100, v83 row_ror:8 row_mask:0xf bank_mask:0xf
	v_fmac_f32_e32 v93, v55, v85
	v_fmac_f32_e32 v94, v56, v85
	v_fmac_f32_e32 v95, v57, v85
	v_fmac_f32_e32 v96, v50, v85
	s_waitcnt lgkmcnt(0)
	v_add_f32_e32 v83, v83, v100
	s_nop 1
	v_mov_b32_dpp v104, v83 row_half_mirror row_mask:0xf bank_mask:0xf
	s_nop 1
	v_mov_b32_dpp v100, v104 quad_perm:[3,2,1,0] row_mask:0xf bank_mask:0xf
	v_fmac_f32_e32 v97, v51, v85
	v_fmac_f32_e32 v98, v52, v85
	v_fmac_f32_e32 v99, v53, v85
	s_waitcnt vmcnt(12)
	v_fmac_f32_e32 v92, v46, v86
	s_waitcnt lgkmcnt(0)
	v_add_f32_e32 v83, v83, v100
	s_nop 1
	v_mov_b32_dpp v100, v83 quad_perm:[2,3,0,1] row_mask:0xf bank_mask:0xf
	v_fmac_f32_e32 v93, v47, v86
	v_fmac_f32_e32 v94, v48, v86
	v_fmac_f32_e32 v95, v49, v86
	s_waitcnt vmcnt(11)
	v_fmac_f32_e32 v96, v42, v86
	s_waitcnt lgkmcnt(0)
	v_add_f32_e32 v83, v83, v100
	s_nop 1
	v_mov_b32_dpp v100, v83 quad_perm:[1,0,3,2] row_mask:0xf bank_mask:0xf
	v_fmac_f32_e32 v97, v43, v86
	v_fmac_f32_e32 v98, v44, v86
	v_fmac_f32_e32 v99, v45, v86
	s_waitcnt vmcnt(9)
	v_fmac_f32_e32 v92, v38, v87
	s_waitcnt lgkmcnt(0)
	v_add_f32_e32 v83, v83, v100
	v_fmamk_f32 v85, v83, 0xbb000000, v85
	v_fmamk_f32 v84, v83, 0xbb000000, v84
	v_mul_f32_e32 v85, v85, v85
	v_fmamk_f32 v86, v83, 0xbb000000, v86
	v_fmac_f32_e32 v85, v84, v84
	v_fmac_f32_e32 v93, v39, v87
	v_fmac_f32_e32 v94, v40, v87
	v_fmac_f32_e32 v95, v41, v87
	v_fmac_f32_e32 v96, v26, v87
	v_fmac_f32_e32 v97, v27, v87
	v_fmac_f32_e32 v98, v28, v87
	v_fmac_f32_e32 v99, v29, v87
	v_fmamk_f32 v87, v83, 0xbb000000, v87
	v_fmac_f32_e32 v85, v86, v86
	v_fmamk_f32 v100, v83, 0xbb000000, v66
	v_fmac_f32_e32 v85, v87, v87
	v_fmamk_f32 v101, v83, 0xbb000000, v67
	v_fmac_f32_e32 v85, v100, v100
	v_fmamk_f32 v102, v83, 0xbb000000, v68
	v_fmac_f32_e32 v85, v101, v101
	v_fmamk_f32 v103, v83, 0xbb000000, v69
	v_fmac_f32_e32 v85, v102, v102
	s_waitcnt vmcnt(7)
	v_fmac_f32_e32 v92, v30, v66
	v_fmac_f32_e32 v96, v18, v66
	v_fmac_f32_e32 v85, v103, v103
	v_fmac_f32_e32 v93, v31, v66
	v_fmac_f32_e32 v97, v19, v66
	ds_bpermute_b32 v84, v79, v85
	s_waitcnt vmcnt(5)
	v_fmac_f32_e32 v92, v34, v67
	v_fmac_f32_e32 v96, v22, v67
	v_fmac_f32_e32 v94, v32, v66
	v_fmac_f32_e32 v95, v33, v66
	v_fmac_f32_e32 v98, v20, v66
	v_fmac_f32_e32 v99, v21, v66
	v_fmac_f32_e32 v93, v35, v67
	v_fmac_f32_e32 v97, v23, v67
	s_waitcnt vmcnt(1)
	v_fmac_f32_e32 v92, v14, v68
	v_fmac_f32_e32 v96, v10, v68
	v_fmac_f32_e32 v94, v36, v67
	v_fmac_f32_e32 v95, v37, v67
	v_fmac_f32_e32 v98, v24, v67
	v_fmac_f32_e32 v99, v25, v67
	v_fmac_f32_e32 v93, v15, v68
	v_fmac_f32_e32 v97, v11, v68
	v_fmac_f32_e32 v92, v6, v69
	v_fmac_f32_e32 v96, v2, v69
	v_fmac_f32_e32 v94, v16, v68
	v_fmac_f32_e32 v95, v17, v68
	v_fmac_f32_e32 v98, v12, v68
	v_fmac_f32_e32 v99, v13, v68
	v_fmac_f32_e32 v93, v7, v69
	v_cndmask_b32_e64 v68, v92, v96, s[8:9]
	v_fmac_f32_e32 v97, v3, v69
	v_fmac_f32_e32 v94, v8, v69
	ds_bpermute_b32 v68, v79, v68
	v_fmac_f32_e32 v95, v9, v69
	v_fmac_f32_e32 v98, v4, v69
	v_fmac_f32_e32 v99, v5, v69
	v_cndmask_b32_e64 v69, v93, v97, s[8:9]
	s_waitcnt lgkmcnt(0)
	v_add_f32_e32 v66, v85, v84
	ds_bpermute_b32 v69, v79, v69
	v_cndmask_b32_e64 v85, v94, v98, s[8:9]
	ds_bpermute_b32 v85, v79, v85
	v_cndmask_b32_e64 v86, v95, v99, s[8:9]
	ds_bpermute_b32 v86, v79, v86
	v_cndmask_b32_e64 v67, v96, v92, s[8:9]
	s_waitcnt lgkmcnt(0)
	v_add_f32_e32 v67, v67, v68
	v_cndmask_b32_e64 v68, v97, v93, s[8:9]
	s_waitcnt lgkmcnt(0)
	v_add_f32_e32 v68, v68, v69
	v_cndmask_b32_e64 v69, v98, v94, s[8:9]
	s_waitcnt lgkmcnt(0)
	v_add_f32_e32 v69, v69, v85
	v_cndmask_b32_e64 v85, v99, v95, s[8:9]
	s_waitcnt lgkmcnt(0)
	v_add_f32_e32 v85, v85, v86
	v_cndmask_b32_e64 v86, v69, v67, s[2:3]
	v_cndmask_b32_e64 v67, v67, v69, s[2:3]
	v_cndmask_b32_e64 v69, v68, v85, s[2:3]
	ds_bpermute_b32 v67, v78, v67
	ds_bpermute_b32 v69, v78, v69
	ds_bpermute_b32 v84, v78, v66
	v_cndmask_b32_e64 v68, v85, v68, s[2:3]
	s_waitcnt lgkmcnt(0)
	v_add_f32_e32 v67, v86, v67
	s_waitcnt lgkmcnt(0)
	v_add_f32_e32 v68, v68, v69
	s_waitcnt lgkmcnt(0)
	v_add_f32_e32 v66, v66, v84
	v_cndmask_b32_e64 v69, v68, v67, s[4:5]
	v_cndmask_b32_e64 v67, v67, v68, s[4:5]
	s_nop 1
	v_mov_b32_dpp v84, v66 row_ror:8 row_mask:0xf bank_mask:0xf
	s_nop 1
	v_mov_b32_dpp v67, v67 row_ror:8 row_mask:0xf bank_mask:0xf
	s_waitcnt lgkmcnt(0)
	v_add_f32_e32 v66, v66, v84
	s_waitcnt lgkmcnt(0)
	v_add_f32_e32 v67, v69, v67
	s_nop 1
	v_mov_b32_dpp v104, v66 row_half_mirror row_mask:0xf bank_mask:0xf
	s_nop 1
	v_mov_b32_dpp v68, v104 quad_perm:[3,2,1,0] row_mask:0xf bank_mask:0xf
	s_nop 1
	v_mov_b32_dpp v104, v67 row_half_mirror row_mask:0xf bank_mask:0xf
	s_nop 1
	v_mov_b32_dpp v69, v104 quad_perm:[3,2,1,0] row_mask:0xf bank_mask:0xf
	s_waitcnt lgkmcnt(0)
	v_add_f32_e32 v66, v66, v68
	s_waitcnt lgkmcnt(0)
	v_add_f32_e32 v69, v67, v69
	s_nop 1
	v_mov_b32_dpp v68, v66 quad_perm:[2,3,0,1] row_mask:0xf bank_mask:0xf
	s_nop 1
	v_mov_b32_dpp v84, v69 quad_perm:[2,3,0,1] row_mask:0xf bank_mask:0xf
	s_waitcnt lgkmcnt(0)
	v_add_f32_e32 v66, v66, v68
	s_waitcnt lgkmcnt(0)
	v_add_f32_e32 v84, v69, v84
	s_nop 1
	v_mov_b32_dpp v67, v66 quad_perm:[1,0,3,2] row_mask:0xf bank_mask:0xf
	s_nop 1
	v_mov_b32_dpp v85, v84 quad_perm:[1,0,3,2] row_mask:0xf bank_mask:0xf
	v_and_b32_e32 v68, 7, v0
	v_cmp_eq_u32_e64 s[6:7], 0, v68
	v_or_b32_e32 v68, 0x8200, v91
	v_mad_u32_u24 v69, v81, 36, v68
	s_and_saveexec_b64 s[10:11], s[6:7]
	s_cbranch_execz .LBB7_9
	s_waitcnt lgkmcnt(0)
	v_add_f32_e32 v84, v84, v85
	s_waitcnt vmcnt(0)
	v_add_f32_e32 v84, v73, v84
	ds_write_b32 v69, v84
.LBB7_9:
	s_or_b64 exec, exec, s[10:11]
	v_cmp_eq_u32_e64 s[10:11], 0, v82
	s_and_saveexec_b64 s[16:17], s[10:11]
	s_cbranch_execz .LBB7_11
	s_waitcnt lgkmcnt(0)
	v_add_f32_e32 v66, v66, v67
	v_mov_b32_e32 v67, 0x3727c5ac
	v_fmac_f32_e32 v67, 0x3b000000, v66
	s_mov_b32 s12, 0xf800000
	v_mul_f32_e32 v66, 0x4f800000, v67
	v_cmp_gt_f32_e32 vcc, s12, v67
	s_nop 1
	v_cndmask_b32_e32 v66, v67, v66, vcc
	v_sqrt_f32_e32 v67, v66
	s_nop 0
	v_add_u32_e32 v82, -1, v67
	v_fma_f32 v84, -v82, v67, v66
	v_cmp_ge_f32_e64 s[12:13], 0, v84
	v_add_u32_e32 v84, 1, v67
	s_nop 0
	v_cndmask_b32_e64 v82, v67, v82, s[12:13]
	v_fma_f32 v67, -v84, v67, v66
	v_cmp_lt_f32_e64 s[12:13], 0, v67
	s_nop 1
	v_cndmask_b32_e64 v67, v82, v84, s[12:13]
	v_mul_f32_e32 v82, 0x37800000, v67
	v_cndmask_b32_e32 v67, v67, v82, vcc
	v_mov_b32_e32 v82, 0x260
	v_cmp_class_f32_e32 vcc, v66, v82
	s_nop 1
	v_cndmask_b32_e32 v67, v67, v66, vcc
	v_div_scale_f32 v82, s[12:13], v67, v67, 1.0
	v_rcp_f32_e32 v84, v82
	v_mul_f32_e32 v66, 0x3b000000, v83
	v_fma_f32 v83, -v82, v84, 1.0
	v_fmac_f32_e32 v84, v83, v84
	v_div_scale_f32 v83, vcc, 1.0, v67, 1.0
	s_waitcnt lgkmcnt(0)
	v_mul_f32_e32 v85, v83, v84
	v_fma_f32 v86, -v82, v85, v83
	v_fmac_f32_e32 v85, v86, v84
	v_fma_f32 v82, -v82, v85, v83
	v_div_fmas_f32 v82, v82, v84, v85
	v_div_fixup_f32 v67, v82, v67, 1.0
	v_lshlrev_b32_e32 v82, 1, v72
	v_ashrrev_i32_e32 v83, 31, v82
	v_lshl_add_u64 v[82:83], v[82:83], 2, s[14:15]
	global_store_dwordx2 v[82:83], v[66:67], off
.LBB7_11:
	s_or_b64 exec, exec, s[16:17]
	v_add3_u32 v66, s24, v81, 1
	s_waitcnt lgkmcnt(0)
	v_ashrrev_i32_e32 v67, 31, v66
	v_lshlrev_b64 v[82:83], 11, v[66:67]
	v_lshl_add_u64 v[90:91], v[70:71], 0, v[82:83]
	s_waitcnt lgkmcnt(0)
	global_load_dwordx4 v[82:85], v[90:91], off
	global_load_dwordx4 v[86:89], v[90:91], off offset:16
	s_waitcnt vmcnt(1)
	v_add_f32_e32 v67, 0, v82
	v_add_f32_e32 v67, v67, v83
	v_add_f32_e32 v67, v67, v84
	v_add_f32_e32 v67, v67, v85
	s_waitcnt vmcnt(0)
	v_add_f32_e32 v67, v67, v86
	v_add_f32_e32 v67, v67, v87
	v_add_f32_e32 v67, v67, v88
	v_add_f32_e32 v67, v67, v89
	ds_bpermute_b32 v97, v79, v67
	v_fma_f32 v72, v62, v82, 0
	v_fma_f32 v93, v58, v82, 0
	v_fmac_f32_e32 v72, v54, v83
	v_fmac_f32_e32 v93, v50, v83
	s_waitcnt lgkmcnt(0)
	v_add_f32_e32 v67, v67, v97
	v_fmac_f32_e32 v72, v46, v84
	v_fmac_f32_e32 v93, v42, v84
	ds_bpermute_b32 v97, v78, v67
	v_fmac_f32_e32 v72, v38, v85
	v_fmac_f32_e32 v93, v26, v85
	v_fmac_f32_e32 v72, v30, v86
	v_fmac_f32_e32 v93, v18, v86
	v_fmac_f32_e32 v72, v34, v87
	v_fmac_f32_e32 v93, v22, v87
	v_fmac_f32_e32 v72, v14, v88
	v_fmac_f32_e32 v93, v10, v88
	v_fmac_f32_e32 v72, v6, v89
	v_fmac_f32_e32 v93, v2, v89
	s_waitcnt lgkmcnt(0)
	v_add_f32_e32 v67, v67, v97
	v_cndmask_b32_e64 v98, v93, v72, s[8:9]
	v_cndmask_b32_e64 v72, v72, v93, s[8:9]
	s_nop 1
	v_mov_b32_dpp v93, v67 row_ror:8 row_mask:0xf bank_mask:0xf
	v_fma_f32 v90, v63, v82, 0
	v_fma_f32 v91, v64, v82, 0
	v_fma_f32 v92, v65, v82, 0
	v_fma_f32 v94, v59, v82, 0
	s_waitcnt lgkmcnt(0)
	v_add_f32_e32 v67, v67, v93
	s_nop 1
	v_mov_b32_dpp v104, v67 row_half_mirror row_mask:0xf bank_mask:0xf
	s_nop 1
	v_mov_b32_dpp v93, v104 quad_perm:[3,2,1,0] row_mask:0xf bank_mask:0xf
	v_fma_f32 v95, v60, v82, 0
	v_fma_f32 v96, v61, v82, 0
	v_fmac_f32_e32 v90, v55, v83
	v_fmac_f32_e32 v91, v56, v83
	s_waitcnt lgkmcnt(0)
	v_add_f32_e32 v67, v67, v93
	s_nop 1
	v_mov_b32_dpp v93, v67 quad_perm:[2,3,0,1] row_mask:0xf bank_mask:0xf
	v_fmac_f32_e32 v92, v57, v83
	v_fmac_f32_e32 v94, v51, v83
	v_fmac_f32_e32 v95, v52, v83
	v_fmac_f32_e32 v96, v53, v83
	s_waitcnt lgkmcnt(0)
	v_add_f32_e32 v67, v67, v93
	s_nop 1
	v_mov_b32_dpp v93, v67 quad_perm:[1,0,3,2] row_mask:0xf bank_mask:0xf
	v_fmac_f32_e32 v90, v47, v84
	v_fmac_f32_e32 v91, v48, v84
	v_fmac_f32_e32 v92, v49, v84
	v_fmac_f32_e32 v94, v43, v84
	s_waitcnt lgkmcnt(0)
	v_add_f32_e32 v67, v67, v93
	v_fmac_f32_e32 v95, v44, v84
	v_fmac_f32_e32 v96, v45, v84
	v_fmamk_f32 v83, v67, 0xbb000000, v83
	v_fmac_f32_e32 v90, v39, v85
	v_fmac_f32_e32 v91, v40, v85
	v_fmac_f32_e32 v92, v41, v85
	v_fmac_f32_e32 v94, v27, v85
	v_fmac_f32_e32 v95, v28, v85
	v_fmac_f32_e32 v96, v29, v85
	v_fmamk_f32 v82, v67, 0xbb000000, v82
	v_mul_f32_e32 v83, v83, v83
	v_fmac_f32_e32 v90, v31, v86
	v_fmac_f32_e32 v91, v32, v86
	v_fmac_f32_e32 v92, v33, v86
	v_fmac_f32_e32 v94, v19, v86
	v_fmac_f32_e32 v95, v20, v86
	v_fmac_f32_e32 v96, v21, v86
	v_fmamk_f32 v84, v67, 0xbb000000, v84
	v_fmac_f32_e32 v83, v82, v82
	v_fmac_f32_e32 v90, v35, v87
	v_fmac_f32_e32 v91, v36, v87
	v_fmac_f32_e32 v92, v37, v87
	v_fmac_f32_e32 v94, v23, v87
	v_fmac_f32_e32 v95, v24, v87
	v_fmac_f32_e32 v96, v25, v87
	v_fmamk_f32 v85, v67, 0xbb000000, v85
	v_fmac_f32_e32 v83, v84, v84
	v_fmac_f32_e32 v90, v15, v88
	v_fmac_f32_e32 v91, v16, v88
	v_fmac_f32_e32 v92, v17, v88
	v_fmac_f32_e32 v94, v11, v88
	v_fmac_f32_e32 v95, v12, v88
	v_fmac_f32_e32 v96, v13, v88
	v_fmamk_f32 v86, v67, 0xbb000000, v86
	v_fmac_f32_e32 v83, v85, v85
	v_fmac_f32_e32 v90, v7, v89
	v_fmac_f32_e32 v91, v8, v89
	v_fmac_f32_e32 v92, v9, v89
	v_fmac_f32_e32 v94, v3, v89
	v_fmac_f32_e32 v95, v4, v89
	v_fmac_f32_e32 v96, v5, v89
	v_fmamk_f32 v87, v67, 0xbb000000, v87
	v_fmac_f32_e32 v83, v86, v86
	v_cndmask_b32_e64 v97, v94, v90, s[8:9]
	v_cndmask_b32_e64 v90, v90, v94, s[8:9]
	v_cndmask_b32_e64 v94, v95, v91, s[8:9]
	v_cndmask_b32_e64 v91, v91, v95, s[8:9]
	v_cndmask_b32_e64 v95, v96, v92, s[8:9]
	v_cndmask_b32_e64 v92, v92, v96, s[8:9]
	v_fmamk_f32 v88, v67, 0xbb000000, v88
	v_fmac_f32_e32 v83, v87, v87
	ds_bpermute_b32 v72, v79, v72
	ds_bpermute_b32 v90, v79, v90
	ds_bpermute_b32 v91, v79, v91
	ds_bpermute_b32 v92, v79, v92
	v_fmamk_f32 v89, v67, 0xbb000000, v89
	v_fmac_f32_e32 v83, v88, v88
	v_fmac_f32_e32 v83, v89, v89
	ds_bpermute_b32 v82, v79, v83
	s_waitcnt lgkmcnt(0)
	v_add_f32_e32 v72, v98, v72
	s_waitcnt lgkmcnt(0)
	v_add_f32_e32 v90, v97, v90
	s_waitcnt lgkmcnt(0)
	v_add_f32_e32 v91, v94, v91
	s_waitcnt lgkmcnt(0)
	v_add_f32_e32 v92, v95, v92
	v_cndmask_b32_e64 v94, v91, v72, s[2:3]
	v_cndmask_b32_e64 v72, v72, v91, s[2:3]
	v_cndmask_b32_e64 v84, v90, v92, s[2:3]
	ds_bpermute_b32 v72, v78, v72
	ds_bpermute_b32 v84, v78, v84
	s_waitcnt lgkmcnt(0)
	v_add_f32_e32 v82, v83, v82
	ds_bpermute_b32 v83, v78, v82
	v_cndmask_b32_e64 v85, v92, v90, s[2:3]
	s_waitcnt lgkmcnt(0)
	v_add_f32_e32 v72, v94, v72
	s_waitcnt lgkmcnt(0)
	v_add_f32_e32 v84, v85, v84
	v_cndmask_b32_e64 v85, v72, v84, s[4:5]
	s_waitcnt lgkmcnt(0)
	v_add_f32_e32 v82, v82, v83
	s_nop 1
	v_mov_b32_dpp v85, v85 row_ror:8 row_mask:0xf bank_mask:0xf
	s_nop 1
	v_mov_b32_dpp v83, v82 row_ror:8 row_mask:0xf bank_mask:0xf
	v_cndmask_b32_e64 v72, v84, v72, s[4:5]
	s_waitcnt lgkmcnt(0)
	v_add_f32_e32 v72, v72, v85
	s_waitcnt lgkmcnt(0)
	v_add_f32_e32 v82, v82, v83
	s_nop 1
	v_mov_b32_dpp v104, v72 row_half_mirror row_mask:0xf bank_mask:0xf
	s_nop 1
	v_mov_b32_dpp v84, v104 quad_perm:[3,2,1,0] row_mask:0xf bank_mask:0xf
	s_nop 1
	v_mov_b32_dpp v104, v82 row_half_mirror row_mask:0xf bank_mask:0xf
	s_nop 1
	v_mov_b32_dpp v83, v104 quad_perm:[3,2,1,0] row_mask:0xf bank_mask:0xf
	s_waitcnt lgkmcnt(0)
	v_add_f32_e32 v72, v72, v84
	s_waitcnt lgkmcnt(0)
	v_add_f32_e32 v82, v82, v83
	s_nop 1
	v_mov_b32_dpp v84, v72 quad_perm:[2,3,0,1] row_mask:0xf bank_mask:0xf
	s_nop 1
	v_mov_b32_dpp v85, v82 quad_perm:[2,3,0,1] row_mask:0xf bank_mask:0xf
	s_waitcnt lgkmcnt(0)
	v_add_f32_e32 v83, v72, v84
	s_waitcnt lgkmcnt(0)
	v_add_f32_e32 v72, v82, v85
	s_nop 1
	v_mov_b32_dpp v82, v72 quad_perm:[1,0,3,2] row_mask:0xf bank_mask:0xf
	s_nop 1
	v_mov_b32_dpp v84, v83 quad_perm:[1,0,3,2] row_mask:0xf bank_mask:0xf
	s_and_saveexec_b64 s[12:13], s[6:7]
	s_cbranch_execz .LBB7_13
	s_waitcnt lgkmcnt(0)
	v_add_f32_e32 v83, v83, v84
	v_add_f32_e32 v83, v73, v83
	ds_write_b32 v69, v83 offset:36
.LBB7_13:
	s_or_b64 exec, exec, s[12:13]
	s_and_saveexec_b64 s[16:17], s[10:11]
	s_cbranch_execz .LBB7_15
	s_waitcnt lgkmcnt(0)
	v_add_f32_e32 v72, v72, v82
	v_mov_b32_e32 v82, 0x3727c5ac
	v_fmac_f32_e32 v82, 0x3b000000, v72
	s_mov_b32 s12, 0xf800000
	v_mul_f32_e32 v72, 0x4f800000, v82
	v_cmp_gt_f32_e32 vcc, s12, v82
	v_lshlrev_b32_e32 v66, 1, v66
	s_nop 0
	v_cndmask_b32_e32 v72, v82, v72, vcc
	v_sqrt_f32_e32 v82, v72
	s_nop 0
	v_add_u32_e32 v83, -1, v82
	s_waitcnt lgkmcnt(0)
	v_fma_f32 v84, -v83, v82, v72
	v_cmp_ge_f32_e64 s[12:13], 0, v84
	v_add_u32_e32 v84, 1, v82
	s_nop 0
	v_cndmask_b32_e64 v83, v82, v83, s[12:13]
	v_fma_f32 v82, -v84, v82, v72
	v_cmp_lt_f32_e64 s[12:13], 0, v82
	s_nop 1
	v_cndmask_b32_e64 v82, v83, v84, s[12:13]
	v_mul_f32_e32 v83, 0x37800000, v82
	v_cndmask_b32_e32 v82, v82, v83, vcc
	v_mov_b32_e32 v83, 0x260
	v_cmp_class_f32_e32 vcc, v72, v83
	s_nop 1
	v_cndmask_b32_e32 v72, v82, v72, vcc
	v_div_scale_f32 v83, s[12:13], v72, v72, 1.0
	v_rcp_f32_e32 v84, v83
	v_mul_f32_e32 v82, 0x3b000000, v67
	v_fma_f32 v67, -v83, v84, 1.0
	v_fmac_f32_e32 v84, v67, v84
	v_div_scale_f32 v67, vcc, 1.0, v72, 1.0
	v_mul_f32_e32 v85, v67, v84
	v_fma_f32 v86, -v83, v85, v67
	v_fmac_f32_e32 v85, v86, v84
	v_fma_f32 v67, -v83, v85, v67
	v_div_fmas_f32 v67, v67, v84, v85
	v_div_fixup_f32 v83, v67, v72, 1.0
	v_ashrrev_i32_e32 v67, 31, v66
	v_lshl_add_u64 v[66:67], v[66:67], 2, s[14:15]
	global_store_dwordx2 v[66:67], v[82:83], off
.LBB7_15:
	s_or_b64 exec, exec, s[16:17]
	v_add3_u32 v66, s24, v81, 2
	v_ashrrev_i32_e32 v67, 31, v66
	s_waitcnt lgkmcnt(0)
	v_lshlrev_b64 v[82:83], 11, v[66:67]
	v_lshl_add_u64 v[90:91], v[70:71], 0, v[82:83]
	s_waitcnt lgkmcnt(0)
	global_load_dwordx4 v[82:85], v[90:91], off
	global_load_dwordx4 v[86:89], v[90:91], off offset:16
	s_waitcnt vmcnt(1)
	v_add_f32_e32 v67, 0, v82
	v_add_f32_e32 v67, v67, v83
	v_add_f32_e32 v67, v67, v84
	v_add_f32_e32 v67, v67, v85
	s_waitcnt vmcnt(0)
	v_add_f32_e32 v67, v67, v86
	v_add_f32_e32 v67, v67, v87
	v_add_f32_e32 v67, v67, v88
	v_add_f32_e32 v67, v67, v89
	ds_bpermute_b32 v97, v79, v67
	v_fma_f32 v72, v62, v82, 0
	v_fma_f32 v93, v58, v82, 0
	v_fmac_f32_e32 v72, v54, v83
	v_fmac_f32_e32 v93, v50, v83
	s_waitcnt lgkmcnt(0)
	v_add_f32_e32 v67, v67, v97
	v_fmac_f32_e32 v72, v46, v84
	v_fmac_f32_e32 v93, v42, v84
	ds_bpermute_b32 v97, v78, v67
	v_fmac_f32_e32 v72, v38, v85
	v_fmac_f32_e32 v93, v26, v85
	v_fmac_f32_e32 v72, v30, v86
	v_fmac_f32_e32 v93, v18, v86
	v_fmac_f32_e32 v72, v34, v87
	v_fmac_f32_e32 v93, v22, v87
	v_fmac_f32_e32 v72, v14, v88
	v_fmac_f32_e32 v93, v10, v88
	v_fmac_f32_e32 v72, v6, v89
	v_fmac_f32_e32 v93, v2, v89
	s_waitcnt lgkmcnt(0)
	v_add_f32_e32 v67, v67, v97
	v_cndmask_b32_e64 v98, v93, v72, s[8:9]
	v_cndmask_b32_e64 v72, v72, v93, s[8:9]
	s_nop 1
	v_mov_b32_dpp v93, v67 row_ror:8 row_mask:0xf bank_mask:0xf
	v_fma_f32 v90, v63, v82, 0
	v_fma_f32 v91, v64, v82, 0
	v_fma_f32 v92, v65, v82, 0
	v_fma_f32 v94, v59, v82, 0
	s_waitcnt lgkmcnt(0)
	v_add_f32_e32 v67, v67, v93
	s_nop 1
	v_mov_b32_dpp v104, v67 row_half_mirror row_mask:0xf bank_mask:0xf
	s_nop 1
	v_mov_b32_dpp v93, v104 quad_perm:[3,2,1,0] row_mask:0xf bank_mask:0xf
	v_fma_f32 v95, v60, v82, 0
	v_fma_f32 v96, v61, v82, 0
	v_fmac_f32_e32 v90, v55, v83
	v_fmac_f32_e32 v91, v56, v83
	s_waitcnt lgkmcnt(0)
	v_add_f32_e32 v67, v67, v93
	s_nop 1
	v_mov_b32_dpp v93, v67 quad_perm:[2,3,0,1] row_mask:0xf bank_mask:0xf
	v_fmac_f32_e32 v92, v57, v83
	v_fmac_f32_e32 v94, v51, v83
	v_fmac_f32_e32 v95, v52, v83
	v_fmac_f32_e32 v96, v53, v83
	s_waitcnt lgkmcnt(0)
	v_add_f32_e32 v67, v67, v93
	s_nop 1
	v_mov_b32_dpp v93, v67 quad_perm:[1,0,3,2] row_mask:0xf bank_mask:0xf
	v_fmac_f32_e32 v90, v47, v84
	v_fmac_f32_e32 v91, v48, v84
	v_fmac_f32_e32 v92, v49, v84
	v_fmac_f32_e32 v94, v43, v84
	s_waitcnt lgkmcnt(0)
	v_add_f32_e32 v67, v67, v93
	v_fmac_f32_e32 v95, v44, v84
	v_fmac_f32_e32 v96, v45, v84
	v_fmamk_f32 v83, v67, 0xbb000000, v83
	v_fmac_f32_e32 v90, v39, v85
	v_fmac_f32_e32 v91, v40, v85
	v_fmac_f32_e32 v92, v41, v85
	v_fmac_f32_e32 v94, v27, v85
	v_fmac_f32_e32 v95, v28, v85
	v_fmac_f32_e32 v96, v29, v85
	v_fmamk_f32 v82, v67, 0xbb000000, v82
	v_mul_f32_e32 v83, v83, v83
	v_fmac_f32_e32 v90, v31, v86
	v_fmac_f32_e32 v91, v32, v86
	v_fmac_f32_e32 v92, v33, v86
	v_fmac_f32_e32 v94, v19, v86
	v_fmac_f32_e32 v95, v20, v86
	v_fmac_f32_e32 v96, v21, v86
	v_fmamk_f32 v84, v67, 0xbb000000, v84
	v_fmac_f32_e32 v83, v82, v82
	v_fmac_f32_e32 v90, v35, v87
	v_fmac_f32_e32 v91, v36, v87
	v_fmac_f32_e32 v92, v37, v87
	v_fmac_f32_e32 v94, v23, v87
	v_fmac_f32_e32 v95, v24, v87
	v_fmac_f32_e32 v96, v25, v87
	v_fmamk_f32 v85, v67, 0xbb000000, v85
	v_fmac_f32_e32 v83, v84, v84
	v_fmac_f32_e32 v90, v15, v88
	v_fmac_f32_e32 v91, v16, v88
	v_fmac_f32_e32 v92, v17, v88
	v_fmac_f32_e32 v94, v11, v88
	v_fmac_f32_e32 v95, v12, v88
	v_fmac_f32_e32 v96, v13, v88
	v_fmamk_f32 v86, v67, 0xbb000000, v86
	v_fmac_f32_e32 v83, v85, v85
	v_fmac_f32_e32 v90, v7, v89
	v_fmac_f32_e32 v91, v8, v89
	v_fmac_f32_e32 v92, v9, v89
	v_fmac_f32_e32 v94, v3, v89
	v_fmac_f32_e32 v95, v4, v89
	v_fmac_f32_e32 v96, v5, v89
	v_fmamk_f32 v87, v67, 0xbb000000, v87
	v_fmac_f32_e32 v83, v86, v86
	v_cndmask_b32_e64 v97, v94, v90, s[8:9]
	v_cndmask_b32_e64 v90, v90, v94, s[8:9]
	v_cndmask_b32_e64 v94, v95, v91, s[8:9]
	v_cndmask_b32_e64 v91, v91, v95, s[8:9]
	v_cndmask_b32_e64 v95, v96, v92, s[8:9]
	v_cndmask_b32_e64 v92, v92, v96, s[8:9]
	v_fmamk_f32 v88, v67, 0xbb000000, v88
	v_fmac_f32_e32 v83, v87, v87
	ds_bpermute_b32 v72, v79, v72
	ds_bpermute_b32 v90, v79, v90
	ds_bpermute_b32 v91, v79, v91
	ds_bpermute_b32 v92, v79, v92
	v_fmamk_f32 v89, v67, 0xbb000000, v89
	v_fmac_f32_e32 v83, v88, v88
	v_fmac_f32_e32 v83, v89, v89
	ds_bpermute_b32 v82, v79, v83
	s_waitcnt lgkmcnt(0)
	v_add_f32_e32 v72, v98, v72
	s_waitcnt lgkmcnt(0)
	v_add_f32_e32 v90, v97, v90
	s_waitcnt lgkmcnt(0)
	v_add_f32_e32 v91, v94, v91
	s_waitcnt lgkmcnt(0)
	v_add_f32_e32 v92, v95, v92
	v_cndmask_b32_e64 v94, v91, v72, s[2:3]
	v_cndmask_b32_e64 v72, v72, v91, s[2:3]
	v_cndmask_b32_e64 v84, v90, v92, s[2:3]
	ds_bpermute_b32 v72, v78, v72
	ds_bpermute_b32 v84, v78, v84
	s_waitcnt lgkmcnt(0)
	v_add_f32_e32 v82, v83, v82
	ds_bpermute_b32 v83, v78, v82
	v_cndmask_b32_e64 v85, v92, v90, s[2:3]
	s_waitcnt lgkmcnt(0)
	v_add_f32_e32 v72, v94, v72
	s_waitcnt lgkmcnt(0)
	v_add_f32_e32 v84, v85, v84
	v_cndmask_b32_e64 v85, v72, v84, s[4:5]
	s_waitcnt lgkmcnt(0)
	v_add_f32_e32 v82, v82, v83
	s_nop 1
	v_mov_b32_dpp v85, v85 row_ror:8 row_mask:0xf bank_mask:0xf
	s_nop 1
	v_mov_b32_dpp v83, v82 row_ror:8 row_mask:0xf bank_mask:0xf
	v_cndmask_b32_e64 v72, v84, v72, s[4:5]
	s_waitcnt lgkmcnt(0)
	v_add_f32_e32 v72, v72, v85
	s_waitcnt lgkmcnt(0)
	v_add_f32_e32 v82, v82, v83
	s_nop 1
	v_mov_b32_dpp v104, v72 row_half_mirror row_mask:0xf bank_mask:0xf
	s_nop 1
	v_mov_b32_dpp v84, v104 quad_perm:[3,2,1,0] row_mask:0xf bank_mask:0xf
	s_nop 1
	v_mov_b32_dpp v104, v82 row_half_mirror row_mask:0xf bank_mask:0xf
	s_nop 1
	v_mov_b32_dpp v83, v104 quad_perm:[3,2,1,0] row_mask:0xf bank_mask:0xf
	s_waitcnt lgkmcnt(0)
	v_add_f32_e32 v72, v72, v84
	s_waitcnt lgkmcnt(0)
	v_add_f32_e32 v82, v82, v83
	s_nop 1
	v_mov_b32_dpp v84, v72 quad_perm:[2,3,0,1] row_mask:0xf bank_mask:0xf
	s_nop 1
	v_mov_b32_dpp v85, v82 quad_perm:[2,3,0,1] row_mask:0xf bank_mask:0xf
	s_waitcnt lgkmcnt(0)
	v_add_f32_e32 v83, v72, v84
	s_waitcnt lgkmcnt(0)
	v_add_f32_e32 v72, v82, v85
	s_nop 1
	v_mov_b32_dpp v82, v72 quad_perm:[1,0,3,2] row_mask:0xf bank_mask:0xf
	s_nop 1
	v_mov_b32_dpp v84, v83 quad_perm:[1,0,3,2] row_mask:0xf bank_mask:0xf
	s_and_saveexec_b64 s[12:13], s[6:7]
	s_cbranch_execz .LBB7_17
	s_waitcnt lgkmcnt(0)
	v_add_f32_e32 v83, v83, v84
	v_add_f32_e32 v83, v73, v83
	ds_write_b32 v69, v83 offset:72

.LBB7_19:
	s_or_b64 exec, exec, s[16:17]
	v_add3_u32 v66, s24, v81, 3
	v_ashrrev_i32_e32 v67, 31, v66
	s_waitcnt lgkmcnt(0)
	v_lshlrev_b64 v[82:83], 11, v[66:67]
	v_lshl_add_u64 v[90:91], v[70:71], 0, v[82:83]
	s_waitcnt lgkmcnt(0)
	global_load_dwordx4 v[82:85], v[90:91], off
	global_load_dwordx4 v[86:89], v[90:91], off offset:16
	s_waitcnt vmcnt(1)
	v_add_f32_e32 v67, 0, v82
	v_add_f32_e32 v67, v67, v83
	v_add_f32_e32 v67, v67, v84
	v_add_f32_e32 v67, v67, v85
	s_waitcnt vmcnt(0)
	v_add_f32_e32 v67, v67, v86
	v_add_f32_e32 v67, v67, v87
	v_add_f32_e32 v67, v67, v88
	v_add_f32_e32 v67, v67, v89
	ds_bpermute_b32 v97, v79, v67
	v_fma_f32 v72, v62, v82, 0
	v_fma_f32 v93, v58, v82, 0
	v_fmac_f32_e32 v72, v54, v83
	v_fmac_f32_e32 v93, v50, v83
	s_waitcnt lgkmcnt(0)
	v_add_f32_e32 v67, v67, v97
	v_fmac_f32_e32 v72, v46, v84
	v_fmac_f32_e32 v93, v42, v84
	ds_bpermute_b32 v97, v78, v67
	v_fmac_f32_e32 v72, v38, v85
	v_fmac_f32_e32 v93, v26, v85
	v_fmac_f32_e32 v72, v30, v86
	v_fmac_f32_e32 v93, v18, v86
	v_fmac_f32_e32 v72, v34, v87
	v_fmac_f32_e32 v93, v22, v87
	v_fmac_f32_e32 v72, v14, v88
	v_fmac_f32_e32 v93, v10, v88
	v_fmac_f32_e32 v72, v6, v89
	v_fmac_f32_e32 v93, v2, v89
	s_waitcnt lgkmcnt(0)
	v_add_f32_e32 v67, v67, v97
	v_cndmask_b32_e64 v98, v93, v72, s[8:9]
	v_cndmask_b32_e64 v72, v72, v93, s[8:9]
	s_nop 1
	v_mov_b32_dpp v93, v67 row_ror:8 row_mask:0xf bank_mask:0xf
	v_fma_f32 v90, v63, v82, 0
	v_fma_f32 v91, v64, v82, 0
	v_fma_f32 v92, v65, v82, 0
	v_fma_f32 v94, v59, v82, 0
	s_waitcnt lgkmcnt(0)
	v_add_f32_e32 v67, v67, v93
	s_nop 1
	v_mov_b32_dpp v104, v67 row_half_mirror row_mask:0xf bank_mask:0xf
	s_nop 1
	v_mov_b32_dpp v93, v104 quad_perm:[3,2,1,0] row_mask:0xf bank_mask:0xf
	v_fma_f32 v95, v60, v82, 0
	v_fma_f32 v96, v61, v82, 0
	v_fmac_f32_e32 v90, v55, v83
	v_fmac_f32_e32 v91, v56, v83
	s_waitcnt lgkmcnt(0)
	v_add_f32_e32 v67, v67, v93
	s_nop 1
	v_mov_b32_dpp v93, v67 quad_perm:[2,3,0,1] row_mask:0xf bank_mask:0xf
	v_fmac_f32_e32 v92, v57, v83
	v_fmac_f32_e32 v94, v51, v83
	v_fmac_f32_e32 v95, v52, v83
	v_fmac_f32_e32 v96, v53, v83
	s_waitcnt lgkmcnt(0)
	v_add_f32_e32 v67, v67, v93
	s_nop 1
	v_mov_b32_dpp v93, v67 quad_perm:[1,0,3,2] row_mask:0xf bank_mask:0xf
	v_fmac_f32_e32 v90, v47, v84
	v_fmac_f32_e32 v91, v48, v84
	v_fmac_f32_e32 v92, v49, v84
	v_fmac_f32_e32 v94, v43, v84
	s_waitcnt lgkmcnt(0)
	v_add_f32_e32 v67, v67, v93
	v_fmac_f32_e32 v95, v44, v84
	v_fmac_f32_e32 v96, v45, v84
	v_fmamk_f32 v83, v67, 0xbb000000, v83
	v_fmac_f32_e32 v90, v39, v85
	v_fmac_f32_e32 v91, v40, v85
	v_fmac_f32_e32 v92, v41, v85
	v_fmac_f32_e32 v94, v27, v85
	v_fmac_f32_e32 v95, v28, v85
	v_fmac_f32_e32 v96, v29, v85
	v_fmamk_f32 v82, v67, 0xbb000000, v82
	v_mul_f32_e32 v83, v83, v83
	v_fmac_f32_e32 v90, v31, v86
	v_fmac_f32_e32 v91, v32, v86
	v_fmac_f32_e32 v92, v33, v86
	v_fmac_f32_e32 v94, v19, v86
	v_fmac_f32_e32 v95, v20, v86
	v_fmac_f32_e32 v96, v21, v86
	v_fmamk_f32 v84, v67, 0xbb000000, v84
	v_fmac_f32_e32 v83, v82, v82
	v_fmac_f32_e32 v90, v35, v87
	v_fmac_f32_e32 v91, v36, v87
	v_fmac_f32_e32 v92, v37, v87
	v_fmac_f32_e32 v94, v23, v87
	v_fmac_f32_e32 v95, v24, v87
	v_fmac_f32_e32 v96, v25, v87
	v_fmamk_f32 v85, v67, 0xbb000000, v85
	v_fmac_f32_e32 v83, v84, v84
	v_fmac_f32_e32 v90, v15, v88
	v_fmac_f32_e32 v91, v16, v88
	v_fmac_f32_e32 v92, v17, v88
	v_fmac_f32_e32 v94, v11, v88
	v_fmac_f32_e32 v95, v12, v88
	v_fmac_f32_e32 v96, v13, v88
	v_fmamk_f32 v86, v67, 0xbb000000, v86
	v_fmac_f32_e32 v83, v85, v85
	v_fmac_f32_e32 v90, v7, v89
	v_fmac_f32_e32 v91, v8, v89
	v_fmac_f32_e32 v92, v9, v89
	v_fmac_f32_e32 v94, v3, v89
	v_fmac_f32_e32 v95, v4, v89
	v_fmac_f32_e32 v96, v5, v89
	v_fmamk_f32 v87, v67, 0xbb000000, v87
	v_fmac_f32_e32 v83, v86, v86
	v_cndmask_b32_e64 v97, v94, v90, s[8:9]
	v_cndmask_b32_e64 v90, v90, v94, s[8:9]
	v_cndmask_b32_e64 v94, v95, v91, s[8:9]
	v_cndmask_b32_e64 v91, v91, v95, s[8:9]
	v_cndmask_b32_e64 v95, v96, v92, s[8:9]
	v_cndmask_b32_e64 v92, v92, v96, s[8:9]
	v_fmamk_f32 v88, v67, 0xbb000000, v88
	v_fmac_f32_e32 v83, v87, v87
	ds_bpermute_b32 v72, v79, v72
	ds_bpermute_b32 v90, v79, v90
	ds_bpermute_b32 v91, v79, v91
	ds_bpermute_b32 v92, v79, v92
	v_fmamk_f32 v89, v67, 0xbb000000, v89
	v_fmac_f32_e32 v83, v88, v88
	v_fmac_f32_e32 v83, v89, v89
	ds_bpermute_b32 v82, v79, v83
	s_waitcnt lgkmcnt(0)
	v_add_f32_e32 v72, v98, v72
	s_waitcnt lgkmcnt(0)
	v_add_f32_e32 v90, v97, v90
	s_waitcnt lgkmcnt(0)
	v_add_f32_e32 v91, v94, v91
	s_waitcnt lgkmcnt(0)
	v_add_f32_e32 v92, v95, v92
	v_cndmask_b32_e64 v94, v91, v72, s[2:3]
	v_cndmask_b32_e64 v72, v72, v91, s[2:3]
	v_cndmask_b32_e64 v84, v90, v92, s[2:3]
	ds_bpermute_b32 v72, v78, v72
	ds_bpermute_b32 v84, v78, v84
	s_waitcnt lgkmcnt(0)
	v_add_f32_e32 v82, v83, v82
	ds_bpermute_b32 v83, v78, v82
	v_cndmask_b32_e64 v85, v92, v90, s[2:3]
	s_waitcnt lgkmcnt(0)
	v_add_f32_e32 v72, v94, v72
	s_waitcnt lgkmcnt(0)
	v_add_f32_e32 v84, v85, v84
	v_cndmask_b32_e64 v85, v72, v84, s[4:5]
	s_waitcnt lgkmcnt(0)
	v_add_f32_e32 v82, v82, v83
	s_nop 1
	v_mov_b32_dpp v85, v85 row_ror:8 row_mask:0xf bank_mask:0xf
	s_nop 1
	v_mov_b32_dpp v83, v82 row_ror:8 row_mask:0xf bank_mask:0xf
	v_cndmask_b32_e64 v72, v84, v72, s[4:5]
	s_waitcnt lgkmcnt(0)
	v_add_f32_e32 v72, v72, v85
	s_waitcnt lgkmcnt(0)
	v_add_f32_e32 v82, v82, v83
	s_nop 1
	v_mov_b32_dpp v104, v72 row_half_mirror row_mask:0xf bank_mask:0xf
	s_nop 1
	v_mov_b32_dpp v84, v104 quad_perm:[3,2,1,0] row_mask:0xf bank_mask:0xf
	s_nop 1
	v_mov_b32_dpp v104, v82 row_half_mirror row_mask:0xf bank_mask:0xf
	s_nop 1
	v_mov_b32_dpp v83, v104 quad_perm:[3,2,1,0] row_mask:0xf bank_mask:0xf
	s_waitcnt lgkmcnt(0)
	v_add_f32_e32 v72, v72, v84
	s_waitcnt lgkmcnt(0)
	v_add_f32_e32 v82, v82, v83
	s_nop 1
	v_mov_b32_dpp v84, v72 quad_perm:[2,3,0,1] row_mask:0xf bank_mask:0xf
	s_nop 1
	v_mov_b32_dpp v85, v82 quad_perm:[2,3,0,1] row_mask:0xf bank_mask:0xf
	s_waitcnt lgkmcnt(0)
	v_add_f32_e32 v83, v72, v84
	s_waitcnt lgkmcnt(0)
	v_add_f32_e32 v72, v82, v85
	s_nop 1
	v_mov_b32_dpp v82, v72 quad_perm:[1,0,3,2] row_mask:0xf bank_mask:0xf
	s_nop 1
	v_mov_b32_dpp v84, v83 quad_perm:[1,0,3,2] row_mask:0xf bank_mask:0xf
	s_and_saveexec_b64 s[12:13], s[6:7]
	s_cbranch_execz .LBB7_21
	s_waitcnt lgkmcnt(0)
	v_add_f32_e32 v83, v83, v84
	v_add_f32_e32 v83, v73, v83
	ds_write_b32 v69, v83 offset:108

.LBB7_23:
	s_or_b64 exec, exec, s[16:17]
	v_add3_u32 v66, s24, v81, 4
	v_ashrrev_i32_e32 v67, 31, v66
	s_waitcnt lgkmcnt(0)
	v_lshlrev_b64 v[82:83], 11, v[66:67]
	v_lshl_add_u64 v[90:91], v[70:71], 0, v[82:83]
	s_waitcnt lgkmcnt(0)
	global_load_dwordx4 v[82:85], v[90:91], off
	global_load_dwordx4 v[86:89], v[90:91], off offset:16
	s_waitcnt vmcnt(1)
	v_add_f32_e32 v67, 0, v82
	v_add_f32_e32 v67, v67, v83
	v_add_f32_e32 v67, v67, v84
	v_add_f32_e32 v67, v67, v85
	s_waitcnt vmcnt(0)
	v_add_f32_e32 v67, v67, v86
	v_add_f32_e32 v67, v67, v87
	v_add_f32_e32 v67, v67, v88
	v_add_f32_e32 v67, v67, v89
	ds_bpermute_b32 v97, v79, v67
	v_fma_f32 v72, v62, v82, 0
	v_fma_f32 v93, v58, v82, 0
	v_fmac_f32_e32 v72, v54, v83
	v_fmac_f32_e32 v93, v50, v83
	s_waitcnt lgkmcnt(0)
	v_add_f32_e32 v67, v67, v97
	v_fmac_f32_e32 v72, v46, v84
	v_fmac_f32_e32 v93, v42, v84
	ds_bpermute_b32 v97, v78, v67
	v_fmac_f32_e32 v72, v38, v85
	v_fmac_f32_e32 v93, v26, v85
	v_fmac_f32_e32 v72, v30, v86
	v_fmac_f32_e32 v93, v18, v86
	v_fmac_f32_e32 v72, v34, v87
	v_fmac_f32_e32 v93, v22, v87
	v_fmac_f32_e32 v72, v14, v88
	v_fmac_f32_e32 v93, v10, v88
	v_fmac_f32_e32 v72, v6, v89
	v_fmac_f32_e32 v93, v2, v89
	s_waitcnt lgkmcnt(0)
	v_add_f32_e32 v67, v67, v97
	v_cndmask_b32_e64 v98, v93, v72, s[8:9]
	v_cndmask_b32_e64 v72, v72, v93, s[8:9]
	s_nop 1
	v_mov_b32_dpp v93, v67 row_ror:8 row_mask:0xf bank_mask:0xf
	v_fma_f32 v90, v63, v82, 0
	v_fma_f32 v91, v64, v82, 0
	v_fma_f32 v92, v65, v82, 0
	v_fma_f32 v94, v59, v82, 0
	s_waitcnt lgkmcnt(0)
	v_add_f32_e32 v67, v67, v93
	s_nop 1
	v_mov_b32_dpp v104, v67 row_half_mirror row_mask:0xf bank_mask:0xf
	s_nop 1
	v_mov_b32_dpp v93, v104 quad_perm:[3,2,1,0] row_mask:0xf bank_mask:0xf
	v_fma_f32 v95, v60, v82, 0
	v_fma_f32 v96, v61, v82, 0
	v_fmac_f32_e32 v90, v55, v83
	v_fmac_f32_e32 v91, v56, v83
	s_waitcnt lgkmcnt(0)
	v_add_f32_e32 v67, v67, v93
	s_nop 1
	v_mov_b32_dpp v93, v67 quad_perm:[2,3,0,1] row_mask:0xf bank_mask:0xf
	v_fmac_f32_e32 v92, v57, v83
	v_fmac_f32_e32 v94, v51, v83
	v_fmac_f32_e32 v95, v52, v83
	v_fmac_f32_e32 v96, v53, v83
	s_waitcnt lgkmcnt(0)
	v_add_f32_e32 v67, v67, v93
	s_nop 1
	v_mov_b32_dpp v93, v67 quad_perm:[1,0,3,2] row_mask:0xf bank_mask:0xf
	v_fmac_f32_e32 v90, v47, v84
	v_fmac_f32_e32 v91, v48, v84
	v_fmac_f32_e32 v92, v49, v84
	v_fmac_f32_e32 v94, v43, v84
	s_waitcnt lgkmcnt(0)
	v_add_f32_e32 v67, v67, v93
	v_fmac_f32_e32 v95, v44, v84
	v_fmac_f32_e32 v96, v45, v84
	v_fmamk_f32 v83, v67, 0xbb000000, v83
	v_fmac_f32_e32 v90, v39, v85
	v_fmac_f32_e32 v91, v40, v85
	v_fmac_f32_e32 v92, v41, v85
	v_fmac_f32_e32 v94, v27, v85
	v_fmac_f32_e32 v95, v28, v85
	v_fmac_f32_e32 v96, v29, v85
	v_fmamk_f32 v82, v67, 0xbb000000, v82
	v_mul_f32_e32 v83, v83, v83
	v_fmac_f32_e32 v90, v31, v86
	v_fmac_f32_e32 v91, v32, v86
	v_fmac_f32_e32 v92, v33, v86
	v_fmac_f32_e32 v94, v19, v86
	v_fmac_f32_e32 v95, v20, v86
	v_fmac_f32_e32 v96, v21, v86
	v_fmamk_f32 v84, v67, 0xbb000000, v84
	v_fmac_f32_e32 v83, v82, v82
	v_fmac_f32_e32 v90, v35, v87
	v_fmac_f32_e32 v91, v36, v87
	v_fmac_f32_e32 v92, v37, v87
	v_fmac_f32_e32 v94, v23, v87
	v_fmac_f32_e32 v95, v24, v87
	v_fmac_f32_e32 v96, v25, v87
	v_fmamk_f32 v85, v67, 0xbb000000, v85
	v_fmac_f32_e32 v83, v84, v84
	v_fmac_f32_e32 v90, v15, v88
	v_fmac_f32_e32 v91, v16, v88
	v_fmac_f32_e32 v92, v17, v88
	v_fmac_f32_e32 v94, v11, v88
	v_fmac_f32_e32 v95, v12, v88
	v_fmac_f32_e32 v96, v13, v88
	v_fmamk_f32 v86, v67, 0xbb000000, v86
	v_fmac_f32_e32 v83, v85, v85
	v_fmac_f32_e32 v90, v7, v89
	v_fmac_f32_e32 v91, v8, v89
	v_fmac_f32_e32 v92, v9, v89
	v_fmac_f32_e32 v94, v3, v89
	v_fmac_f32_e32 v95, v4, v89
	v_fmac_f32_e32 v96, v5, v89
	v_fmamk_f32 v87, v67, 0xbb000000, v87
	v_fmac_f32_e32 v83, v86, v86
	v_cndmask_b32_e64 v97, v94, v90, s[8:9]
	v_cndmask_b32_e64 v90, v90, v94, s[8:9]
	v_cndmask_b32_e64 v94, v95, v91, s[8:9]
	v_cndmask_b32_e64 v91, v91, v95, s[8:9]
	v_cndmask_b32_e64 v95, v96, v92, s[8:9]
	v_cndmask_b32_e64 v92, v92, v96, s[8:9]
	v_fmamk_f32 v88, v67, 0xbb000000, v88
	v_fmac_f32_e32 v83, v87, v87
	ds_bpermute_b32 v72, v79, v72
	ds_bpermute_b32 v90, v79, v90
	ds_bpermute_b32 v91, v79, v91
	ds_bpermute_b32 v92, v79, v92
	v_fmamk_f32 v89, v67, 0xbb000000, v89
	v_fmac_f32_e32 v83, v88, v88
	v_fmac_f32_e32 v83, v89, v89
	ds_bpermute_b32 v82, v79, v83
	s_waitcnt lgkmcnt(0)
	v_add_f32_e32 v72, v98, v72
	s_waitcnt lgkmcnt(0)
	v_add_f32_e32 v90, v97, v90
	s_waitcnt lgkmcnt(0)
	v_add_f32_e32 v91, v94, v91
	s_waitcnt lgkmcnt(0)
	v_add_f32_e32 v92, v95, v92
	v_cndmask_b32_e64 v94, v91, v72, s[2:3]
	v_cndmask_b32_e64 v72, v72, v91, s[2:3]
	v_cndmask_b32_e64 v84, v90, v92, s[2:3]
	ds_bpermute_b32 v72, v78, v72
	ds_bpermute_b32 v84, v78, v84
	s_waitcnt lgkmcnt(0)
	v_add_f32_e32 v82, v83, v82
	ds_bpermute_b32 v83, v78, v82
	v_cndmask_b32_e64 v85, v92, v90, s[2:3]
	s_waitcnt lgkmcnt(0)
	v_add_f32_e32 v72, v94, v72
	s_waitcnt lgkmcnt(0)
	v_add_f32_e32 v84, v85, v84
	v_cndmask_b32_e64 v85, v72, v84, s[4:5]
	s_waitcnt lgkmcnt(0)
	v_add_f32_e32 v82, v82, v83
	s_nop 1
	v_mov_b32_dpp v85, v85 row_ror:8 row_mask:0xf bank_mask:0xf
	s_nop 1
	v_mov_b32_dpp v83, v82 row_ror:8 row_mask:0xf bank_mask:0xf
	v_cndmask_b32_e64 v72, v84, v72, s[4:5]
	s_waitcnt lgkmcnt(0)
	v_add_f32_e32 v72, v72, v85
	s_waitcnt lgkmcnt(0)
	v_add_f32_e32 v82, v82, v83
	s_nop 1
	v_mov_b32_dpp v104, v72 row_half_mirror row_mask:0xf bank_mask:0xf
	s_nop 1
	v_mov_b32_dpp v84, v104 quad_perm:[3,2,1,0] row_mask:0xf bank_mask:0xf
	s_nop 1
	v_mov_b32_dpp v104, v82 row_half_mirror row_mask:0xf bank_mask:0xf
	s_nop 1
	v_mov_b32_dpp v83, v104 quad_perm:[3,2,1,0] row_mask:0xf bank_mask:0xf
	s_waitcnt lgkmcnt(0)
	v_add_f32_e32 v72, v72, v84
	s_waitcnt lgkmcnt(0)
	v_add_f32_e32 v82, v82, v83
	s_nop 1
	v_mov_b32_dpp v84, v72 quad_perm:[2,3,0,1] row_mask:0xf bank_mask:0xf
	s_nop 1
	v_mov_b32_dpp v85, v82 quad_perm:[2,3,0,1] row_mask:0xf bank_mask:0xf
	s_waitcnt lgkmcnt(0)
	v_add_f32_e32 v83, v72, v84
	s_waitcnt lgkmcnt(0)
	v_add_f32_e32 v72, v82, v85
	s_nop 1
	v_mov_b32_dpp v82, v72 quad_perm:[1,0,3,2] row_mask:0xf bank_mask:0xf
	s_nop 1
	v_mov_b32_dpp v84, v83 quad_perm:[1,0,3,2] row_mask:0xf bank_mask:0xf
	s_and_saveexec_b64 s[12:13], s[6:7]
	s_cbranch_execz .LBB7_25
	s_waitcnt lgkmcnt(0)
	v_add_f32_e32 v83, v83, v84
	v_add_f32_e32 v83, v73, v83
	ds_write_b32 v69, v83 offset:144

.LBB7_27:
	s_or_b64 exec, exec, s[16:17]
	v_add3_u32 v66, s24, v81, 5
	v_ashrrev_i32_e32 v67, 31, v66
	s_waitcnt lgkmcnt(0)
	v_lshlrev_b64 v[82:83], 11, v[66:67]
	v_lshl_add_u64 v[90:91], v[70:71], 0, v[82:83]
	s_waitcnt lgkmcnt(0)
	global_load_dwordx4 v[82:85], v[90:91], off
	global_load_dwordx4 v[86:89], v[90:91], off offset:16
	s_waitcnt vmcnt(1)
	v_add_f32_e32 v67, 0, v82
	v_add_f32_e32 v67, v67, v83
	v_add_f32_e32 v67, v67, v84
	v_add_f32_e32 v67, v67, v85
	s_waitcnt vmcnt(0)
	v_add_f32_e32 v67, v67, v86
	v_add_f32_e32 v67, v67, v87
	v_add_f32_e32 v67, v67, v88
	v_add_f32_e32 v67, v67, v89
	ds_bpermute_b32 v97, v79, v67
	v_fma_f32 v72, v62, v82, 0
	v_fma_f32 v93, v58, v82, 0
	v_fmac_f32_e32 v72, v54, v83
	v_fmac_f32_e32 v93, v50, v83
	s_waitcnt lgkmcnt(0)
	v_add_f32_e32 v67, v67, v97
	v_fmac_f32_e32 v72, v46, v84
	v_fmac_f32_e32 v93, v42, v84
	ds_bpermute_b32 v97, v78, v67
	v_fmac_f32_e32 v72, v38, v85
	v_fmac_f32_e32 v93, v26, v85
	v_fmac_f32_e32 v72, v30, v86
	v_fmac_f32_e32 v93, v18, v86
	v_fmac_f32_e32 v72, v34, v87
	v_fmac_f32_e32 v93, v22, v87
	v_fmac_f32_e32 v72, v14, v88
	v_fmac_f32_e32 v93, v10, v88
	v_fmac_f32_e32 v72, v6, v89
	v_fmac_f32_e32 v93, v2, v89
	s_waitcnt lgkmcnt(0)
	v_add_f32_e32 v67, v67, v97
	v_cndmask_b32_e64 v98, v93, v72, s[8:9]
	v_cndmask_b32_e64 v72, v72, v93, s[8:9]
	s_nop 1
	v_mov_b32_dpp v93, v67 row_ror:8 row_mask:0xf bank_mask:0xf
	v_fma_f32 v90, v63, v82, 0
	v_fma_f32 v91, v64, v82, 0
	v_fma_f32 v92, v65, v82, 0
	v_fma_f32 v94, v59, v82, 0
	s_waitcnt lgkmcnt(0)
	v_add_f32_e32 v67, v67, v93
	s_nop 1
	v_mov_b32_dpp v104, v67 row_half_mirror row_mask:0xf bank_mask:0xf
	s_nop 1
	v_mov_b32_dpp v93, v104 quad_perm:[3,2,1,0] row_mask:0xf bank_mask:0xf
	v_fma_f32 v95, v60, v82, 0
	v_fma_f32 v96, v61, v82, 0
	v_fmac_f32_e32 v90, v55, v83
	v_fmac_f32_e32 v91, v56, v83
	s_waitcnt lgkmcnt(0)
	v_add_f32_e32 v67, v67, v93
	s_nop 1
	v_mov_b32_dpp v93, v67 quad_perm:[2,3,0,1] row_mask:0xf bank_mask:0xf
	v_fmac_f32_e32 v92, v57, v83
	v_fmac_f32_e32 v94, v51, v83
	v_fmac_f32_e32 v95, v52, v83
	v_fmac_f32_e32 v96, v53, v83
	s_waitcnt lgkmcnt(0)
	v_add_f32_e32 v67, v67, v93
	s_nop 1
	v_mov_b32_dpp v93, v67 quad_perm:[1,0,3,2] row_mask:0xf bank_mask:0xf
	v_fmac_f32_e32 v90, v47, v84
	v_fmac_f32_e32 v91, v48, v84
	v_fmac_f32_e32 v92, v49, v84
	v_fmac_f32_e32 v94, v43, v84
	s_waitcnt lgkmcnt(0)
	v_add_f32_e32 v67, v67, v93
	v_fmac_f32_e32 v95, v44, v84
	v_fmac_f32_e32 v96, v45, v84
	v_fmamk_f32 v83, v67, 0xbb000000, v83
	v_fmac_f32_e32 v90, v39, v85
	v_fmac_f32_e32 v91, v40, v85
	v_fmac_f32_e32 v92, v41, v85
	v_fmac_f32_e32 v94, v27, v85
	v_fmac_f32_e32 v95, v28, v85
	v_fmac_f32_e32 v96, v29, v85
	v_fmamk_f32 v82, v67, 0xbb000000, v82
	v_mul_f32_e32 v83, v83, v83
	v_fmac_f32_e32 v90, v31, v86
	v_fmac_f32_e32 v91, v32, v86
	v_fmac_f32_e32 v92, v33, v86
	v_fmac_f32_e32 v94, v19, v86
	v_fmac_f32_e32 v95, v20, v86
	v_fmac_f32_e32 v96, v21, v86
	v_fmamk_f32 v84, v67, 0xbb000000, v84
	v_fmac_f32_e32 v83, v82, v82
	v_fmac_f32_e32 v90, v35, v87
	v_fmac_f32_e32 v91, v36, v87
	v_fmac_f32_e32 v92, v37, v87
	v_fmac_f32_e32 v94, v23, v87
	v_fmac_f32_e32 v95, v24, v87
	v_fmac_f32_e32 v96, v25, v87
	v_fmamk_f32 v85, v67, 0xbb000000, v85
	v_fmac_f32_e32 v83, v84, v84
	v_fmac_f32_e32 v90, v15, v88
	v_fmac_f32_e32 v91, v16, v88
	v_fmac_f32_e32 v92, v17, v88
	v_fmac_f32_e32 v94, v11, v88
	v_fmac_f32_e32 v95, v12, v88
	v_fmac_f32_e32 v96, v13, v88
	v_fmamk_f32 v86, v67, 0xbb000000, v86
	v_fmac_f32_e32 v83, v85, v85
	v_fmac_f32_e32 v90, v7, v89
	v_fmac_f32_e32 v91, v8, v89
	v_fmac_f32_e32 v92, v9, v89
	v_fmac_f32_e32 v94, v3, v89
	v_fmac_f32_e32 v95, v4, v89
	v_fmac_f32_e32 v96, v5, v89
	v_fmamk_f32 v87, v67, 0xbb000000, v87
	v_fmac_f32_e32 v83, v86, v86
	v_cndmask_b32_e64 v97, v94, v90, s[8:9]
	v_cndmask_b32_e64 v90, v90, v94, s[8:9]
	v_cndmask_b32_e64 v94, v95, v91, s[8:9]
	v_cndmask_b32_e64 v91, v91, v95, s[8:9]
	v_cndmask_b32_e64 v95, v96, v92, s[8:9]
	v_cndmask_b32_e64 v92, v92, v96, s[8:9]
	v_fmamk_f32 v88, v67, 0xbb000000, v88
	v_fmac_f32_e32 v83, v87, v87
	ds_bpermute_b32 v72, v79, v72
	ds_bpermute_b32 v90, v79, v90
	ds_bpermute_b32 v91, v79, v91
	ds_bpermute_b32 v92, v79, v92
	v_fmamk_f32 v89, v67, 0xbb000000, v89
	v_fmac_f32_e32 v83, v88, v88
	v_fmac_f32_e32 v83, v89, v89
	ds_bpermute_b32 v82, v79, v83
	s_waitcnt lgkmcnt(0)
	v_add_f32_e32 v72, v98, v72
	s_waitcnt lgkmcnt(0)
	v_add_f32_e32 v90, v97, v90
	s_waitcnt lgkmcnt(0)
	v_add_f32_e32 v91, v94, v91
	s_waitcnt lgkmcnt(0)
	v_add_f32_e32 v92, v95, v92
	v_cndmask_b32_e64 v94, v91, v72, s[2:3]
	v_cndmask_b32_e64 v72, v72, v91, s[2:3]
	v_cndmask_b32_e64 v84, v90, v92, s[2:3]
	ds_bpermute_b32 v72, v78, v72
	ds_bpermute_b32 v84, v78, v84
	s_waitcnt lgkmcnt(0)
	v_add_f32_e32 v82, v83, v82
	ds_bpermute_b32 v83, v78, v82
	v_cndmask_b32_e64 v85, v92, v90, s[2:3]
	s_waitcnt lgkmcnt(0)
	v_add_f32_e32 v72, v94, v72
	s_waitcnt lgkmcnt(0)
	v_add_f32_e32 v84, v85, v84
	v_cndmask_b32_e64 v85, v72, v84, s[4:5]
	s_waitcnt lgkmcnt(0)
	v_add_f32_e32 v82, v82, v83
	s_nop 1
	v_mov_b32_dpp v85, v85 row_ror:8 row_mask:0xf bank_mask:0xf
	s_nop 1
	v_mov_b32_dpp v83, v82 row_ror:8 row_mask:0xf bank_mask:0xf
	v_cndmask_b32_e64 v72, v84, v72, s[4:5]
	s_waitcnt lgkmcnt(0)
	v_add_f32_e32 v72, v72, v85
	s_waitcnt lgkmcnt(0)
	v_add_f32_e32 v82, v82, v83
	s_nop 1
	v_mov_b32_dpp v104, v72 row_half_mirror row_mask:0xf bank_mask:0xf
	s_nop 1
	v_mov_b32_dpp v84, v104 quad_perm:[3,2,1,0] row_mask:0xf bank_mask:0xf
	s_nop 1
	v_mov_b32_dpp v104, v82 row_half_mirror row_mask:0xf bank_mask:0xf
	s_nop 1
	v_mov_b32_dpp v83, v104 quad_perm:[3,2,1,0] row_mask:0xf bank_mask:0xf
	s_waitcnt lgkmcnt(0)
	v_add_f32_e32 v72, v72, v84
	s_waitcnt lgkmcnt(0)
	v_add_f32_e32 v82, v82, v83
	s_nop 1
	v_mov_b32_dpp v84, v72 quad_perm:[2,3,0,1] row_mask:0xf bank_mask:0xf
	s_nop 1
	v_mov_b32_dpp v85, v82 quad_perm:[2,3,0,1] row_mask:0xf bank_mask:0xf
	s_waitcnt lgkmcnt(0)
	v_add_f32_e32 v83, v72, v84
	s_waitcnt lgkmcnt(0)
	v_add_f32_e32 v72, v82, v85
	s_nop 1
	v_mov_b32_dpp v82, v72 quad_perm:[1,0,3,2] row_mask:0xf bank_mask:0xf
	s_nop 1
	v_mov_b32_dpp v84, v83 quad_perm:[1,0,3,2] row_mask:0xf bank_mask:0xf
	s_and_saveexec_b64 s[12:13], s[6:7]
	s_cbranch_execz .LBB7_29
	s_waitcnt lgkmcnt(0)
	v_add_f32_e32 v83, v83, v84
	v_add_f32_e32 v83, v73, v83
	ds_write_b32 v69, v83 offset:180

.LBB7_31:
	s_or_b64 exec, exec, s[16:17]
	v_add3_u32 v66, s24, v81, 6
	v_ashrrev_i32_e32 v67, 31, v66
	s_waitcnt lgkmcnt(0)
	v_lshlrev_b64 v[82:83], 11, v[66:67]
	v_lshl_add_u64 v[90:91], v[70:71], 0, v[82:83]
	s_waitcnt lgkmcnt(0)
	global_load_dwordx4 v[82:85], v[90:91], off
	global_load_dwordx4 v[86:89], v[90:91], off offset:16
	s_waitcnt vmcnt(1)
	v_add_f32_e32 v67, 0, v82
	v_add_f32_e32 v67, v67, v83
	v_add_f32_e32 v67, v67, v84
	v_add_f32_e32 v67, v67, v85
	s_waitcnt vmcnt(0)
	v_add_f32_e32 v67, v67, v86
	v_add_f32_e32 v67, v67, v87
	v_add_f32_e32 v67, v67, v88
	v_add_f32_e32 v67, v67, v89
	ds_bpermute_b32 v96, v79, v67
	v_fma_f32 v72, v62, v82, 0
	v_fma_f32 v92, v58, v82, 0
	v_fmac_f32_e32 v72, v54, v83
	v_fmac_f32_e32 v92, v50, v83
	s_waitcnt lgkmcnt(0)
	v_add_f32_e32 v67, v67, v96
	v_fmac_f32_e32 v72, v46, v84
	v_fmac_f32_e32 v92, v42, v84
	ds_bpermute_b32 v96, v78, v67
	v_fmac_f32_e32 v72, v38, v85
	v_fmac_f32_e32 v92, v26, v85
	v_fmac_f32_e32 v72, v30, v86
	v_fmac_f32_e32 v92, v18, v86
	v_fmac_f32_e32 v72, v34, v87
	v_fmac_f32_e32 v92, v22, v87
	v_fmac_f32_e32 v72, v14, v88
	v_fmac_f32_e32 v92, v10, v88
	v_fmac_f32_e32 v72, v6, v89
	v_fmac_f32_e32 v92, v2, v89
	s_waitcnt lgkmcnt(0)
	v_add_f32_e32 v67, v67, v96
	v_cndmask_b32_e64 v97, v92, v72, s[8:9]
	v_cndmask_b32_e64 v72, v72, v92, s[8:9]
	s_nop 1
	v_mov_b32_dpp v92, v67 row_ror:8 row_mask:0xf bank_mask:0xf
	v_fma_f32 v81, v63, v82, 0
	v_fma_f32 v90, v64, v82, 0
	v_fma_f32 v91, v65, v82, 0
	v_fma_f32 v93, v59, v82, 0
	s_waitcnt lgkmcnt(0)
	v_add_f32_e32 v67, v67, v92
	s_nop 1
	v_mov_b32_dpp v104, v67 row_half_mirror row_mask:0xf bank_mask:0xf
	s_nop 1
	v_mov_b32_dpp v92, v104 quad_perm:[3,2,1,0] row_mask:0xf bank_mask:0xf
	v_fma_f32 v94, v60, v82, 0
	v_fma_f32 v95, v61, v82, 0
	v_fmac_f32_e32 v81, v55, v83
	v_fmac_f32_e32 v90, v56, v83
	s_waitcnt lgkmcnt(0)
	v_add_f32_e32 v67, v67, v92
	s_nop 1
	v_mov_b32_dpp v92, v67 quad_perm:[2,3,0,1] row_mask:0xf bank_mask:0xf
	v_fmac_f32_e32 v91, v57, v83
	v_fmac_f32_e32 v93, v51, v83
	v_fmac_f32_e32 v94, v52, v83
	v_fmac_f32_e32 v95, v53, v83
	s_waitcnt lgkmcnt(0)
	v_add_f32_e32 v67, v67, v92
	s_nop 1
	v_mov_b32_dpp v92, v67 quad_perm:[1,0,3,2] row_mask:0xf bank_mask:0xf
	v_fmac_f32_e32 v81, v47, v84
	v_fmac_f32_e32 v90, v48, v84
	v_fmac_f32_e32 v91, v49, v84
	v_fmac_f32_e32 v93, v43, v84
	s_waitcnt lgkmcnt(0)
	v_add_f32_e32 v67, v67, v92
	v_fmac_f32_e32 v94, v44, v84
	v_fmac_f32_e32 v95, v45, v84
	v_fmamk_f32 v83, v67, 0xbb000000, v83
	v_fmac_f32_e32 v81, v39, v85
	v_fmac_f32_e32 v90, v40, v85
	v_fmac_f32_e32 v91, v41, v85
	v_fmac_f32_e32 v93, v27, v85
	v_fmac_f32_e32 v94, v28, v85
	v_fmac_f32_e32 v95, v29, v85
	v_fmamk_f32 v82, v67, 0xbb000000, v82
	v_mul_f32_e32 v83, v83, v83
	v_fmac_f32_e32 v81, v31, v86
	v_fmac_f32_e32 v90, v32, v86
	v_fmac_f32_e32 v91, v33, v86
	v_fmac_f32_e32 v93, v19, v86
	v_fmac_f32_e32 v94, v20, v86
	v_fmac_f32_e32 v95, v21, v86
	v_fmamk_f32 v84, v67, 0xbb000000, v84
	v_fmac_f32_e32 v83, v82, v82
	v_fmac_f32_e32 v81, v35, v87
	v_fmac_f32_e32 v90, v36, v87
	v_fmac_f32_e32 v91, v37, v87
	v_fmac_f32_e32 v93, v23, v87
	v_fmac_f32_e32 v94, v24, v87
	v_fmac_f32_e32 v95, v25, v87
	v_fmamk_f32 v85, v67, 0xbb000000, v85
	v_fmac_f32_e32 v83, v84, v84
	v_fmac_f32_e32 v81, v15, v88
	v_fmac_f32_e32 v90, v16, v88
	v_fmac_f32_e32 v91, v17, v88
	v_fmac_f32_e32 v93, v11, v88
	v_fmac_f32_e32 v94, v12, v88
	v_fmac_f32_e32 v95, v13, v88
	v_fmamk_f32 v86, v67, 0xbb000000, v86
	v_fmac_f32_e32 v83, v85, v85
	v_fmac_f32_e32 v81, v7, v89
	v_fmac_f32_e32 v90, v8, v89
	v_fmac_f32_e32 v91, v9, v89
	v_fmac_f32_e32 v93, v3, v89
	v_fmac_f32_e32 v94, v4, v89
	v_fmac_f32_e32 v95, v5, v89
	v_fmamk_f32 v87, v67, 0xbb000000, v87
	v_fmac_f32_e32 v83, v86, v86
	v_cndmask_b32_e64 v96, v93, v81, s[8:9]
	v_cndmask_b32_e64 v81, v81, v93, s[8:9]
	v_cndmask_b32_e64 v93, v94, v90, s[8:9]
	v_cndmask_b32_e64 v90, v90, v94, s[8:9]
	v_cndmask_b32_e64 v94, v95, v91, s[8:9]
	v_cndmask_b32_e64 v91, v91, v95, s[8:9]
	v_fmamk_f32 v88, v67, 0xbb000000, v88
	v_fmac_f32_e32 v83, v87, v87
	ds_bpermute_b32 v72, v79, v72
	ds_bpermute_b32 v81, v79, v81
	ds_bpermute_b32 v90, v79, v90
	ds_bpermute_b32 v91, v79, v91
	v_fmamk_f32 v89, v67, 0xbb000000, v89
	v_fmac_f32_e32 v83, v88, v88
	v_fmac_f32_e32 v83, v89, v89
	ds_bpermute_b32 v82, v79, v83
	s_waitcnt lgkmcnt(0)
	v_add_f32_e32 v72, v97, v72
	s_waitcnt lgkmcnt(0)
	v_add_f32_e32 v81, v96, v81
	s_waitcnt lgkmcnt(0)
	v_add_f32_e32 v90, v93, v90
	s_waitcnt lgkmcnt(0)
	v_add_f32_e32 v91, v94, v91
	v_cndmask_b32_e64 v93, v90, v72, s[2:3]
	v_cndmask_b32_e64 v72, v72, v90, s[2:3]
	v_cndmask_b32_e64 v84, v81, v91, s[2:3]
	ds_bpermute_b32 v72, v78, v72
	ds_bpermute_b32 v84, v78, v84
	s_waitcnt lgkmcnt(0)
	v_add_f32_e32 v82, v83, v82
	ds_bpermute_b32 v83, v78, v82
	v_cndmask_b32_e64 v81, v91, v81, s[2:3]
	s_waitcnt lgkmcnt(0)
	v_add_f32_e32 v72, v93, v72
	s_waitcnt lgkmcnt(0)
	v_add_f32_e32 v81, v81, v84
	v_cndmask_b32_e64 v84, v72, v81, s[4:5]
	s_waitcnt lgkmcnt(0)
	v_add_f32_e32 v82, v82, v83
	s_nop 1
	v_mov_b32_dpp v84, v84 row_ror:8 row_mask:0xf bank_mask:0xf
	s_nop 1
	v_mov_b32_dpp v83, v82 row_ror:8 row_mask:0xf bank_mask:0xf
	v_cndmask_b32_e64 v72, v81, v72, s[4:5]
	s_waitcnt lgkmcnt(0)
	v_add_f32_e32 v72, v72, v84
	s_waitcnt lgkmcnt(0)
	v_add_f32_e32 v82, v82, v83
	s_nop 1
	v_mov_b32_dpp v104, v72 row_half_mirror row_mask:0xf bank_mask:0xf
	s_nop 1
	v_mov_b32_dpp v81, v104 quad_perm:[3,2,1,0] row_mask:0xf bank_mask:0xf
	s_nop 1
	v_mov_b32_dpp v104, v82 row_half_mirror row_mask:0xf bank_mask:0xf
	s_nop 1
	v_mov_b32_dpp v83, v104 quad_perm:[3,2,1,0] row_mask:0xf bank_mask:0xf
	s_waitcnt lgkmcnt(0)
	v_add_f32_e32 v72, v72, v81
	s_waitcnt lgkmcnt(0)
	v_add_f32_e32 v83, v82, v83
	s_nop 1
	v_mov_b32_dpp v81, v72 quad_perm:[2,3,0,1] row_mask:0xf bank_mask:0xf
	s_nop 1
	v_mov_b32_dpp v84, v83 quad_perm:[2,3,0,1] row_mask:0xf bank_mask:0xf
	s_waitcnt lgkmcnt(0)
	v_add_f32_e32 v82, v72, v81
	s_waitcnt lgkmcnt(0)
	v_add_f32_e32 v72, v83, v84
	s_nop 1
	v_mov_b32_dpp v81, v72 quad_perm:[1,0,3,2] row_mask:0xf bank_mask:0xf
	s_nop 1
	v_mov_b32_dpp v83, v82 quad_perm:[1,0,3,2] row_mask:0xf bank_mask:0xf
	s_and_saveexec_b64 s[12:13], s[6:7]
	s_cbranch_execz .LBB7_33
	s_waitcnt lgkmcnt(0)
	v_add_f32_e32 v82, v82, v83
	v_add_f32_e32 v82, v73, v82
	ds_write_b32 v69, v82 offset:216
.LBB7_33:
	s_or_b64 exec, exec, s[12:13]
	s_and_saveexec_b64 s[16:17], s[10:11]
	s_cbranch_execz .LBB7_35
	s_waitcnt lgkmcnt(0)
	v_add_f32_e32 v69, v72, v81
	v_mov_b32_e32 v72, 0x3727c5ac
	v_fmac_f32_e32 v72, 0x3b000000, v69
	s_mov_b32 s12, 0xf800000
	v_mul_f32_e32 v69, 0x4f800000, v72
	v_cmp_gt_f32_e32 vcc, s12, v72
	v_lshlrev_b32_e32 v66, 1, v66
	s_nop 0
	v_cndmask_b32_e32 v69, v72, v69, vcc
	v_sqrt_f32_e32 v72, v69
	s_nop 0
	v_add_u32_e32 v81, -1, v72
	v_fma_f32 v82, -v81, v72, v69
	v_cmp_ge_f32_e64 s[12:13], 0, v82
	v_add_u32_e32 v82, 1, v72
	s_nop 0
	v_cndmask_b32_e64 v81, v72, v81, s[12:13]
	v_fma_f32 v72, -v82, v72, v69
	v_cmp_lt_f32_e64 s[12:13], 0, v72
	s_nop 1
	v_cndmask_b32_e64 v72, v81, v82, s[12:13]
	v_mul_f32_e32 v81, 0x37800000, v72
	v_cndmask_b32_e32 v72, v72, v81, vcc
	v_mov_b32_e32 v81, 0x260
	v_cmp_class_f32_e32 vcc, v69, v81
	v_mul_f32_e32 v82, 0x3b000000, v67
	s_nop 0
	v_cndmask_b32_e32 v69, v72, v69, vcc
	v_div_scale_f32 v72, s[12:13], v69, v69, 1.0
	v_rcp_f32_e32 v81, v72
	s_nop 0
	v_fma_f32 v67, -v72, v81, 1.0
	v_fmac_f32_e32 v81, v67, v81
	v_div_scale_f32 v67, vcc, 1.0, v69, 1.0
	s_waitcnt lgkmcnt(0)
	v_mul_f32_e32 v83, v67, v81
	v_fma_f32 v84, -v72, v83, v67
	v_fmac_f32_e32 v83, v84, v81
	v_fma_f32 v67, -v72, v83, v67
	v_div_fmas_f32 v67, v67, v81, v83
	v_div_fixup_f32 v83, v67, v69, 1.0
	v_ashrrev_i32_e32 v67, 31, v66
	v_lshl_add_u64 v[66:67], v[66:67], 2, s[14:15]
	global_store_dwordx2 v[66:67], v[82:83], off
.LBB7_35:
	s_or_b64 exec, exec, s[16:17]
	v_or_b32_e32 v69, 7, v80
	v_add_u32_e32 v66, s24, v69
	v_ashrrev_i32_e32 v67, 31, v66
	s_waitcnt lgkmcnt(0)
	v_lshlrev_b64 v[80:81], 11, v[66:67]
	v_lshl_add_u64 v[70:71], v[70:71], 0, v[80:81]
	s_waitcnt lgkmcnt(0)
	global_load_dwordx4 v[80:83], v[70:71], off
	global_load_dwordx4 v[84:87], v[70:71], off offset:16
	s_waitcnt vmcnt(1)
	v_add_f32_e32 v67, 0, v80
	v_fma_f32 v62, v62, v80, 0
	v_fma_f32 v58, v58, v80, 0
	v_add_f32_e32 v67, v67, v81
	v_fmac_f32_e32 v62, v54, v81
	v_fmac_f32_e32 v58, v50, v81
	v_add_f32_e32 v50, v67, v82
	v_fmac_f32_e32 v62, v46, v82
	v_fmac_f32_e32 v58, v42, v82
	v_add_f32_e32 v42, v50, v83
	v_fmac_f32_e32 v62, v38, v83
	v_fmac_f32_e32 v58, v26, v83
	s_waitcnt vmcnt(0)
	v_add_f32_e32 v26, v42, v84
	v_fmac_f32_e32 v62, v30, v84
	v_fmac_f32_e32 v58, v18, v84
	v_add_f32_e32 v18, v26, v85
	v_fmac_f32_e32 v62, v34, v85
	v_fmac_f32_e32 v58, v22, v85
	v_add_f32_e32 v18, v18, v86
	v_fma_f32 v59, v59, v80, 0
	v_fmac_f32_e32 v62, v14, v86
	v_fmac_f32_e32 v58, v10, v86
	v_add_f32_e32 v10, v18, v87
	v_fmac_f32_e32 v59, v51, v81
	v_fmac_f32_e32 v62, v6, v87
	ds_bpermute_b32 v6, v79, v10
	v_fmac_f32_e32 v59, v43, v82
	v_fmac_f32_e32 v59, v27, v83
	v_fmac_f32_e32 v59, v19, v84
	v_fmac_f32_e32 v59, v23, v85
	v_fmac_f32_e32 v59, v11, v86
	v_fmac_f32_e32 v58, v2, v87
	s_waitcnt lgkmcnt(0)
	v_add_f32_e32 v2, v10, v6
	v_fmac_f32_e32 v59, v3, v87
	ds_bpermute_b32 v3, v78, v2
	v_fma_f32 v63, v63, v80, 0
	v_fma_f32 v64, v64, v80, 0
	v_fma_f32 v60, v60, v80, 0
	v_fma_f32 v65, v65, v80, 0
	s_waitcnt lgkmcnt(0)
	v_add_f32_e32 v2, v2, v3
	s_nop 1
	v_mov_b32_dpp v3, v2 row_ror:8 row_mask:0xf bank_mask:0xf
	v_fma_f32 v61, v61, v80, 0
	v_fmac_f32_e32 v63, v55, v81
	v_fmac_f32_e32 v64, v56, v81
	v_fmac_f32_e32 v60, v52, v81
	s_waitcnt lgkmcnt(0)
	v_add_f32_e32 v2, v2, v3
	s_nop 1
	v_mov_b32_dpp v104, v2 row_half_mirror row_mask:0xf bank_mask:0xf
	s_nop 1
	v_mov_b32_dpp v3, v104 quad_perm:[3,2,1,0] row_mask:0xf bank_mask:0xf
	v_fmac_f32_e32 v65, v57, v81
	v_fmac_f32_e32 v61, v53, v81
	v_fmac_f32_e32 v63, v47, v82
	v_fmac_f32_e32 v64, v48, v82
	v_fmac_f32_e32 v60, v44, v82
	s_waitcnt lgkmcnt(0)
	v_add_f32_e32 v2, v2, v3
	v_fmac_f32_e32 v65, v49, v82
	v_fmac_f32_e32 v61, v45, v82
	v_fmac_f32_e32 v63, v39, v83
	v_fmac_f32_e32 v64, v40, v83
	v_fmac_f32_e32 v60, v28, v83
	s_nop 1
	v_mov_b32_dpp v3, v2 quad_perm:[2,3,0,1] row_mask:0xf bank_mask:0xf
	v_fmac_f32_e32 v65, v41, v83
	v_fmac_f32_e32 v61, v29, v83
	v_fmac_f32_e32 v63, v31, v84
	v_fmac_f32_e32 v64, v32, v84
	v_fmac_f32_e32 v60, v20, v84
	v_fmac_f32_e32 v65, v33, v84
	v_fmac_f32_e32 v61, v21, v84
	v_fmac_f32_e32 v63, v35, v85
	v_fmac_f32_e32 v64, v36, v85
	v_fmac_f32_e32 v60, v24, v85
	v_fmac_f32_e32 v65, v37, v85
	v_fmac_f32_e32 v61, v25, v85
	v_fmac_f32_e32 v63, v15, v86
	v_fmac_f32_e32 v64, v16, v86
	v_fmac_f32_e32 v60, v12, v86
	v_fmac_f32_e32 v65, v17, v86
	v_fmac_f32_e32 v61, v13, v86
	v_fmac_f32_e32 v63, v7, v87
	v_fmac_f32_e32 v64, v8, v87
	v_fmac_f32_e32 v60, v4, v87
	v_fmac_f32_e32 v65, v9, v87
	v_fmac_f32_e32 v61, v5, v87
	v_cndmask_b32_e64 v5, v62, v58, s[8:9]
	v_cndmask_b32_e64 v7, v63, v59, s[8:9]
	v_cndmask_b32_e64 v9, v64, v60, s[8:9]
	s_waitcnt lgkmcnt(0)
	v_add_f32_e32 v2, v2, v3
	ds_bpermute_b32 v5, v79, v5
	ds_bpermute_b32 v7, v79, v7
	ds_bpermute_b32 v9, v79, v9
	s_nop 1
	v_mov_b32_dpp v3, v2 quad_perm:[1,0,3,2] row_mask:0xf bank_mask:0xf
	v_cndmask_b32_e64 v11, v65, v61, s[8:9]
	v_cndmask_b32_e64 v4, v58, v62, s[8:9]
	v_cndmask_b32_e64 v6, v59, v63, s[8:9]
	v_cndmask_b32_e64 v8, v60, v64, s[8:9]
	ds_bpermute_b32 v11, v79, v11
	s_waitcnt lgkmcnt(0)
	v_add_f32_e32 v4, v4, v5
	s_waitcnt lgkmcnt(0)
	v_add_f32_e32 v5, v6, v7
	s_waitcnt lgkmcnt(0)
	v_add_f32_e32 v6, v8, v9
	s_waitcnt lgkmcnt(0)
	v_add_f32_e32 v2, v2, v3
	v_cndmask_b32_e64 v8, v6, v4, s[2:3]
	v_cndmask_b32_e64 v4, v4, v6, s[2:3]
	v_fmamk_f32 v6, v2, 0xbb000000, v81
	v_fmamk_f32 v3, v2, 0xbb000000, v80
	v_mul_f32_e32 v6, v6, v6
	v_cndmask_b32_e64 v10, v61, v65, s[8:9]
	v_fmamk_f32 v9, v2, 0xbb000000, v82
	v_fmac_f32_e32 v6, v3, v3
	s_waitcnt lgkmcnt(0)
	v_add_f32_e32 v7, v10, v11
	v_fmamk_f32 v10, v2, 0xbb000000, v83
	v_fmac_f32_e32 v6, v9, v9
	v_fmamk_f32 v11, v2, 0xbb000000, v84
	v_fmac_f32_e32 v6, v10, v10
	v_fmamk_f32 v12, v2, 0xbb000000, v85
	v_fmac_f32_e32 v6, v11, v11
	v_fmamk_f32 v13, v2, 0xbb000000, v86
	v_fmac_f32_e32 v6, v12, v12
	v_fmamk_f32 v14, v2, 0xbb000000, v87
	v_fmac_f32_e32 v6, v13, v13
	v_fmac_f32_e32 v6, v14, v14
	ds_bpermute_b32 v3, v79, v6
	v_cndmask_b32_e64 v9, v5, v7, s[2:3]
	ds_bpermute_b32 v4, v78, v4
	ds_bpermute_b32 v9, v78, v9
	v_cndmask_b32_e64 v5, v7, v5, s[2:3]
	s_waitcnt lgkmcnt(0)
	v_add_f32_e32 v3, v6, v3
	ds_bpermute_b32 v6, v78, v3
	s_waitcnt lgkmcnt(0)
	v_add_f32_e32 v4, v8, v4
	s_waitcnt lgkmcnt(0)
	v_add_f32_e32 v5, v5, v9
	v_cndmask_b32_e64 v7, v4, v5, s[4:5]
	s_nop 1
	v_mov_b32_dpp v7, v7 row_ror:8 row_mask:0xf bank_mask:0xf
	s_waitcnt lgkmcnt(0)
	v_add_f32_e32 v3, v3, v6
	s_nop 1
	v_mov_b32_dpp v6, v3 row_ror:8 row_mask:0xf bank_mask:0xf
	v_cndmask_b32_e64 v4, v5, v4, s[4:5]
	s_waitcnt lgkmcnt(0)
	v_add_f32_e32 v4, v4, v7
	s_nop 1
	v_mov_b32_dpp v104, v4 row_half_mirror row_mask:0xf bank_mask:0xf
	s_nop 1
	v_mov_b32_dpp v5, v104 quad_perm:[3,2,1,0] row_mask:0xf bank_mask:0xf
	s_waitcnt lgkmcnt(0)
	v_add_f32_e32 v3, v3, v6
	s_nop 1
	v_mov_b32_dpp v104, v3 row_half_mirror row_mask:0xf bank_mask:0xf
	s_nop 1
	v_mov_b32_dpp v6, v104 quad_perm:[3,2,1,0] row_mask:0xf bank_mask:0xf
	s_waitcnt lgkmcnt(0)
	v_add_f32_e32 v4, v4, v5
	s_nop 1
	v_mov_b32_dpp v5, v4 quad_perm:[2,3,0,1] row_mask:0xf bank_mask:0xf
	s_waitcnt lgkmcnt(0)
	v_add_f32_e32 v3, v3, v6
	s_nop 1
	v_mov_b32_dpp v6, v3 quad_perm:[2,3,0,1] row_mask:0xf bank_mask:0xf
	s_waitcnt lgkmcnt(0)
	v_add_f32_e32 v5, v4, v5
	s_waitcnt lgkmcnt(0)
	v_add_f32_e32 v3, v3, v6
	s_nop 1
	v_mov_b32_dpp v4, v3 quad_perm:[1,0,3,2] row_mask:0xf bank_mask:0xf
	s_nop 1
	v_mov_b32_dpp v6, v5 quad_perm:[1,0,3,2] row_mask:0xf bank_mask:0xf
	s_and_saveexec_b64 s[2:3], s[6:7]
	s_cbranch_execz .LBB7_37
	s_waitcnt lgkmcnt(0)
	v_add_f32_e32 v5, v5, v6
	v_add_f32_e32 v5, v73, v5
	v_mad_u32_u24 v6, v69, 36, v68
	ds_write_b32 v6, v5
.LBB7_37:
	s_or_b64 exec, exec, s[2:3]
	s_and_saveexec_b64 s[4:5], s[10:11]
	s_cbranch_execz .LBB7_39
	s_waitcnt lgkmcnt(0)
	v_add_f32_e32 v3, v3, v4
	v_mov_b32_e32 v4, 0x3727c5ac
	v_fmac_f32_e32 v4, 0x3b000000, v3
	s_mov_b32 s2, 0xf800000
	v_mul_f32_e32 v3, 0x4f800000, v4
	v_cmp_gt_f32_e32 vcc, s2, v4
	v_mul_f32_e32 v2, 0x3b000000, v2
	s_nop 0
	v_cndmask_b32_e32 v3, v4, v3, vcc
	v_sqrt_f32_e32 v4, v3
	s_nop 0
	v_add_u32_e32 v5, -1, v4
	s_waitcnt lgkmcnt(0)
	v_fma_f32 v6, -v5, v4, v3
	v_cmp_ge_f32_e64 s[2:3], 0, v6
	v_add_u32_e32 v6, 1, v4
	s_nop 0
	v_cndmask_b32_e64 v5, v4, v5, s[2:3]
	v_fma_f32 v4, -v6, v4, v3
	v_cmp_lt_f32_e64 s[2:3], 0, v4
	s_nop 1
	v_cndmask_b32_e64 v4, v5, v6, s[2:3]
	v_mul_f32_e32 v5, 0x37800000, v4
	v_cndmask_b32_e32 v4, v4, v5, vcc
	v_mov_b32_e32 v5, 0x260
	v_cmp_class_f32_e32 vcc, v3, v5
	s_nop 1
	v_cndmask_b32_e32 v3, v4, v3, vcc
	v_div_scale_f32 v4, s[2:3], v3, v3, 1.0
	v_rcp_f32_e32 v5, v4
	s_nop 0
	v_fma_f32 v6, -v4, v5, 1.0
	v_fmac_f32_e32 v5, v6, v5
	v_div_scale_f32 v6, vcc, 1.0, v3, 1.0
	v_mul_f32_e32 v7, v6, v5
	v_fma_f32 v8, -v4, v7, v6
	v_fmac_f32_e32 v7, v8, v5
	v_fma_f32 v4, -v4, v7, v6
	v_div_fmas_f32 v4, v4, v5, v7
	v_div_fixup_f32 v3, v4, v3, 1.0
	v_lshlrev_b32_e32 v4, 1, v66
	v_ashrrev_i32_e32 v5, 31, v4
	v_lshl_add_u64 v[4:5], v[4:5], 2, s[14:15]
	global_store_dwordx2 v[4:5], v[2:3], off

	.amdhsa_kernel _Z18fused_router_wprepILb1EEvPKfS1_S1_PKiPfS4_PiS5_S5_S5_S4_S1_PDF16_S6_S1_S6_
		.amdhsa_group_segment_fixed_size 34432
		.amdhsa_private_segment_fixed_size 0
		.amdhsa_kernarg_size 128
		.amdhsa_user_sgpr_count 2
		.amdhsa_user_sgpr_dispatch_ptr 0
		.amdhsa_user_sgpr_queue_ptr 0
		.amdhsa_user_sgpr_kernarg_segment_ptr 1
		.amdhsa_user_sgpr_dispatch_id 0
		.amdhsa_user_sgpr_kernarg_preload_length 0
		.amdhsa_user_sgpr_kernarg_preload_offset 0
		.amdhsa_user_sgpr_private_segment_size 0
		.amdhsa_uses_dynamic_stack 0
		.amdhsa_enable_private_segment 0
		.amdhsa_system_sgpr_workgroup_id_x 1
		.amdhsa_system_sgpr_workgroup_id_y 0
		.amdhsa_system_sgpr_workgroup_id_z 0
		.amdhsa_system_sgpr_workgroup_info 0
		.amdhsa_system_vgpr_workitem_id 0
		.amdhsa_next_free_vgpr 105
		.amdhsa_next_free_sgpr 96
		.amdhsa_accum_offset 108
		.amdhsa_reserve_vcc 1
		.amdhsa_float_round_mode_32 0
		.amdhsa_float_round_mode_16_64 0
		.amdhsa_float_denorm_mode_32 3
		.amdhsa_float_denorm_mode_16_64 3
		.amdhsa_dx10_clamp 1
		.amdhsa_ieee_mode 1
		.amdhsa_fp16_overflow 0
		.amdhsa_tg_split 0
		.amdhsa_exception_fp_ieee_invalid_op 0
		.amdhsa_exception_fp_denorm_src 0
		.amdhsa_exception_fp_ieee_div_zero 0
		.amdhsa_exception_fp_ieee_overflow 0
		.amdhsa_exception_fp_ieee_underflow 0
		.amdhsa_exception_fp_ieee_inexact 0
		.amdhsa_exception_int_div_zero 0
	.end_amdhsa_kernel

.LBB8_6:
	s_andn2_b64 vcc, exec, s[4:5]
	s_cbranch_vccnz .LBB8_70
	s_load_dwordx4 s[4:7], s[0:1], 0x0
	s_load_dwordx2 s[8:9], s[0:1], 0x10
	v_lshrrev_b32_e32 v78, 3, v0
	v_and_b32_e32 v87, 24, v78
	s_lshl_b32 s24, s2, 5
	v_and_b32_e32 v89, 63, v0
	v_or_b32_e32 v76, s24, v87
	v_lshlrev_b32_e32 v2, 5, v89
	v_mov_b32_e32 v3, 0
	v_ashrrev_i32_e32 v77, 31, v76
	s_waitcnt lgkmcnt(0)
	v_lshl_add_u64 v[74:75], s[4:5], 0, v[2:3]
	v_lshlrev_b64 v[2:3], 11, v[76:77]
	v_lshl_add_u64 v[34:35], v[74:75], 0, v[2:3]
	global_load_dwordx4 v[70:73], v[34:35], off
	v_lshlrev_b32_e32 v77, 8, v89
	global_load_dwordx4 v[22:25], v77, s[6:7]
	global_load_dwordx4 v[18:21], v77, s[6:7] offset:16
	global_load_dwordx4 v[14:17], v77, s[6:7] offset:32
	global_load_dwordx4 v[10:13], v77, s[6:7] offset:48
	global_load_dwordx4 v[6:9], v77, s[6:7] offset:64
	global_load_dwordx4 v[2:5], v77, s[6:7] offset:80
	global_load_dwordx4 v[66:69], v[34:35], off offset:16
	global_load_dwordx4 v[26:29], v77, s[6:7] offset:96
	global_load_dwordx4 v[30:33], v77, s[6:7] offset:112
	v_mbcnt_lo_u32_b32 v1, -1, 0
	v_mbcnt_hi_u32_b32 v1, -1, v1
	v_and_b32_e32 v42, 64, v1
	v_xor_b32_e32 v46, 32, v1
	v_add_u32_e32 v53, 64, v42
	v_xor_b32_e32 v47, 16, v1
	v_cmp_lt_i32_e32 vcc, v46, v53
	v_xor_b32_e32 v48, 8, v1
	v_xor_b32_e32 v50, 4, v1
	v_cndmask_b32_e32 v54, v1, v46, vcc
	v_cmp_lt_i32_e32 vcc, v47, v53
	v_xor_b32_e32 v51, 2, v1
	global_load_dwordx4 v[34:37], v77, s[6:7] offset:128
	global_load_dwordx4 v[38:41], v77, s[6:7] offset:144
	v_cndmask_b32_e32 v55, v1, v47, vcc
	v_cmp_lt_i32_e32 vcc, v48, v53
	v_xor_b32_e32 v52, 1, v1
	global_load_dwordx4 v[42:45], v77, s[6:7] offset:160
	v_cndmask_b32_e32 v56, v1, v48, vcc
	v_cmp_lt_i32_e32 vcc, v50, v53
	global_load_dwordx4 v[46:49], v77, s[6:7] offset:176
	global_load_dwordx4 v[62:65], v77, s[6:7] offset:208
	v_cndmask_b32_e32 v57, v1, v50, vcc
	v_cmp_lt_i32_e32 vcc, v51, v53
	v_lshlrev_b32_e32 v84, 2, v54
	v_lshlrev_b32_e32 v81, 2, v55
	v_cndmask_b32_e32 v58, v1, v51, vcc
	v_cmp_lt_i32_e32 vcc, v52, v53
	v_lshlrev_b32_e32 v83, 2, v56
	v_lshlrev_b32_e32 v80, 2, v57
	v_cndmask_b32_e32 v59, v1, v52, vcc
	global_load_dwordx4 v[50:53], v77, s[6:7] offset:192
	v_lshlrev_b32_e32 v79, 2, v58
	v_lshlrev_b32_e32 v82, 2, v59
	global_load_dwordx4 v[58:61], v77, s[6:7] offset:224
	global_load_dwordx4 v[54:57], v77, s[6:7] offset:240
	s_load_dwordx2 s[14:15], s[0:1], 0x28
	s_waitcnt vmcnt(17)
	v_add_f32_e32 v77, 0, v70
	v_add_f32_e32 v77, v77, v71
	v_add_f32_e32 v77, v77, v72
	v_add_f32_e32 v77, v77, v73
	s_waitcnt vmcnt(10)
	v_add_f32_e32 v77, v77, v66
	v_add_f32_e32 v77, v77, v67
	v_add_f32_e32 v77, v77, v68
	v_add_f32_e32 v77, v77, v69
	ds_bpermute_b32 v85, v84, v77
	v_fma_f32 v86, v22, v70, 0
	v_fma_f32 v88, v23, v70, 0
	v_fma_f32 v90, v24, v70, 0
	v_fma_f32 v91, v25, v70, 0
	s_waitcnt lgkmcnt(0)
	v_add_f32_e32 v77, v77, v85
	ds_bpermute_b32 v85, v81, v77
	v_fma_f32 v92, v18, v70, 0
	v_fma_f32 v93, v19, v70, 0
	v_fma_f32 v94, v20, v70, 0
	v_fma_f32 v95, v21, v70, 0
	s_waitcnt lgkmcnt(0)
	v_add_f32_e32 v77, v77, v85
	s_nop 1
	v_mov_b32_dpp v85, v77 row_ror:8 row_mask:0xf bank_mask:0xf
	v_fmac_f32_e32 v86, v14, v71
	v_fmac_f32_e32 v88, v15, v71
	v_fmac_f32_e32 v90, v16, v71
	v_fmac_f32_e32 v91, v17, v71
	s_waitcnt lgkmcnt(0)
	v_add_f32_e32 v77, v77, v85
	s_nop 1
	v_mov_b32_dpp v99, v77 row_half_mirror row_mask:0xf bank_mask:0xf
	s_nop 1
	v_mov_b32_dpp v85, v99 quad_perm:[3,2,1,0] row_mask:0xf bank_mask:0xf
	v_fmac_f32_e32 v92, v10, v71
	v_fmac_f32_e32 v93, v11, v71
	v_fmac_f32_e32 v94, v12, v71
	v_fmac_f32_e32 v95, v13, v71
	s_waitcnt lgkmcnt(0)
	v_add_f32_e32 v77, v77, v85
	s_nop 1
	v_mov_b32_dpp v85, v77 quad_perm:[2,3,0,1] row_mask:0xf bank_mask:0xf
	v_fmac_f32_e32 v86, v6, v72
	v_fmac_f32_e32 v88, v7, v72
	v_fmac_f32_e32 v90, v8, v72
	v_fmac_f32_e32 v91, v9, v72
	s_waitcnt lgkmcnt(0)
	v_add_f32_e32 v77, v77, v85
	s_nop 1
	v_mov_b32_dpp v85, v77 quad_perm:[1,0,3,2] row_mask:0xf bank_mask:0xf
	v_fmac_f32_e32 v92, v2, v72
	v_fmac_f32_e32 v93, v3, v72
	v_fmac_f32_e32 v94, v4, v72
	v_fmac_f32_e32 v95, v5, v72
	s_waitcnt lgkmcnt(0)
	v_add_f32_e32 v77, v77, v85
	v_lshrrev_b32_e32 v85, 1, v0
	v_and_b32_e32 v96, 28, v85
	global_load_dword v85, v96, s[8:9]
	v_fmamk_f32 v71, v77, 0xbb000000, v71
	v_fmamk_f32 v70, v77, 0xbb000000, v70
	v_mul_f32_e32 v71, v71, v71
	v_fmamk_f32 v72, v77, 0xbb000000, v72
	v_fmac_f32_e32 v71, v70, v70
	s_waitcnt vmcnt(10)
	v_fmac_f32_e32 v86, v26, v73
	v_fmac_f32_e32 v88, v27, v73
	v_fmac_f32_e32 v90, v28, v73
	v_fmac_f32_e32 v91, v29, v73
	s_waitcnt vmcnt(9)
	v_fmac_f32_e32 v92, v30, v73
	v_fmac_f32_e32 v93, v31, v73
	v_fmac_f32_e32 v94, v32, v73
	v_fmac_f32_e32 v95, v33, v73
	v_fmamk_f32 v73, v77, 0xbb000000, v73
	v_fmac_f32_e32 v71, v72, v72
	s_waitcnt vmcnt(8)
	v_fmac_f32_e32 v86, v34, v66
	v_fmac_f32_e32 v88, v35, v66
	v_fmac_f32_e32 v90, v36, v66
	v_fmac_f32_e32 v91, v37, v66
	s_waitcnt vmcnt(7)
	v_fmac_f32_e32 v92, v38, v66
	v_fmac_f32_e32 v93, v39, v66
	v_fmac_f32_e32 v94, v40, v66
	v_fmac_f32_e32 v95, v41, v66
	v_fmamk_f32 v66, v77, 0xbb000000, v66
	v_fmac_f32_e32 v71, v73, v73
	s_waitcnt vmcnt(6)
	v_fmac_f32_e32 v86, v42, v67
	v_fmac_f32_e32 v88, v43, v67
	v_fmac_f32_e32 v90, v44, v67
	v_fmac_f32_e32 v91, v45, v67
	s_waitcnt vmcnt(5)
	v_fmac_f32_e32 v92, v46, v67
	v_fmac_f32_e32 v93, v47, v67
	v_fmac_f32_e32 v94, v48, v67
	v_fmac_f32_e32 v95, v49, v67
	v_fmamk_f32 v67, v77, 0xbb000000, v67
	v_fmac_f32_e32 v71, v66, v66
	s_waitcnt vmcnt(3)
	v_fmac_f32_e32 v86, v50, v68
	v_fmac_f32_e32 v88, v51, v68
	v_fmac_f32_e32 v90, v52, v68
	v_fmac_f32_e32 v91, v53, v68
	v_fmac_f32_e32 v92, v62, v68
	v_fmac_f32_e32 v93, v63, v68
	v_fmac_f32_e32 v94, v64, v68
	v_fmac_f32_e32 v95, v65, v68
	v_fmamk_f32 v68, v77, 0xbb000000, v68
	v_fmac_f32_e32 v71, v67, v67
	v_fmamk_f32 v97, v77, 0xbb000000, v69
	v_fmac_f32_e32 v71, v68, v68
	v_fmac_f32_e32 v71, v97, v97
	ds_bpermute_b32 v66, v84, v71
	v_and_b32_e32 v67, 32, v0
	s_waitcnt vmcnt(2)
	v_fmac_f32_e32 v86, v58, v69
	s_waitcnt vmcnt(1)
	v_fmac_f32_e32 v92, v54, v69
	v_cmp_eq_u32_e64 s[10:11], 0, v67
	v_fmac_f32_e32 v88, v59, v69
	v_fmac_f32_e32 v93, v55, v69
	v_cndmask_b32_e64 v68, v86, v92, s[10:11]
	v_fmac_f32_e32 v90, v60, v69
	ds_bpermute_b32 v68, v84, v68
	v_fmac_f32_e32 v94, v56, v69
	v_cndmask_b32_e64 v70, v88, v93, s[10:11]
	v_fmac_f32_e32 v91, v61, v69
	v_fmac_f32_e32 v95, v57, v69
	s_waitcnt lgkmcnt(0)
	v_add_f32_e32 v66, v71, v66
	ds_bpermute_b32 v70, v84, v70
	v_cndmask_b32_e64 v71, v90, v94, s[10:11]
	ds_bpermute_b32 v71, v84, v71
	v_cndmask_b32_e64 v72, v91, v95, s[10:11]
	ds_bpermute_b32 v72, v84, v72
	v_cndmask_b32_e64 v67, v92, v86, s[10:11]
	s_waitcnt lgkmcnt(0)
	v_add_f32_e32 v67, v67, v68
	v_cndmask_b32_e64 v68, v93, v88, s[10:11]
	s_waitcnt lgkmcnt(0)
	v_add_f32_e32 v68, v68, v70
	v_cndmask_b32_e64 v70, v94, v90, s[10:11]
	s_waitcnt lgkmcnt(0)
	v_add_f32_e32 v70, v70, v71
	v_cndmask_b32_e64 v71, v95, v91, s[10:11]
	s_waitcnt lgkmcnt(0)
	v_add_f32_e32 v71, v71, v72
	v_and_b32_e32 v72, 16, v0
	v_cmp_eq_u32_e64 s[2:3], 0, v72
	ds_bpermute_b32 v69, v81, v66
	v_or_b32_e32 v86, 0x4100, v96
	v_cndmask_b32_e64 v72, v70, v67, s[2:3]
	v_cndmask_b32_e64 v67, v67, v70, s[2:3]
	v_cndmask_b32_e64 v70, v68, v71, s[2:3]
	ds_bpermute_b32 v70, v81, v70
	ds_bpermute_b32 v67, v81, v67
	v_cndmask_b32_e64 v68, v71, v68, s[2:3]
	s_waitcnt lgkmcnt(0)
	v_add_f32_e32 v66, v66, v69
	s_nop 1
	v_mov_b32_dpp v69, v66 row_ror:8 row_mask:0xf bank_mask:0xf
	s_waitcnt lgkmcnt(0)
	v_add_f32_e32 v68, v68, v70
	v_and_b32_e32 v70, 8, v0
	s_waitcnt lgkmcnt(0)
	v_add_f32_e32 v67, v72, v67
	v_cmp_eq_u32_e64 s[4:5], 0, v70
	s_waitcnt lgkmcnt(0)
	v_add_f32_e32 v66, v66, v69
	v_mad_u32_u24 v88, v87, 36, v86
	v_cndmask_b32_e64 v70, v68, v67, s[4:5]
	v_cndmask_b32_e64 v67, v67, v68, s[4:5]
	s_nop 1
	v_mov_b32_dpp v67, v67 row_ror:8 row_mask:0xf bank_mask:0xf
	s_nop 1
	v_mov_b32_dpp v99, v66 row_half_mirror row_mask:0xf bank_mask:0xf
	s_nop 1
	v_mov_b32_dpp v68, v99 quad_perm:[3,2,1,0] row_mask:0xf bank_mask:0xf
	s_waitcnt lgkmcnt(0)
	v_add_f32_e32 v67, v70, v67
	s_nop 1
	v_mov_b32_dpp v99, v67 row_half_mirror row_mask:0xf bank_mask:0xf
	s_nop 1
	v_mov_b32_dpp v69, v99 quad_perm:[3,2,1,0] row_mask:0xf bank_mask:0xf
	s_waitcnt lgkmcnt(0)
	v_add_f32_e32 v66, v66, v68
	s_nop 1
	v_mov_b32_dpp v68, v66 quad_perm:[2,3,0,1] row_mask:0xf bank_mask:0xf
	v_and_b32_e32 v70, 7, v0
	v_cmp_eq_u32_e64 s[6:7], 0, v70
	s_waitcnt lgkmcnt(0)
	v_add_f32_e32 v67, v67, v69
	s_nop 1
	v_mov_b32_dpp v69, v67 quad_perm:[2,3,0,1] row_mask:0xf bank_mask:0xf
	s_waitcnt lgkmcnt(0)
	v_add_f32_e32 v66, v66, v68
	s_waitcnt lgkmcnt(0)
	v_add_f32_e32 v68, v67, v69
	s_nop 1
	v_mov_b32_dpp v67, v66 quad_perm:[1,0,3,2] row_mask:0xf bank_mask:0xf
	s_nop 1
	v_mov_b32_dpp v69, v68 quad_perm:[1,0,3,2] row_mask:0xf bank_mask:0xf
	s_and_saveexec_b64 s[8:9], s[6:7]
	s_cbranch_execz .LBB8_9
	s_waitcnt lgkmcnt(0)
	v_add_f32_e32 v68, v68, v69
	s_waitcnt vmcnt(0)
	v_add_f32_e32 v68, v85, v68
	ds_write_b32 v88, v68
.LBB8_9:
	s_or_b64 exec, exec, s[8:9]
	v_cmp_eq_u32_e64 s[8:9], 0, v89
	s_and_saveexec_b64 s[16:17], s[8:9]
	s_cbranch_execz .LBB8_11
	s_waitcnt lgkmcnt(0)
	v_add_f32_e32 v66, v66, v67
	v_mov_b32_e32 v67, 0x3727c5ac
	v_fmac_f32_e32 v67, 0x3b000000, v66
	s_mov_b32 s12, 0xf800000
	v_mul_f32_e32 v66, 0x4f800000, v67
	v_cmp_gt_f32_e32 vcc, s12, v67
	s_nop 1
	v_cndmask_b32_e32 v66, v67, v66, vcc
	v_sqrt_f32_e32 v67, v66
	s_nop 0
	v_add_u32_e32 v68, -1, v67
	s_waitcnt lgkmcnt(0)
	v_fma_f32 v69, -v68, v67, v66
	v_cmp_ge_f32_e64 s[12:13], 0, v69
	v_add_u32_e32 v69, 1, v67
	s_nop 0
	v_cndmask_b32_e64 v68, v67, v68, s[12:13]
	v_fma_f32 v67, -v69, v67, v66
	v_cmp_lt_f32_e64 s[12:13], 0, v67
	s_nop 1
	v_cndmask_b32_e64 v67, v68, v69, s[12:13]
	v_mul_f32_e32 v68, 0x37800000, v67
	v_cndmask_b32_e32 v67, v67, v68, vcc
	v_mov_b32_e32 v68, 0x260
	v_cmp_class_f32_e32 vcc, v66, v68
	s_nop 1
	v_cndmask_b32_e32 v67, v67, v66, vcc
	v_div_scale_f32 v68, s[12:13], v67, v67, 1.0
	v_rcp_f32_e32 v69, v68
	v_mul_f32_e32 v66, 0x3b000000, v77
	v_fma_f32 v70, -v68, v69, 1.0
	v_fmac_f32_e32 v69, v70, v69
	v_div_scale_f32 v70, vcc, 1.0, v67, 1.0
	v_mul_f32_e32 v71, v70, v69
	v_fma_f32 v72, -v68, v71, v70
	v_fmac_f32_e32 v71, v72, v69
	v_fma_f32 v68, -v68, v71, v70
	v_div_fmas_f32 v68, v68, v69, v71
	v_div_fixup_f32 v67, v68, v67, 1.0
	v_lshlrev_b32_e32 v68, 1, v76
	v_ashrrev_i32_e32 v69, 31, v68
	v_lshl_add_u64 v[68:69], v[68:69], 2, s[14:15]
	global_store_dwordx2 v[68:69], v[66:67], off
.LBB8_11:
	s_or_b64 exec, exec, s[16:17]
	v_add3_u32 v76, s24, v87, 1
	v_ashrrev_i32_e32 v77, 31, v76
	s_waitcnt lgkmcnt(0)
	v_lshlrev_b64 v[66:67], 11, v[76:77]
	v_lshl_add_u64 v[90:91], v[74:75], 0, v[66:67]
	global_load_dwordx4 v[70:73], v[90:91], off
	s_waitcnt lgkmcnt(0)
	global_load_dwordx4 v[66:69], v[90:91], off offset:16
	s_waitcnt vmcnt(1)
	v_add_f32_e32 v77, 0, v70
	v_add_f32_e32 v77, v77, v71
	v_add_f32_e32 v77, v77, v72
	v_add_f32_e32 v77, v77, v73
	s_waitcnt vmcnt(0)
	v_add_f32_e32 v77, v77, v66
	v_add_f32_e32 v77, v77, v67
	v_add_f32_e32 v77, v77, v68
	v_add_f32_e32 v77, v77, v69
	ds_bpermute_b32 v97, v84, v77
	v_fma_f32 v89, v22, v70, 0
	v_fma_f32 v93, v18, v70, 0
	v_fmac_f32_e32 v89, v14, v71
	v_fmac_f32_e32 v93, v10, v71
	s_waitcnt lgkmcnt(0)
	v_add_f32_e32 v77, v77, v97
	v_fmac_f32_e32 v89, v6, v72
	v_fmac_f32_e32 v93, v2, v72
	ds_bpermute_b32 v97, v81, v77
	v_fmac_f32_e32 v89, v26, v73
	v_fmac_f32_e32 v93, v30, v73
	v_fmac_f32_e32 v89, v34, v66
	v_fmac_f32_e32 v93, v38, v66
	v_fmac_f32_e32 v89, v42, v67
	v_fmac_f32_e32 v93, v46, v67
	v_fmac_f32_e32 v89, v50, v68
	v_fmac_f32_e32 v93, v62, v68
	v_fmac_f32_e32 v89, v58, v69
	v_fmac_f32_e32 v93, v54, v69
	s_waitcnt lgkmcnt(0)
	v_add_f32_e32 v77, v77, v97
	v_cndmask_b32_e64 v98, v93, v89, s[10:11]
	v_cndmask_b32_e64 v89, v89, v93, s[10:11]
	s_nop 1
	v_mov_b32_dpp v93, v77 row_ror:8 row_mask:0xf bank_mask:0xf
	v_fma_f32 v90, v23, v70, 0
	v_fma_f32 v91, v24, v70, 0
	v_fma_f32 v92, v25, v70, 0
	v_fma_f32 v94, v19, v70, 0
	s_waitcnt lgkmcnt(0)
	v_add_f32_e32 v77, v77, v93
	s_nop 1
	v_mov_b32_dpp v99, v77 row_half_mirror row_mask:0xf bank_mask:0xf
	s_nop 1
	v_mov_b32_dpp v93, v99 quad_perm:[3,2,1,0] row_mask:0xf bank_mask:0xf
	v_fma_f32 v95, v20, v70, 0
	v_fma_f32 v96, v21, v70, 0
	v_fmac_f32_e32 v90, v15, v71
	v_fmac_f32_e32 v91, v16, v71
	s_waitcnt lgkmcnt(0)
	v_add_f32_e32 v77, v77, v93
	s_nop 1
	v_mov_b32_dpp v93, v77 quad_perm:[2,3,0,1] row_mask:0xf bank_mask:0xf
	v_fmac_f32_e32 v92, v17, v71
	v_fmac_f32_e32 v94, v11, v71
	v_fmac_f32_e32 v95, v12, v71
	v_fmac_f32_e32 v96, v13, v71
	s_waitcnt lgkmcnt(0)
	v_add_f32_e32 v77, v77, v93
	s_nop 1
	v_mov_b32_dpp v93, v77 quad_perm:[1,0,3,2] row_mask:0xf bank_mask:0xf
	v_fmac_f32_e32 v90, v7, v72
	v_fmac_f32_e32 v91, v8, v72
	v_fmac_f32_e32 v92, v9, v72
	v_fmac_f32_e32 v94, v3, v72
	s_waitcnt lgkmcnt(0)
	v_add_f32_e32 v77, v77, v93
	v_fmac_f32_e32 v95, v4, v72
	v_fmac_f32_e32 v96, v5, v72
	v_fmamk_f32 v71, v77, 0xbb000000, v71
	v_fmac_f32_e32 v90, v27, v73
	v_fmac_f32_e32 v91, v28, v73
	v_fmac_f32_e32 v92, v29, v73
	v_fmac_f32_e32 v94, v31, v73
	v_fmac_f32_e32 v95, v32, v73
	v_fmac_f32_e32 v96, v33, v73
	v_fmamk_f32 v70, v77, 0xbb000000, v70
	v_mul_f32_e32 v71, v71, v71
	v_fmac_f32_e32 v90, v35, v66
	v_fmac_f32_e32 v91, v36, v66
	v_fmac_f32_e32 v92, v37, v66
	v_fmac_f32_e32 v94, v39, v66
	v_fmac_f32_e32 v95, v40, v66
	v_fmac_f32_e32 v96, v41, v66
	v_fmamk_f32 v72, v77, 0xbb000000, v72
	v_fmac_f32_e32 v71, v70, v70
	v_fmac_f32_e32 v90, v43, v67
	v_fmac_f32_e32 v91, v44, v67
	v_fmac_f32_e32 v92, v45, v67
	v_fmac_f32_e32 v94, v47, v67
	v_fmac_f32_e32 v95, v48, v67
	v_fmac_f32_e32 v96, v49, v67
	v_fmamk_f32 v73, v77, 0xbb000000, v73
	v_fmac_f32_e32 v71, v72, v72
	v_fmac_f32_e32 v90, v51, v68
	v_fmac_f32_e32 v91, v52, v68
	v_fmac_f32_e32 v92, v53, v68
	v_fmac_f32_e32 v94, v63, v68
	v_fmac_f32_e32 v95, v64, v68
	v_fmac_f32_e32 v96, v65, v68
	v_fmamk_f32 v66, v77, 0xbb000000, v66
	v_fmac_f32_e32 v71, v73, v73
	v_fmac_f32_e32 v90, v59, v69
	v_fmac_f32_e32 v91, v60, v69
	v_fmac_f32_e32 v92, v61, v69
	v_fmac_f32_e32 v94, v55, v69
	v_fmac_f32_e32 v95, v56, v69
	v_fmac_f32_e32 v96, v57, v69
	v_fmamk_f32 v67, v77, 0xbb000000, v67
	v_fmac_f32_e32 v71, v66, v66
	v_cndmask_b32_e64 v97, v94, v90, s[10:11]
	v_cndmask_b32_e64 v90, v90, v94, s[10:11]
	v_cndmask_b32_e64 v94, v95, v91, s[10:11]
	v_cndmask_b32_e64 v91, v91, v95, s[10:11]
	v_cndmask_b32_e64 v95, v96, v92, s[10:11]
	v_cndmask_b32_e64 v92, v92, v96, s[10:11]
	v_fmamk_f32 v68, v77, 0xbb000000, v68
	v_fmac_f32_e32 v71, v67, v67
	ds_bpermute_b32 v89, v84, v89
	ds_bpermute_b32 v90, v84, v90
	ds_bpermute_b32 v91, v84, v91
	ds_bpermute_b32 v92, v84, v92
	v_fmamk_f32 v69, v77, 0xbb000000, v69
	v_fmac_f32_e32 v71, v68, v68
	v_fmac_f32_e32 v71, v69, v69
	ds_bpermute_b32 v66, v84, v71
	s_waitcnt lgkmcnt(0)
	v_add_f32_e32 v89, v98, v89
	s_waitcnt lgkmcnt(0)
	v_add_f32_e32 v90, v97, v90
	s_waitcnt lgkmcnt(0)
	v_add_f32_e32 v91, v94, v91
	s_waitcnt lgkmcnt(0)
	v_add_f32_e32 v92, v95, v92
	v_cndmask_b32_e64 v94, v91, v89, s[2:3]
	v_cndmask_b32_e64 v89, v89, v91, s[2:3]
	v_cndmask_b32_e64 v67, v90, v92, s[2:3]
	ds_bpermute_b32 v68, v81, v89
	ds_bpermute_b32 v67, v81, v67
	s_waitcnt lgkmcnt(0)
	v_add_f32_e32 v66, v71, v66
	ds_bpermute_b32 v70, v81, v66
	v_cndmask_b32_e64 v69, v92, v90, s[2:3]
	s_waitcnt lgkmcnt(0)
	v_add_f32_e32 v68, v94, v68
	s_waitcnt lgkmcnt(0)
	v_add_f32_e32 v67, v69, v67
	v_cndmask_b32_e64 v69, v68, v67, s[4:5]
	s_waitcnt lgkmcnt(0)
	v_add_f32_e32 v66, v66, v70
	s_nop 1
	v_mov_b32_dpp v69, v69 row_ror:8 row_mask:0xf bank_mask:0xf
	s_nop 1
	v_mov_b32_dpp v70, v66 row_ror:8 row_mask:0xf bank_mask:0xf
	v_cndmask_b32_e64 v67, v67, v68, s[4:5]
	s_waitcnt lgkmcnt(0)
	v_add_f32_e32 v67, v67, v69
	s_waitcnt lgkmcnt(0)
	v_add_f32_e32 v66, v66, v70
	s_nop 1
	v_mov_b32_dpp v99, v67 row_half_mirror row_mask:0xf bank_mask:0xf
	s_nop 1
	v_mov_b32_dpp v68, v99 quad_perm:[3,2,1,0] row_mask:0xf bank_mask:0xf
	s_nop 1
	v_mov_b32_dpp v99, v66 row_half_mirror row_mask:0xf bank_mask:0xf
	s_nop 1
	v_mov_b32_dpp v69, v99 quad_perm:[3,2,1,0] row_mask:0xf bank_mask:0xf
	s_waitcnt lgkmcnt(0)
	v_add_f32_e32 v67, v67, v68
	s_waitcnt lgkmcnt(0)
	v_add_f32_e32 v66, v66, v69
	s_nop 1
	v_mov_b32_dpp v68, v67 quad_perm:[2,3,0,1] row_mask:0xf bank_mask:0xf
	s_nop 1
	v_mov_b32_dpp v69, v66 quad_perm:[2,3,0,1] row_mask:0xf bank_mask:0xf
	s_waitcnt lgkmcnt(0)
	v_add_f32_e32 v68, v67, v68
	s_waitcnt lgkmcnt(0)
	v_add_f32_e32 v66, v66, v69
	s_nop 1
	v_mov_b32_dpp v67, v66 quad_perm:[1,0,3,2] row_mask:0xf bank_mask:0xf
	s_nop 1
	v_mov_b32_dpp v69, v68 quad_perm:[1,0,3,2] row_mask:0xf bank_mask:0xf
	s_and_saveexec_b64 s[12:13], s[6:7]
	s_cbranch_execz .LBB8_13
	s_waitcnt lgkmcnt(0)
	v_add_f32_e32 v68, v68, v69
	v_add_f32_e32 v68, v85, v68
	ds_write_b32 v88, v68 offset:36
.LBB8_13:
	s_or_b64 exec, exec, s[12:13]
	s_and_saveexec_b64 s[16:17], s[8:9]
	s_cbranch_execz .LBB8_15
	s_waitcnt lgkmcnt(0)
	v_add_f32_e32 v66, v66, v67
	v_mov_b32_e32 v67, 0x3727c5ac
	v_fmac_f32_e32 v67, 0x3b000000, v66
	s_mov_b32 s12, 0xf800000
	v_mul_f32_e32 v66, 0x4f800000, v67
	v_cmp_gt_f32_e32 vcc, s12, v67
	s_nop 1
	v_cndmask_b32_e32 v66, v67, v66, vcc
	v_sqrt_f32_e32 v67, v66
	s_nop 0
	v_add_u32_e32 v68, -1, v67
	s_waitcnt lgkmcnt(0)
	v_fma_f32 v69, -v68, v67, v66
	v_cmp_ge_f32_e64 s[12:13], 0, v69
	v_add_u32_e32 v69, 1, v67
	s_nop 0
	v_cndmask_b32_e64 v68, v67, v68, s[12:13]
	v_fma_f32 v67, -v69, v67, v66
	v_cmp_lt_f32_e64 s[12:13], 0, v67
	s_nop 1
	v_cndmask_b32_e64 v67, v68, v69, s[12:13]
	v_mul_f32_e32 v68, 0x37800000, v67
	v_cndmask_b32_e32 v67, v67, v68, vcc
	v_mov_b32_e32 v68, 0x260
	v_cmp_class_f32_e32 vcc, v66, v68
	s_nop 1
	v_cndmask_b32_e32 v67, v67, v66, vcc
	v_div_scale_f32 v68, s[12:13], v67, v67, 1.0
	v_rcp_f32_e32 v69, v68
	v_mul_f32_e32 v66, 0x3b000000, v77
	v_fma_f32 v70, -v68, v69, 1.0
	v_fmac_f32_e32 v69, v70, v69
	v_div_scale_f32 v70, vcc, 1.0, v67, 1.0
	v_mul_f32_e32 v71, v70, v69
	v_fma_f32 v72, -v68, v71, v70
	v_fmac_f32_e32 v71, v72, v69
	v_fma_f32 v68, -v68, v71, v70
	v_div_fmas_f32 v68, v68, v69, v71
	v_div_fixup_f32 v67, v68, v67, 1.0
	v_lshlrev_b32_e32 v68, 1, v76
	v_ashrrev_i32_e32 v69, 31, v68
	v_lshl_add_u64 v[68:69], v[68:69], 2, s[14:15]
	global_store_dwordx2 v[68:69], v[66:67], off
.LBB8_15:
	s_or_b64 exec, exec, s[16:17]
	v_add3_u32 v66, s24, v87, 2
	s_waitcnt lgkmcnt(0)
	v_ashrrev_i32_e32 v67, 31, v66
	s_waitcnt lgkmcnt(0)
	v_lshlrev_b64 v[68:69], 11, v[66:67]
	v_lshl_add_u64 v[72:73], v[74:75], 0, v[68:69]
	global_load_dwordx4 v[68:71], v[72:73], off
	global_load_dwordx4 v[90:93], v[72:73], off offset:16
	s_waitcnt vmcnt(1)
	v_add_f32_e32 v67, 0, v68
	v_add_f32_e32 v67, v67, v69
	v_add_f32_e32 v67, v67, v70
	v_add_f32_e32 v67, v67, v71
	s_waitcnt vmcnt(0)
	v_add_f32_e32 v67, v67, v90
	v_add_f32_e32 v67, v67, v91
	v_add_f32_e32 v67, v67, v92
	v_add_f32_e32 v67, v67, v93
	ds_bpermute_b32 v97, v84, v67
	v_fma_f32 v72, v22, v68, 0
	v_fma_f32 v89, v18, v68, 0
	v_fmac_f32_e32 v72, v14, v69
	v_fmac_f32_e32 v89, v10, v69
	s_waitcnt lgkmcnt(0)
	v_add_f32_e32 v67, v67, v97
	v_fmac_f32_e32 v72, v6, v70
	v_fmac_f32_e32 v89, v2, v70
	ds_bpermute_b32 v97, v81, v67
	v_fmac_f32_e32 v72, v26, v71
	v_fmac_f32_e32 v89, v30, v71
	v_fmac_f32_e32 v72, v34, v90
	v_fmac_f32_e32 v89, v38, v90
	v_fmac_f32_e32 v72, v42, v91
	v_fmac_f32_e32 v89, v46, v91
	v_fmac_f32_e32 v72, v50, v92
	v_fmac_f32_e32 v89, v62, v92
	v_fmac_f32_e32 v72, v58, v93
	v_fmac_f32_e32 v89, v54, v93
	s_waitcnt lgkmcnt(0)
	v_add_f32_e32 v67, v67, v97
	v_cndmask_b32_e64 v98, v89, v72, s[10:11]
	v_cndmask_b32_e64 v72, v72, v89, s[10:11]
	s_nop 1
	v_mov_b32_dpp v89, v67 row_ror:8 row_mask:0xf bank_mask:0xf
	v_fma_f32 v73, v23, v68, 0
	v_fma_f32 v76, v24, v68, 0
	v_fma_f32 v94, v19, v68, 0
	v_fma_f32 v95, v20, v68, 0
	s_waitcnt lgkmcnt(0)
	v_add_f32_e32 v67, v67, v89
	s_nop 1
	v_mov_b32_dpp v99, v67 row_half_mirror row_mask:0xf bank_mask:0xf
	s_nop 1
	v_mov_b32_dpp v89, v99 quad_perm:[3,2,1,0] row_mask:0xf bank_mask:0xf
	v_fmac_f32_e32 v73, v15, v69
	v_fmac_f32_e32 v76, v16, v69
	v_fmac_f32_e32 v94, v11, v69
	v_fmac_f32_e32 v95, v12, v69
	s_waitcnt lgkmcnt(0)
	v_add_f32_e32 v67, v67, v89
	s_nop 1
	v_mov_b32_dpp v89, v67 quad_perm:[2,3,0,1] row_mask:0xf bank_mask:0xf
	v_fmac_f32_e32 v73, v7, v70
	v_fmac_f32_e32 v76, v8, v70
	v_fmac_f32_e32 v94, v3, v70
	v_fmac_f32_e32 v95, v4, v70
	v_fmac_f32_e32 v73, v27, v71
	v_fmac_f32_e32 v76, v28, v71
	v_fmac_f32_e32 v94, v31, v71
	v_fmac_f32_e32 v95, v32, v71
	v_fmac_f32_e32 v73, v35, v90
	v_fmac_f32_e32 v76, v36, v90
	v_fmac_f32_e32 v94, v39, v90
	v_fmac_f32_e32 v95, v40, v90
	s_waitcnt lgkmcnt(0)
	v_add_f32_e32 v67, v67, v89
	v_fmac_f32_e32 v73, v43, v91
	v_fmac_f32_e32 v76, v44, v91
	v_fmac_f32_e32 v94, v47, v91
	v_fmac_f32_e32 v95, v48, v91
	s_nop 1
	v_mov_b32_dpp v89, v67 quad_perm:[1,0,3,2] row_mask:0xf bank_mask:0xf
	v_fmac_f32_e32 v73, v51, v92
	v_fmac_f32_e32 v76, v52, v92
	v_fmac_f32_e32 v94, v63, v92
	v_fmac_f32_e32 v95, v64, v92
	v_fmac_f32_e32 v73, v59, v93
	v_fmac_f32_e32 v76, v60, v93
	v_fmac_f32_e32 v94, v55, v93
	v_fmac_f32_e32 v95, v56, v93
	v_cndmask_b32_e64 v97, v94, v73, s[10:11]
	v_cndmask_b32_e64 v73, v73, v94, s[10:11]
	v_cndmask_b32_e64 v94, v95, v76, s[10:11]
	v_cndmask_b32_e64 v76, v76, v95, s[10:11]
	v_fma_f32 v77, v25, v68, 0
	v_fma_f32 v96, v21, v68, 0
	ds_bpermute_b32 v72, v84, v72
	ds_bpermute_b32 v76, v84, v76
	v_fmac_f32_e32 v77, v17, v69
	v_fmac_f32_e32 v96, v13, v69
	s_waitcnt lgkmcnt(0)
	v_add_f32_e32 v67, v67, v89
	v_fmac_f32_e32 v77, v9, v70
	v_fmac_f32_e32 v96, v5, v70
	v_fmamk_f32 v69, v67, 0xbb000000, v69
	v_fmac_f32_e32 v77, v29, v71
	v_fmac_f32_e32 v96, v33, v71
	v_fmamk_f32 v68, v67, 0xbb000000, v68
	v_mul_f32_e32 v69, v69, v69
	v_fmac_f32_e32 v77, v37, v90
	v_fmac_f32_e32 v96, v41, v90
	v_fmamk_f32 v70, v67, 0xbb000000, v70
	v_fmac_f32_e32 v69, v68, v68
	v_fmac_f32_e32 v77, v45, v91
	v_fmac_f32_e32 v96, v49, v91
	s_waitcnt lgkmcnt(0)
	v_add_f32_e32 v72, v98, v72
	s_waitcnt lgkmcnt(0)
	v_add_f32_e32 v76, v94, v76
	v_fmamk_f32 v71, v67, 0xbb000000, v71
	v_fmac_f32_e32 v69, v70, v70
	v_fmac_f32_e32 v77, v53, v92
	v_fmac_f32_e32 v96, v65, v92
	v_cndmask_b32_e64 v94, v76, v72, s[2:3]
	v_cndmask_b32_e64 v72, v72, v76, s[2:3]
	v_fmamk_f32 v76, v67, 0xbb000000, v90
	v_fmac_f32_e32 v69, v71, v71
	v_fmac_f32_e32 v77, v61, v93
	v_fmac_f32_e32 v96, v57, v93
	v_fmamk_f32 v89, v67, 0xbb000000, v91
	v_fmac_f32_e32 v69, v76, v76
	v_cndmask_b32_e64 v95, v96, v77, s[10:11]
	v_cndmask_b32_e64 v77, v77, v96, s[10:11]
	v_fmamk_f32 v90, v67, 0xbb000000, v92
	v_fmac_f32_e32 v69, v89, v89
	ds_bpermute_b32 v73, v84, v73
	ds_bpermute_b32 v77, v84, v77
	v_fmamk_f32 v91, v67, 0xbb000000, v93
	v_fmac_f32_e32 v69, v90, v90
	v_fmac_f32_e32 v69, v91, v91
	ds_bpermute_b32 v68, v84, v69
	s_waitcnt lgkmcnt(0)
	v_add_f32_e32 v73, v97, v73
	s_waitcnt lgkmcnt(0)
	v_add_f32_e32 v77, v95, v77
	v_cndmask_b32_e64 v70, v73, v77, s[2:3]
	ds_bpermute_b32 v71, v81, v72
	ds_bpermute_b32 v70, v81, v70
	s_waitcnt lgkmcnt(0)
	v_add_f32_e32 v68, v69, v68
	ds_bpermute_b32 v69, v81, v68
	v_cndmask_b32_e64 v72, v77, v73, s[2:3]
	s_waitcnt lgkmcnt(0)
	v_add_f32_e32 v71, v94, v71
	s_waitcnt lgkmcnt(0)
	v_add_f32_e32 v70, v72, v70
	v_cndmask_b32_e64 v72, v71, v70, s[4:5]
	s_waitcnt lgkmcnt(0)
	v_add_f32_e32 v68, v68, v69
	s_nop 1
	v_mov_b32_dpp v72, v72 row_ror:8 row_mask:0xf bank_mask:0xf
	s_nop 1
	v_mov_b32_dpp v69, v68 row_ror:8 row_mask:0xf bank_mask:0xf
	v_cndmask_b32_e64 v70, v70, v71, s[4:5]
	s_waitcnt lgkmcnt(0)
	v_add_f32_e32 v70, v70, v72
	s_waitcnt lgkmcnt(0)
	v_add_f32_e32 v68, v68, v69
	s_nop 1
	v_mov_b32_dpp v99, v70 row_half_mirror row_mask:0xf bank_mask:0xf
	s_nop 1
	v_mov_b32_dpp v71, v99 quad_perm:[3,2,1,0] row_mask:0xf bank_mask:0xf
	s_nop 1
	v_mov_b32_dpp v99, v68 row_half_mirror row_mask:0xf bank_mask:0xf
	s_nop 1
	v_mov_b32_dpp v69, v99 quad_perm:[3,2,1,0] row_mask:0xf bank_mask:0xf
	s_waitcnt lgkmcnt(0)
	v_add_f32_e32 v70, v70, v71
	s_waitcnt lgkmcnt(0)
	v_add_f32_e32 v68, v68, v69
	s_nop 1
	v_mov_b32_dpp v71, v70 quad_perm:[2,3,0,1] row_mask:0xf bank_mask:0xf
	s_nop 1
	v_mov_b32_dpp v69, v68 quad_perm:[2,3,0,1] row_mask:0xf bank_mask:0xf
	s_waitcnt lgkmcnt(0)
	v_add_f32_e32 v70, v70, v71
	s_waitcnt lgkmcnt(0)
	v_add_f32_e32 v68, v68, v69
	s_nop 1
	v_mov_b32_dpp v69, v68 quad_perm:[1,0,3,2] row_mask:0xf bank_mask:0xf
	s_nop 1
	v_mov_b32_dpp v71, v70 quad_perm:[1,0,3,2] row_mask:0xf bank_mask:0xf
	s_and_saveexec_b64 s[12:13], s[6:7]
	s_cbranch_execz .LBB8_17
	s_waitcnt lgkmcnt(0)
	v_add_f32_e32 v70, v70, v71
	v_add_f32_e32 v70, v85, v70
	ds_write_b32 v88, v70 offset:72
.LBB8_17:
	s_or_b64 exec, exec, s[12:13]
	s_and_saveexec_b64 s[16:17], s[8:9]
	s_cbranch_execz .LBB8_19
	s_waitcnt lgkmcnt(0)
	v_add_f32_e32 v68, v68, v69
	v_mov_b32_e32 v69, 0x3727c5ac
	v_fmac_f32_e32 v69, 0x3b000000, v68
	s_mov_b32 s12, 0xf800000
	v_mul_f32_e32 v68, 0x4f800000, v69
	v_cmp_gt_f32_e32 vcc, s12, v69
	v_lshlrev_b32_e32 v66, 1, v66
	s_nop 0
	v_cndmask_b32_e32 v68, v69, v68, vcc
	v_sqrt_f32_e32 v69, v68
	s_nop 0
	v_add_u32_e32 v70, -1, v69
	s_waitcnt lgkmcnt(0)
	v_fma_f32 v71, -v70, v69, v68
	v_cmp_ge_f32_e64 s[12:13], 0, v71
	v_add_u32_e32 v71, 1, v69
	s_nop 0
	v_cndmask_b32_e64 v70, v69, v70, s[12:13]
	v_fma_f32 v69, -v71, v69, v68
	v_cmp_lt_f32_e64 s[12:13], 0, v69
	s_nop 1
	v_cndmask_b32_e64 v69, v70, v71, s[12:13]
	v_mul_f32_e32 v70, 0x37800000, v69
	v_cndmask_b32_e32 v69, v69, v70, vcc
	v_mov_b32_e32 v70, 0x260
	v_cmp_class_f32_e32 vcc, v68, v70
	s_nop 1
	v_cndmask_b32_e32 v69, v69, v68, vcc
	v_div_scale_f32 v70, s[12:13], v69, v69, 1.0
	v_rcp_f32_e32 v71, v70
	v_mul_f32_e32 v68, 0x3b000000, v67
	v_fma_f32 v67, -v70, v71, 1.0
	v_fmac_f32_e32 v71, v67, v71
	v_div_scale_f32 v67, vcc, 1.0, v69, 1.0
	v_mul_f32_e32 v72, v67, v71
	v_fma_f32 v73, -v70, v72, v67
	v_fmac_f32_e32 v72, v73, v71
	v_fma_f32 v67, -v70, v72, v67
	v_div_fmas_f32 v67, v67, v71, v72
	v_div_fixup_f32 v69, v67, v69, 1.0
	v_ashrrev_i32_e32 v67, 31, v66
	v_lshl_add_u64 v[66:67], v[66:67], 2, s[14:15]
	global_store_dwordx2 v[66:67], v[68:69], off
.LBB8_19:
	s_or_b64 exec, exec, s[16:17]
	v_add3_u32 v66, s24, v87, 3
	v_ashrrev_i32_e32 v67, 31, v66
	s_waitcnt lgkmcnt(0)
	v_lshlrev_b64 v[68:69], 11, v[66:67]
	v_lshl_add_u64 v[72:73], v[74:75], 0, v[68:69]
	s_waitcnt lgkmcnt(0)
	global_load_dwordx4 v[68:71], v[72:73], off
	global_load_dwordx4 v[90:93], v[72:73], off offset:16
	s_waitcnt vmcnt(1)
	v_add_f32_e32 v67, 0, v68
	v_add_f32_e32 v67, v67, v69
	v_add_f32_e32 v67, v67, v70
	v_add_f32_e32 v67, v67, v71
	s_waitcnt vmcnt(0)
	v_add_f32_e32 v67, v67, v90
	v_add_f32_e32 v67, v67, v91
	v_add_f32_e32 v67, v67, v92
	v_add_f32_e32 v67, v67, v93
	ds_bpermute_b32 v97, v84, v67
	v_fma_f32 v72, v22, v68, 0
	v_fma_f32 v89, v18, v68, 0
	v_fmac_f32_e32 v72, v14, v69
	v_fmac_f32_e32 v89, v10, v69
	s_waitcnt lgkmcnt(0)
	v_add_f32_e32 v67, v67, v97
	v_fmac_f32_e32 v72, v6, v70
	v_fmac_f32_e32 v89, v2, v70
	ds_bpermute_b32 v97, v81, v67
	v_fmac_f32_e32 v72, v26, v71
	v_fmac_f32_e32 v89, v30, v71
	v_fmac_f32_e32 v72, v34, v90
	v_fmac_f32_e32 v89, v38, v90
	v_fmac_f32_e32 v72, v42, v91
	v_fmac_f32_e32 v89, v46, v91
	v_fmac_f32_e32 v72, v50, v92
	v_fmac_f32_e32 v89, v62, v92
	v_fmac_f32_e32 v72, v58, v93
	v_fmac_f32_e32 v89, v54, v93
	s_waitcnt lgkmcnt(0)
	v_add_f32_e32 v67, v67, v97
	v_cndmask_b32_e64 v98, v89, v72, s[10:11]
	v_cndmask_b32_e64 v72, v72, v89, s[10:11]
	s_nop 1
	v_mov_b32_dpp v89, v67 row_ror:8 row_mask:0xf bank_mask:0xf
	v_fma_f32 v73, v23, v68, 0
	v_fma_f32 v76, v24, v68, 0
	v_fma_f32 v94, v19, v68, 0
	v_fma_f32 v95, v20, v68, 0
	s_waitcnt lgkmcnt(0)
	v_add_f32_e32 v67, v67, v89
	s_nop 1
	v_mov_b32_dpp v99, v67 row_half_mirror row_mask:0xf bank_mask:0xf
	s_nop 1
	v_mov_b32_dpp v89, v99 quad_perm:[3,2,1,0] row_mask:0xf bank_mask:0xf
	v_fmac_f32_e32 v73, v15, v69
	v_fmac_f32_e32 v76, v16, v69
	v_fmac_f32_e32 v94, v11, v69
	v_fmac_f32_e32 v95, v12, v69
	s_waitcnt lgkmcnt(0)
	v_add_f32_e32 v67, v67, v89
	s_nop 1
	v_mov_b32_dpp v89, v67 quad_perm:[2,3,0,1] row_mask:0xf bank_mask:0xf
	v_fmac_f32_e32 v73, v7, v70
	v_fmac_f32_e32 v76, v8, v70
	v_fmac_f32_e32 v94, v3, v70
	v_fmac_f32_e32 v95, v4, v70
	v_fmac_f32_e32 v73, v27, v71
	v_fmac_f32_e32 v76, v28, v71
	v_fmac_f32_e32 v94, v31, v71
	v_fmac_f32_e32 v95, v32, v71
	v_fmac_f32_e32 v73, v35, v90
	v_fmac_f32_e32 v76, v36, v90
	v_fmac_f32_e32 v94, v39, v90
	v_fmac_f32_e32 v95, v40, v90
	s_waitcnt lgkmcnt(0)
	v_add_f32_e32 v67, v67, v89
	v_fmac_f32_e32 v73, v43, v91
	v_fmac_f32_e32 v76, v44, v91
	v_fmac_f32_e32 v94, v47, v91
	v_fmac_f32_e32 v95, v48, v91
	s_nop 1
	v_mov_b32_dpp v89, v67 quad_perm:[1,0,3,2] row_mask:0xf bank_mask:0xf
	v_fmac_f32_e32 v73, v51, v92
	v_fmac_f32_e32 v76, v52, v92
	v_fmac_f32_e32 v94, v63, v92
	v_fmac_f32_e32 v95, v64, v92
	v_fmac_f32_e32 v73, v59, v93
	v_fmac_f32_e32 v76, v60, v93
	v_fmac_f32_e32 v94, v55, v93
	v_fmac_f32_e32 v95, v56, v93
	v_cndmask_b32_e64 v97, v94, v73, s[10:11]
	v_cndmask_b32_e64 v73, v73, v94, s[10:11]
	v_cndmask_b32_e64 v94, v95, v76, s[10:11]
	v_cndmask_b32_e64 v76, v76, v95, s[10:11]
	v_fma_f32 v77, v25, v68, 0
	v_fma_f32 v96, v21, v68, 0
	ds_bpermute_b32 v72, v84, v72
	ds_bpermute_b32 v76, v84, v76
	v_fmac_f32_e32 v77, v17, v69
	v_fmac_f32_e32 v96, v13, v69
	s_waitcnt lgkmcnt(0)
	v_add_f32_e32 v67, v67, v89
	v_fmac_f32_e32 v77, v9, v70
	v_fmac_f32_e32 v96, v5, v70
	v_fmamk_f32 v69, v67, 0xbb000000, v69
	v_fmac_f32_e32 v77, v29, v71
	v_fmac_f32_e32 v96, v33, v71
	v_fmamk_f32 v68, v67, 0xbb000000, v68
	v_mul_f32_e32 v69, v69, v69
	v_fmac_f32_e32 v77, v37, v90
	v_fmac_f32_e32 v96, v41, v90
	v_fmamk_f32 v70, v67, 0xbb000000, v70
	v_fmac_f32_e32 v69, v68, v68
	v_fmac_f32_e32 v77, v45, v91
	v_fmac_f32_e32 v96, v49, v91
	s_waitcnt lgkmcnt(0)
	v_add_f32_e32 v72, v98, v72
	s_waitcnt lgkmcnt(0)
	v_add_f32_e32 v76, v94, v76
	v_fmamk_f32 v71, v67, 0xbb000000, v71
	v_fmac_f32_e32 v69, v70, v70
	v_fmac_f32_e32 v77, v53, v92
	v_fmac_f32_e32 v96, v65, v92
	v_cndmask_b32_e64 v94, v76, v72, s[2:3]
	v_cndmask_b32_e64 v72, v72, v76, s[2:3]
	v_fmamk_f32 v76, v67, 0xbb000000, v90
	v_fmac_f32_e32 v69, v71, v71
	v_fmac_f32_e32 v77, v61, v93
	v_fmac_f32_e32 v96, v57, v93
	v_fmamk_f32 v89, v67, 0xbb000000, v91
	v_fmac_f32_e32 v69, v76, v76
	v_cndmask_b32_e64 v95, v96, v77, s[10:11]
	v_cndmask_b32_e64 v77, v77, v96, s[10:11]
	v_fmamk_f32 v90, v67, 0xbb000000, v92
	v_fmac_f32_e32 v69, v89, v89
	ds_bpermute_b32 v73, v84, v73
	ds_bpermute_b32 v77, v84, v77
	v_fmamk_f32 v91, v67, 0xbb000000, v93
	v_fmac_f32_e32 v69, v90, v90
	v_fmac_f32_e32 v69, v91, v91
	ds_bpermute_b32 v68, v84, v69
	s_waitcnt lgkmcnt(0)
	v_add_f32_e32 v73, v97, v73
	s_waitcnt lgkmcnt(0)
	v_add_f32_e32 v77, v95, v77
	v_cndmask_b32_e64 v70, v73, v77, s[2:3]
	ds_bpermute_b32 v71, v81, v72
	ds_bpermute_b32 v70, v81, v70
	s_waitcnt lgkmcnt(0)
	v_add_f32_e32 v68, v69, v68
	ds_bpermute_b32 v69, v81, v68
	v_cndmask_b32_e64 v72, v77, v73, s[2:3]
	s_waitcnt lgkmcnt(0)
	v_add_f32_e32 v71, v94, v71
	s_waitcnt lgkmcnt(0)
	v_add_f32_e32 v70, v72, v70
	v_cndmask_b32_e64 v72, v71, v70, s[4:5]
	s_waitcnt lgkmcnt(0)
	v_add_f32_e32 v68, v68, v69
	s_nop 1
	v_mov_b32_dpp v72, v72 row_ror:8 row_mask:0xf bank_mask:0xf
	s_nop 1
	v_mov_b32_dpp v69, v68 row_ror:8 row_mask:0xf bank_mask:0xf
	v_cndmask_b32_e64 v70, v70, v71, s[4:5]
	s_waitcnt lgkmcnt(0)
	v_add_f32_e32 v70, v70, v72
	s_waitcnt lgkmcnt(0)
	v_add_f32_e32 v68, v68, v69
	s_nop 1
	v_mov_b32_dpp v99, v70 row_half_mirror row_mask:0xf bank_mask:0xf
	s_nop 1
	v_mov_b32_dpp v71, v99 quad_perm:[3,2,1,0] row_mask:0xf bank_mask:0xf
	s_nop 1
	v_mov_b32_dpp v99, v68 row_half_mirror row_mask:0xf bank_mask:0xf
	s_nop 1
	v_mov_b32_dpp v69, v99 quad_perm:[3,2,1,0] row_mask:0xf bank_mask:0xf
	s_waitcnt lgkmcnt(0)
	v_add_f32_e32 v70, v70, v71
	s_waitcnt lgkmcnt(0)
	v_add_f32_e32 v68, v68, v69
	s_nop 1
	v_mov_b32_dpp v71, v70 quad_perm:[2,3,0,1] row_mask:0xf bank_mask:0xf
	s_nop 1
	v_mov_b32_dpp v69, v68 quad_perm:[2,3,0,1] row_mask:0xf bank_mask:0xf
	s_waitcnt lgkmcnt(0)
	v_add_f32_e32 v70, v70, v71
	s_waitcnt lgkmcnt(0)
	v_add_f32_e32 v68, v68, v69
	s_nop 1
	v_mov_b32_dpp v69, v68 quad_perm:[1,0,3,2] row_mask:0xf bank_mask:0xf
	s_nop 1
	v_mov_b32_dpp v71, v70 quad_perm:[1,0,3,2] row_mask:0xf bank_mask:0xf
	s_and_saveexec_b64 s[12:13], s[6:7]
	s_cbranch_execz .LBB8_21
	s_waitcnt lgkmcnt(0)
	v_add_f32_e32 v70, v70, v71
	v_add_f32_e32 v70, v85, v70
	ds_write_b32 v88, v70 offset:108

.LBB8_23:
	s_or_b64 exec, exec, s[16:17]
	v_add3_u32 v66, s24, v87, 4
	v_ashrrev_i32_e32 v67, 31, v66
	s_waitcnt lgkmcnt(0)
	v_lshlrev_b64 v[68:69], 11, v[66:67]
	v_lshl_add_u64 v[72:73], v[74:75], 0, v[68:69]
	s_waitcnt lgkmcnt(0)
	global_load_dwordx4 v[68:71], v[72:73], off
	global_load_dwordx4 v[90:93], v[72:73], off offset:16
	s_waitcnt vmcnt(1)
	v_add_f32_e32 v67, 0, v68
	v_add_f32_e32 v67, v67, v69
	v_add_f32_e32 v67, v67, v70
	v_add_f32_e32 v67, v67, v71
	s_waitcnt vmcnt(0)
	v_add_f32_e32 v67, v67, v90
	v_add_f32_e32 v67, v67, v91
	v_add_f32_e32 v67, v67, v92
	v_add_f32_e32 v67, v67, v93
	ds_bpermute_b32 v97, v84, v67
	v_fma_f32 v72, v22, v68, 0
	v_fma_f32 v89, v18, v68, 0
	v_fmac_f32_e32 v72, v14, v69
	v_fmac_f32_e32 v89, v10, v69
	s_waitcnt lgkmcnt(0)
	v_add_f32_e32 v67, v67, v97
	v_fmac_f32_e32 v72, v6, v70
	v_fmac_f32_e32 v89, v2, v70
	ds_bpermute_b32 v97, v81, v67
	v_fmac_f32_e32 v72, v26, v71
	v_fmac_f32_e32 v89, v30, v71
	v_fmac_f32_e32 v72, v34, v90
	v_fmac_f32_e32 v89, v38, v90
	v_fmac_f32_e32 v72, v42, v91
	v_fmac_f32_e32 v89, v46, v91
	v_fmac_f32_e32 v72, v50, v92
	v_fmac_f32_e32 v89, v62, v92
	v_fmac_f32_e32 v72, v58, v93
	v_fmac_f32_e32 v89, v54, v93
	s_waitcnt lgkmcnt(0)
	v_add_f32_e32 v67, v67, v97
	v_cndmask_b32_e64 v98, v89, v72, s[10:11]
	v_cndmask_b32_e64 v72, v72, v89, s[10:11]
	s_nop 1
	v_mov_b32_dpp v89, v67 row_ror:8 row_mask:0xf bank_mask:0xf
	v_fma_f32 v73, v23, v68, 0
	v_fma_f32 v76, v24, v68, 0
	v_fma_f32 v94, v19, v68, 0
	v_fma_f32 v95, v20, v68, 0
	s_waitcnt lgkmcnt(0)
	v_add_f32_e32 v67, v67, v89
	s_nop 1
	v_mov_b32_dpp v99, v67 row_half_mirror row_mask:0xf bank_mask:0xf
	s_nop 1
	v_mov_b32_dpp v89, v99 quad_perm:[3,2,1,0] row_mask:0xf bank_mask:0xf
	v_fmac_f32_e32 v73, v15, v69
	v_fmac_f32_e32 v76, v16, v69
	v_fmac_f32_e32 v94, v11, v69
	v_fmac_f32_e32 v95, v12, v69
	s_waitcnt lgkmcnt(0)
	v_add_f32_e32 v67, v67, v89
	s_nop 1
	v_mov_b32_dpp v89, v67 quad_perm:[2,3,0,1] row_mask:0xf bank_mask:0xf
	v_fmac_f32_e32 v73, v7, v70
	v_fmac_f32_e32 v76, v8, v70
	v_fmac_f32_e32 v94, v3, v70
	v_fmac_f32_e32 v95, v4, v70
	v_fmac_f32_e32 v73, v27, v71
	v_fmac_f32_e32 v76, v28, v71
	v_fmac_f32_e32 v94, v31, v71
	v_fmac_f32_e32 v95, v32, v71
	v_fmac_f32_e32 v73, v35, v90
	v_fmac_f32_e32 v76, v36, v90
	v_fmac_f32_e32 v94, v39, v90
	v_fmac_f32_e32 v95, v40, v90
	s_waitcnt lgkmcnt(0)
	v_add_f32_e32 v67, v67, v89
	v_fmac_f32_e32 v73, v43, v91
	v_fmac_f32_e32 v76, v44, v91
	v_fmac_f32_e32 v94, v47, v91
	v_fmac_f32_e32 v95, v48, v91
	s_nop 1
	v_mov_b32_dpp v89, v67 quad_perm:[1,0,3,2] row_mask:0xf bank_mask:0xf
	v_fmac_f32_e32 v73, v51, v92
	v_fmac_f32_e32 v76, v52, v92
	v_fmac_f32_e32 v94, v63, v92
	v_fmac_f32_e32 v95, v64, v92
	v_fmac_f32_e32 v73, v59, v93
	v_fmac_f32_e32 v76, v60, v93
	v_fmac_f32_e32 v94, v55, v93
	v_fmac_f32_e32 v95, v56, v93
	v_cndmask_b32_e64 v97, v94, v73, s[10:11]
	v_cndmask_b32_e64 v73, v73, v94, s[10:11]
	v_cndmask_b32_e64 v94, v95, v76, s[10:11]
	v_cndmask_b32_e64 v76, v76, v95, s[10:11]
	v_fma_f32 v77, v25, v68, 0
	v_fma_f32 v96, v21, v68, 0
	ds_bpermute_b32 v72, v84, v72
	ds_bpermute_b32 v76, v84, v76
	v_fmac_f32_e32 v77, v17, v69
	v_fmac_f32_e32 v96, v13, v69
	s_waitcnt lgkmcnt(0)
	v_add_f32_e32 v67, v67, v89
	v_fmac_f32_e32 v77, v9, v70
	v_fmac_f32_e32 v96, v5, v70
	v_fmamk_f32 v69, v67, 0xbb000000, v69
	v_fmac_f32_e32 v77, v29, v71
	v_fmac_f32_e32 v96, v33, v71
	v_fmamk_f32 v68, v67, 0xbb000000, v68
	v_mul_f32_e32 v69, v69, v69
	v_fmac_f32_e32 v77, v37, v90
	v_fmac_f32_e32 v96, v41, v90
	v_fmamk_f32 v70, v67, 0xbb000000, v70
	v_fmac_f32_e32 v69, v68, v68
	v_fmac_f32_e32 v77, v45, v91
	v_fmac_f32_e32 v96, v49, v91
	s_waitcnt lgkmcnt(0)
	v_add_f32_e32 v72, v98, v72
	s_waitcnt lgkmcnt(0)
	v_add_f32_e32 v76, v94, v76
	v_fmamk_f32 v71, v67, 0xbb000000, v71
	v_fmac_f32_e32 v69, v70, v70
	v_fmac_f32_e32 v77, v53, v92
	v_fmac_f32_e32 v96, v65, v92
	v_cndmask_b32_e64 v94, v76, v72, s[2:3]
	v_cndmask_b32_e64 v72, v72, v76, s[2:3]
	v_fmamk_f32 v76, v67, 0xbb000000, v90
	v_fmac_f32_e32 v69, v71, v71
	v_fmac_f32_e32 v77, v61, v93
	v_fmac_f32_e32 v96, v57, v93
	v_fmamk_f32 v89, v67, 0xbb000000, v91
	v_fmac_f32_e32 v69, v76, v76
	v_cndmask_b32_e64 v95, v96, v77, s[10:11]
	v_cndmask_b32_e64 v77, v77, v96, s[10:11]
	v_fmamk_f32 v90, v67, 0xbb000000, v92
	v_fmac_f32_e32 v69, v89, v89
	ds_bpermute_b32 v73, v84, v73
	ds_bpermute_b32 v77, v84, v77
	v_fmamk_f32 v91, v67, 0xbb000000, v93
	v_fmac_f32_e32 v69, v90, v90
	v_fmac_f32_e32 v69, v91, v91
	ds_bpermute_b32 v68, v84, v69
	s_waitcnt lgkmcnt(0)
	v_add_f32_e32 v73, v97, v73
	s_waitcnt lgkmcnt(0)
	v_add_f32_e32 v77, v95, v77
	v_cndmask_b32_e64 v70, v73, v77, s[2:3]
	ds_bpermute_b32 v71, v81, v72
	ds_bpermute_b32 v70, v81, v70
	s_waitcnt lgkmcnt(0)
	v_add_f32_e32 v68, v69, v68
	ds_bpermute_b32 v69, v81, v68
	v_cndmask_b32_e64 v72, v77, v73, s[2:3]
	s_waitcnt lgkmcnt(0)
	v_add_f32_e32 v71, v94, v71
	s_waitcnt lgkmcnt(0)
	v_add_f32_e32 v70, v72, v70
	v_cndmask_b32_e64 v72, v71, v70, s[4:5]
	s_waitcnt lgkmcnt(0)
	v_add_f32_e32 v68, v68, v69
	s_nop 1
	v_mov_b32_dpp v72, v72 row_ror:8 row_mask:0xf bank_mask:0xf
	s_nop 1
	v_mov_b32_dpp v69, v68 row_ror:8 row_mask:0xf bank_mask:0xf
	v_cndmask_b32_e64 v70, v70, v71, s[4:5]
	s_waitcnt lgkmcnt(0)
	v_add_f32_e32 v70, v70, v72
	s_waitcnt lgkmcnt(0)
	v_add_f32_e32 v68, v68, v69
	s_nop 1
	v_mov_b32_dpp v99, v70 row_half_mirror row_mask:0xf bank_mask:0xf
	s_nop 1
	v_mov_b32_dpp v71, v99 quad_perm:[3,2,1,0] row_mask:0xf bank_mask:0xf
	s_nop 1
	v_mov_b32_dpp v99, v68 row_half_mirror row_mask:0xf bank_mask:0xf
	s_nop 1
	v_mov_b32_dpp v69, v99 quad_perm:[3,2,1,0] row_mask:0xf bank_mask:0xf
	s_waitcnt lgkmcnt(0)
	v_add_f32_e32 v70, v70, v71
	s_waitcnt lgkmcnt(0)
	v_add_f32_e32 v68, v68, v69
	s_nop 1
	v_mov_b32_dpp v71, v70 quad_perm:[2,3,0,1] row_mask:0xf bank_mask:0xf
	s_nop 1
	v_mov_b32_dpp v69, v68 quad_perm:[2,3,0,1] row_mask:0xf bank_mask:0xf
	s_waitcnt lgkmcnt(0)
	v_add_f32_e32 v70, v70, v71
	s_waitcnt lgkmcnt(0)
	v_add_f32_e32 v68, v68, v69
	s_nop 1
	v_mov_b32_dpp v69, v68 quad_perm:[1,0,3,2] row_mask:0xf bank_mask:0xf
	s_nop 1
	v_mov_b32_dpp v71, v70 quad_perm:[1,0,3,2] row_mask:0xf bank_mask:0xf
	s_and_saveexec_b64 s[12:13], s[6:7]
	s_cbranch_execz .LBB8_25
	s_waitcnt lgkmcnt(0)
	v_add_f32_e32 v70, v70, v71
	v_add_f32_e32 v70, v85, v70
	ds_write_b32 v88, v70 offset:144

.LBB8_27:
	s_or_b64 exec, exec, s[16:17]
	v_add3_u32 v66, s24, v87, 5
	v_ashrrev_i32_e32 v67, 31, v66
	s_waitcnt lgkmcnt(0)
	v_lshlrev_b64 v[68:69], 11, v[66:67]
	v_lshl_add_u64 v[72:73], v[74:75], 0, v[68:69]
	s_waitcnt lgkmcnt(0)
	global_load_dwordx4 v[68:71], v[72:73], off
	global_load_dwordx4 v[90:93], v[72:73], off offset:16
	s_waitcnt vmcnt(1)
	v_add_f32_e32 v67, 0, v68
	v_add_f32_e32 v67, v67, v69
	v_add_f32_e32 v67, v67, v70
	v_add_f32_e32 v67, v67, v71
	s_waitcnt vmcnt(0)
	v_add_f32_e32 v67, v67, v90
	v_add_f32_e32 v67, v67, v91
	v_add_f32_e32 v67, v67, v92
	v_add_f32_e32 v67, v67, v93
	ds_bpermute_b32 v97, v84, v67
	v_fma_f32 v72, v22, v68, 0
	v_fma_f32 v89, v18, v68, 0
	v_fmac_f32_e32 v72, v14, v69
	v_fmac_f32_e32 v89, v10, v69
	s_waitcnt lgkmcnt(0)
	v_add_f32_e32 v67, v67, v97
	v_fmac_f32_e32 v72, v6, v70
	v_fmac_f32_e32 v89, v2, v70
	ds_bpermute_b32 v97, v81, v67
	v_fmac_f32_e32 v72, v26, v71
	v_fmac_f32_e32 v89, v30, v71
	v_fmac_f32_e32 v72, v34, v90
	v_fmac_f32_e32 v89, v38, v90
	v_fmac_f32_e32 v72, v42, v91
	v_fmac_f32_e32 v89, v46, v91
	v_fmac_f32_e32 v72, v50, v92
	v_fmac_f32_e32 v89, v62, v92
	v_fmac_f32_e32 v72, v58, v93
	v_fmac_f32_e32 v89, v54, v93
	s_waitcnt lgkmcnt(0)
	v_add_f32_e32 v67, v67, v97
	v_cndmask_b32_e64 v98, v89, v72, s[10:11]
	v_cndmask_b32_e64 v72, v72, v89, s[10:11]
	s_nop 1
	v_mov_b32_dpp v89, v67 row_ror:8 row_mask:0xf bank_mask:0xf
	v_fma_f32 v73, v23, v68, 0
	v_fma_f32 v76, v24, v68, 0
	v_fma_f32 v94, v19, v68, 0
	v_fma_f32 v95, v20, v68, 0
	s_waitcnt lgkmcnt(0)
	v_add_f32_e32 v67, v67, v89
	s_nop 1
	v_mov_b32_dpp v99, v67 row_half_mirror row_mask:0xf bank_mask:0xf
	s_nop 1
	v_mov_b32_dpp v89, v99 quad_perm:[3,2,1,0] row_mask:0xf bank_mask:0xf
	v_fmac_f32_e32 v73, v15, v69
	v_fmac_f32_e32 v76, v16, v69
	v_fmac_f32_e32 v94, v11, v69
	v_fmac_f32_e32 v95, v12, v69
	s_waitcnt lgkmcnt(0)
	v_add_f32_e32 v67, v67, v89
	s_nop 1
	v_mov_b32_dpp v89, v67 quad_perm:[2,3,0,1] row_mask:0xf bank_mask:0xf
	v_fmac_f32_e32 v73, v7, v70
	v_fmac_f32_e32 v76, v8, v70
	v_fmac_f32_e32 v94, v3, v70
	v_fmac_f32_e32 v95, v4, v70
	v_fmac_f32_e32 v73, v27, v71
	v_fmac_f32_e32 v76, v28, v71
	v_fmac_f32_e32 v94, v31, v71
	v_fmac_f32_e32 v95, v32, v71
	v_fmac_f32_e32 v73, v35, v90
	v_fmac_f32_e32 v76, v36, v90
	v_fmac_f32_e32 v94, v39, v90
	v_fmac_f32_e32 v95, v40, v90
	s_waitcnt lgkmcnt(0)
	v_add_f32_e32 v67, v67, v89
	v_fmac_f32_e32 v73, v43, v91
	v_fmac_f32_e32 v76, v44, v91
	v_fmac_f32_e32 v94, v47, v91
	v_fmac_f32_e32 v95, v48, v91
	s_nop 1
	v_mov_b32_dpp v89, v67 quad_perm:[1,0,3,2] row_mask:0xf bank_mask:0xf
	v_fmac_f32_e32 v73, v51, v92
	v_fmac_f32_e32 v76, v52, v92
	v_fmac_f32_e32 v94, v63, v92
	v_fmac_f32_e32 v95, v64, v92
	v_fmac_f32_e32 v73, v59, v93
	v_fmac_f32_e32 v76, v60, v93
	v_fmac_f32_e32 v94, v55, v93
	v_fmac_f32_e32 v95, v56, v93
	v_cndmask_b32_e64 v97, v94, v73, s[10:11]
	v_cndmask_b32_e64 v73, v73, v94, s[10:11]
	v_cndmask_b32_e64 v94, v95, v76, s[10:11]
	v_cndmask_b32_e64 v76, v76, v95, s[10:11]
	v_fma_f32 v77, v25, v68, 0
	v_fma_f32 v96, v21, v68, 0
	ds_bpermute_b32 v72, v84, v72
	ds_bpermute_b32 v76, v84, v76
	v_fmac_f32_e32 v77, v17, v69
	v_fmac_f32_e32 v96, v13, v69
	s_waitcnt lgkmcnt(0)
	v_add_f32_e32 v67, v67, v89
	v_fmac_f32_e32 v77, v9, v70
	v_fmac_f32_e32 v96, v5, v70
	v_fmamk_f32 v69, v67, 0xbb000000, v69
	v_fmac_f32_e32 v77, v29, v71
	v_fmac_f32_e32 v96, v33, v71
	v_fmamk_f32 v68, v67, 0xbb000000, v68
	v_mul_f32_e32 v69, v69, v69
	v_fmac_f32_e32 v77, v37, v90
	v_fmac_f32_e32 v96, v41, v90
	v_fmamk_f32 v70, v67, 0xbb000000, v70
	v_fmac_f32_e32 v69, v68, v68
	v_fmac_f32_e32 v77, v45, v91
	v_fmac_f32_e32 v96, v49, v91
	s_waitcnt lgkmcnt(0)
	v_add_f32_e32 v72, v98, v72
	s_waitcnt lgkmcnt(0)
	v_add_f32_e32 v76, v94, v76
	v_fmamk_f32 v71, v67, 0xbb000000, v71
	v_fmac_f32_e32 v69, v70, v70
	v_fmac_f32_e32 v77, v53, v92
	v_fmac_f32_e32 v96, v65, v92
	v_cndmask_b32_e64 v94, v76, v72, s[2:3]
	v_cndmask_b32_e64 v72, v72, v76, s[2:3]
	v_fmamk_f32 v76, v67, 0xbb000000, v90
	v_fmac_f32_e32 v69, v71, v71
	v_fmac_f32_e32 v77, v61, v93
	v_fmac_f32_e32 v96, v57, v93
	v_fmamk_f32 v89, v67, 0xbb000000, v91
	v_fmac_f32_e32 v69, v76, v76
	v_cndmask_b32_e64 v95, v96, v77, s[10:11]
	v_cndmask_b32_e64 v77, v77, v96, s[10:11]
	v_fmamk_f32 v90, v67, 0xbb000000, v92
	v_fmac_f32_e32 v69, v89, v89
	ds_bpermute_b32 v73, v84, v73
	ds_bpermute_b32 v77, v84, v77
	v_fmamk_f32 v91, v67, 0xbb000000, v93
	v_fmac_f32_e32 v69, v90, v90
	v_fmac_f32_e32 v69, v91, v91
	ds_bpermute_b32 v68, v84, v69
	s_waitcnt lgkmcnt(0)
	v_add_f32_e32 v73, v97, v73
	s_waitcnt lgkmcnt(0)
	v_add_f32_e32 v77, v95, v77
	v_cndmask_b32_e64 v70, v73, v77, s[2:3]
	ds_bpermute_b32 v71, v81, v72
	ds_bpermute_b32 v70, v81, v70
	s_waitcnt lgkmcnt(0)
	v_add_f32_e32 v68, v69, v68
	ds_bpermute_b32 v69, v81, v68
	v_cndmask_b32_e64 v72, v77, v73, s[2:3]
	s_waitcnt lgkmcnt(0)
	v_add_f32_e32 v71, v94, v71
	s_waitcnt lgkmcnt(0)
	v_add_f32_e32 v70, v72, v70
	v_cndmask_b32_e64 v72, v71, v70, s[4:5]
	s_waitcnt lgkmcnt(0)
	v_add_f32_e32 v68, v68, v69
	s_nop 1
	v_mov_b32_dpp v72, v72 row_ror:8 row_mask:0xf bank_mask:0xf
	s_nop 1
	v_mov_b32_dpp v69, v68 row_ror:8 row_mask:0xf bank_mask:0xf
	v_cndmask_b32_e64 v70, v70, v71, s[4:5]
	s_waitcnt lgkmcnt(0)
	v_add_f32_e32 v70, v70, v72
	s_waitcnt lgkmcnt(0)
	v_add_f32_e32 v68, v68, v69
	s_nop 1
	v_mov_b32_dpp v99, v70 row_half_mirror row_mask:0xf bank_mask:0xf
	s_nop 1
	v_mov_b32_dpp v71, v99 quad_perm:[3,2,1,0] row_mask:0xf bank_mask:0xf
	s_nop 1
	v_mov_b32_dpp v99, v68 row_half_mirror row_mask:0xf bank_mask:0xf
	s_nop 1
	v_mov_b32_dpp v69, v99 quad_perm:[3,2,1,0] row_mask:0xf bank_mask:0xf
	s_waitcnt lgkmcnt(0)
	v_add_f32_e32 v70, v70, v71
	s_waitcnt lgkmcnt(0)
	v_add_f32_e32 v68, v68, v69
	s_nop 1
	v_mov_b32_dpp v71, v70 quad_perm:[2,3,0,1] row_mask:0xf bank_mask:0xf
	s_nop 1
	v_mov_b32_dpp v69, v68 quad_perm:[2,3,0,1] row_mask:0xf bank_mask:0xf
	s_waitcnt lgkmcnt(0)
	v_add_f32_e32 v70, v70, v71
	s_waitcnt lgkmcnt(0)
	v_add_f32_e32 v68, v68, v69
	s_nop 1
	v_mov_b32_dpp v69, v68 quad_perm:[1,0,3,2] row_mask:0xf bank_mask:0xf
	s_nop 1
	v_mov_b32_dpp v71, v70 quad_perm:[1,0,3,2] row_mask:0xf bank_mask:0xf
	s_and_saveexec_b64 s[12:13], s[6:7]
	s_cbranch_execz .LBB8_29
	s_waitcnt lgkmcnt(0)
	v_add_f32_e32 v70, v70, v71
	v_add_f32_e32 v70, v85, v70
	ds_write_b32 v88, v70 offset:180

.LBB8_31:
	s_or_b64 exec, exec, s[16:17]
	v_add3_u32 v66, s24, v87, 6
	v_ashrrev_i32_e32 v67, 31, v66
	s_waitcnt lgkmcnt(0)
	v_lshlrev_b64 v[68:69], 11, v[66:67]
	v_lshl_add_u64 v[72:73], v[74:75], 0, v[68:69]
	s_waitcnt lgkmcnt(0)
	global_load_dwordx4 v[68:71], v[72:73], off
	global_load_dwordx4 v[90:93], v[72:73], off offset:16
	s_waitcnt vmcnt(1)
	v_add_f32_e32 v67, 0, v68
	v_add_f32_e32 v67, v67, v69
	v_add_f32_e32 v67, v67, v70
	v_add_f32_e32 v67, v67, v71
	s_waitcnt vmcnt(0)
	v_add_f32_e32 v67, v67, v90
	v_add_f32_e32 v67, v67, v91
	v_add_f32_e32 v67, v67, v92
	v_add_f32_e32 v67, v67, v93
	ds_bpermute_b32 v96, v84, v67
	v_fma_f32 v72, v22, v68, 0
	v_fma_f32 v87, v18, v68, 0
	v_fmac_f32_e32 v72, v14, v69
	v_fmac_f32_e32 v87, v10, v69
	s_waitcnt lgkmcnt(0)
	v_add_f32_e32 v67, v67, v96
	v_fmac_f32_e32 v72, v6, v70
	v_fmac_f32_e32 v87, v2, v70
	ds_bpermute_b32 v96, v81, v67
	v_fmac_f32_e32 v72, v26, v71
	v_fmac_f32_e32 v87, v30, v71
	v_fmac_f32_e32 v72, v34, v90
	v_fmac_f32_e32 v87, v38, v90
	v_fmac_f32_e32 v72, v42, v91
	v_fmac_f32_e32 v87, v46, v91
	v_fmac_f32_e32 v72, v50, v92
	v_fmac_f32_e32 v87, v62, v92
	v_fmac_f32_e32 v72, v58, v93
	v_fmac_f32_e32 v87, v54, v93
	s_waitcnt lgkmcnt(0)
	v_add_f32_e32 v67, v67, v96
	v_cndmask_b32_e64 v97, v87, v72, s[10:11]
	v_cndmask_b32_e64 v72, v72, v87, s[10:11]
	s_nop 1
	v_mov_b32_dpp v87, v67 row_ror:8 row_mask:0xf bank_mask:0xf
	v_fma_f32 v73, v23, v68, 0
	v_fma_f32 v76, v24, v68, 0
	v_fma_f32 v89, v19, v68, 0
	v_fma_f32 v94, v20, v68, 0
	s_waitcnt lgkmcnt(0)
	v_add_f32_e32 v67, v67, v87
	s_nop 1
	v_mov_b32_dpp v99, v67 row_half_mirror row_mask:0xf bank_mask:0xf
	s_nop 1
	v_mov_b32_dpp v87, v99 quad_perm:[3,2,1,0] row_mask:0xf bank_mask:0xf
	v_fmac_f32_e32 v73, v15, v69
	v_fmac_f32_e32 v76, v16, v69
	v_fmac_f32_e32 v89, v11, v69
	v_fmac_f32_e32 v94, v12, v69
	s_waitcnt lgkmcnt(0)
	v_add_f32_e32 v67, v67, v87
	s_nop 1
	v_mov_b32_dpp v87, v67 quad_perm:[2,3,0,1] row_mask:0xf bank_mask:0xf
	v_fmac_f32_e32 v73, v7, v70
	v_fmac_f32_e32 v76, v8, v70
	v_fmac_f32_e32 v89, v3, v70
	v_fmac_f32_e32 v94, v4, v70
	v_fmac_f32_e32 v73, v27, v71
	v_fmac_f32_e32 v76, v28, v71
	v_fmac_f32_e32 v89, v31, v71
	v_fmac_f32_e32 v94, v32, v71
	v_fmac_f32_e32 v73, v35, v90
	v_fmac_f32_e32 v76, v36, v90
	v_fmac_f32_e32 v89, v39, v90
	v_fmac_f32_e32 v94, v40, v90
	s_waitcnt lgkmcnt(0)
	v_add_f32_e32 v67, v67, v87
	v_fmac_f32_e32 v73, v43, v91
	v_fmac_f32_e32 v76, v44, v91
	v_fmac_f32_e32 v89, v47, v91
	v_fmac_f32_e32 v94, v48, v91
	s_nop 1
	v_mov_b32_dpp v87, v67 quad_perm:[1,0,3,2] row_mask:0xf bank_mask:0xf
	v_fmac_f32_e32 v73, v51, v92
	v_fmac_f32_e32 v76, v52, v92
	v_fmac_f32_e32 v89, v63, v92
	v_fmac_f32_e32 v94, v64, v92
	v_fmac_f32_e32 v73, v59, v93
	v_fmac_f32_e32 v76, v60, v93
	v_fmac_f32_e32 v89, v55, v93
	v_fmac_f32_e32 v94, v56, v93
	v_cndmask_b32_e64 v96, v89, v73, s[10:11]
	v_cndmask_b32_e64 v73, v73, v89, s[10:11]
	v_cndmask_b32_e64 v89, v94, v76, s[10:11]
	v_cndmask_b32_e64 v76, v76, v94, s[10:11]
	v_fma_f32 v77, v25, v68, 0
	v_fma_f32 v95, v21, v68, 0
	ds_bpermute_b32 v72, v84, v72
	ds_bpermute_b32 v76, v84, v76
	v_fmac_f32_e32 v77, v17, v69
	v_fmac_f32_e32 v95, v13, v69
	s_waitcnt lgkmcnt(0)
	v_add_f32_e32 v67, v67, v87
	v_fmac_f32_e32 v77, v9, v70
	v_fmac_f32_e32 v95, v5, v70
	v_fmamk_f32 v69, v67, 0xbb000000, v69
	v_fmac_f32_e32 v77, v29, v71
	v_fmac_f32_e32 v95, v33, v71
	v_fmamk_f32 v68, v67, 0xbb000000, v68
	v_mul_f32_e32 v69, v69, v69
	v_fmac_f32_e32 v77, v37, v90
	v_fmac_f32_e32 v95, v41, v90
	v_fmamk_f32 v70, v67, 0xbb000000, v70
	v_fmac_f32_e32 v69, v68, v68
	v_fmac_f32_e32 v77, v45, v91
	v_fmac_f32_e32 v95, v49, v91
	s_waitcnt lgkmcnt(0)
	v_add_f32_e32 v72, v97, v72
	s_waitcnt lgkmcnt(0)
	v_add_f32_e32 v76, v89, v76
	v_fmamk_f32 v71, v67, 0xbb000000, v71
	v_fmac_f32_e32 v69, v70, v70
	v_fmac_f32_e32 v77, v53, v92
	v_fmac_f32_e32 v95, v65, v92
	v_cndmask_b32_e64 v89, v76, v72, s[2:3]
	v_cndmask_b32_e64 v72, v72, v76, s[2:3]
	v_fmamk_f32 v76, v67, 0xbb000000, v90
	v_fmac_f32_e32 v69, v71, v71
	v_fmac_f32_e32 v77, v61, v93
	v_fmac_f32_e32 v95, v57, v93
	v_fmamk_f32 v87, v67, 0xbb000000, v91
	v_fmac_f32_e32 v69, v76, v76
	v_cndmask_b32_e64 v94, v95, v77, s[10:11]
	v_cndmask_b32_e64 v77, v77, v95, s[10:11]
	v_fmamk_f32 v90, v67, 0xbb000000, v92
	v_fmac_f32_e32 v69, v87, v87
	ds_bpermute_b32 v73, v84, v73
	ds_bpermute_b32 v77, v84, v77
	v_fmamk_f32 v91, v67, 0xbb000000, v93
	v_fmac_f32_e32 v69, v90, v90
	v_fmac_f32_e32 v69, v91, v91
	ds_bpermute_b32 v68, v84, v69
	s_waitcnt lgkmcnt(0)
	v_add_f32_e32 v73, v96, v73
	s_waitcnt lgkmcnt(0)
	v_add_f32_e32 v77, v94, v77
	v_cndmask_b32_e64 v70, v73, v77, s[2:3]
	ds_bpermute_b32 v71, v81, v72
	ds_bpermute_b32 v70, v81, v70
	s_waitcnt lgkmcnt(0)
	v_add_f32_e32 v68, v69, v68
	ds_bpermute_b32 v69, v81, v68
	v_cndmask_b32_e64 v72, v77, v73, s[2:3]
	s_waitcnt lgkmcnt(0)
	v_add_f32_e32 v71, v89, v71
	s_waitcnt lgkmcnt(0)
	v_add_f32_e32 v70, v72, v70
	v_cndmask_b32_e64 v72, v71, v70, s[4:5]
	s_waitcnt lgkmcnt(0)
	v_add_f32_e32 v68, v68, v69
	s_nop 1
	v_mov_b32_dpp v72, v72 row_ror:8 row_mask:0xf bank_mask:0xf
	s_nop 1
	v_mov_b32_dpp v69, v68 row_ror:8 row_mask:0xf bank_mask:0xf
	v_cndmask_b32_e64 v70, v70, v71, s[4:5]
	s_waitcnt lgkmcnt(0)
	v_add_f32_e32 v70, v70, v72
	s_waitcnt lgkmcnt(0)
	v_add_f32_e32 v68, v68, v69
	s_nop 1
	v_mov_b32_dpp v99, v70 row_half_mirror row_mask:0xf bank_mask:0xf
	s_nop 1
	v_mov_b32_dpp v71, v99 quad_perm:[3,2,1,0] row_mask:0xf bank_mask:0xf
	s_nop 1
	v_mov_b32_dpp v99, v68 row_half_mirror row_mask:0xf bank_mask:0xf
	s_nop 1
	v_mov_b32_dpp v69, v99 quad_perm:[3,2,1,0] row_mask:0xf bank_mask:0xf
	s_waitcnt lgkmcnt(0)
	v_add_f32_e32 v70, v70, v71
	s_waitcnt lgkmcnt(0)
	v_add_f32_e32 v68, v68, v69
	s_nop 1
	v_mov_b32_dpp v71, v70 quad_perm:[2,3,0,1] row_mask:0xf bank_mask:0xf
	s_nop 1
	v_mov_b32_dpp v69, v68 quad_perm:[2,3,0,1] row_mask:0xf bank_mask:0xf
	s_waitcnt lgkmcnt(0)
	v_add_f32_e32 v70, v70, v71
	s_waitcnt lgkmcnt(0)
	v_add_f32_e32 v68, v68, v69
	s_nop 1
	v_mov_b32_dpp v69, v68 quad_perm:[1,0,3,2] row_mask:0xf bank_mask:0xf
	s_nop 1
	v_mov_b32_dpp v71, v70 quad_perm:[1,0,3,2] row_mask:0xf bank_mask:0xf
	s_and_saveexec_b64 s[12:13], s[6:7]
	s_cbranch_execz .LBB8_33
	s_waitcnt lgkmcnt(0)
	v_add_f32_e32 v70, v70, v71
	v_add_f32_e32 v70, v85, v70
	ds_write_b32 v88, v70 offset:216

.LBB8_35:
	s_or_b64 exec, exec, s[16:17]
	v_or_b32_e32 v68, 7, v78
	v_add_u32_e32 v66, s24, v68
	v_ashrrev_i32_e32 v67, 31, v66
	s_waitcnt lgkmcnt(0)
	v_lshlrev_b64 v[70:71], 11, v[66:67]
	v_lshl_add_u64 v[88:89], v[74:75], 0, v[70:71]
	global_load_dwordx4 v[70:73], v[88:89], off
	global_load_dwordx4 v[74:77], v[88:89], off offset:16
	s_waitcnt vmcnt(1)
	v_add_f32_e32 v67, 0, v70
	v_fma_f32 v18, v18, v70, 0
	v_add_f32_e32 v67, v67, v71
	v_fmac_f32_e32 v18, v10, v71
	v_add_f32_e32 v10, v67, v72
	v_fmac_f32_e32 v18, v2, v72
	v_add_f32_e32 v2, v10, v73
	s_waitcnt vmcnt(0)
	v_add_f32_e32 v2, v2, v74
	v_add_f32_e32 v2, v2, v75
	v_fma_f32 v19, v19, v70, 0
	v_add_f32_e32 v2, v2, v76
	v_fmac_f32_e32 v19, v11, v71
	v_add_f32_e32 v2, v2, v77
	v_fmac_f32_e32 v19, v3, v72
	ds_bpermute_b32 v3, v84, v2
	v_fma_f32 v22, v22, v70, 0
	v_fma_f32 v23, v23, v70, 0
	v_fma_f32 v24, v24, v70, 0
	v_fma_f32 v20, v20, v70, 0
	s_waitcnt lgkmcnt(0)
	v_add_f32_e32 v2, v2, v3
	ds_bpermute_b32 v3, v81, v2
	v_fmac_f32_e32 v22, v14, v71
	v_fmac_f32_e32 v23, v15, v71
	v_fmac_f32_e32 v24, v16, v71
	v_fmac_f32_e32 v20, v12, v71
	s_waitcnt lgkmcnt(0)
	v_add_f32_e32 v2, v2, v3
	s_nop 1
	v_mov_b32_dpp v3, v2 row_ror:8 row_mask:0xf bank_mask:0xf
	v_fmac_f32_e32 v22, v6, v72
	v_fmac_f32_e32 v23, v7, v72
	v_fmac_f32_e32 v24, v8, v72
	v_fmac_f32_e32 v20, v4, v72
	s_waitcnt lgkmcnt(0)
	v_add_f32_e32 v2, v2, v3
	s_nop 1
	v_mov_b32_dpp v99, v2 row_half_mirror row_mask:0xf bank_mask:0xf
	s_nop 1
	v_mov_b32_dpp v3, v99 quad_perm:[3,2,1,0] row_mask:0xf bank_mask:0xf
	v_fmac_f32_e32 v22, v26, v73
	v_fmac_f32_e32 v23, v27, v73
	v_fmac_f32_e32 v24, v28, v73
	v_fmac_f32_e32 v18, v30, v73
	s_waitcnt lgkmcnt(0)
	v_add_f32_e32 v2, v2, v3
	v_fmac_f32_e32 v19, v31, v73
	v_fmac_f32_e32 v20, v32, v73
	s_nop 1
	v_mov_b32_dpp v3, v2 quad_perm:[2,3,0,1] row_mask:0xf bank_mask:0xf
	v_fma_f32 v25, v25, v70, 0
	v_fma_f32 v21, v21, v70, 0
	v_fmac_f32_e32 v22, v34, v74
	v_fmac_f32_e32 v23, v35, v74
	v_fmac_f32_e32 v24, v36, v74
	v_fmac_f32_e32 v18, v38, v74
	v_fmac_f32_e32 v19, v39, v74
	v_fmac_f32_e32 v20, v40, v74
	v_fmac_f32_e32 v25, v17, v71
	v_fmac_f32_e32 v21, v13, v71
	v_fmac_f32_e32 v22, v42, v75
	v_fmac_f32_e32 v23, v43, v75
	v_fmac_f32_e32 v24, v44, v75
	v_fmac_f32_e32 v18, v46, v75
	v_fmac_f32_e32 v19, v47, v75
	v_fmac_f32_e32 v20, v48, v75
	v_fmac_f32_e32 v25, v9, v72
	v_fmac_f32_e32 v21, v5, v72
	v_fmac_f32_e32 v22, v50, v76
	v_fmac_f32_e32 v23, v51, v76
	v_fmac_f32_e32 v24, v52, v76
	v_fmac_f32_e32 v18, v62, v76
	v_fmac_f32_e32 v19, v63, v76
	v_fmac_f32_e32 v20, v64, v76
	v_fmac_f32_e32 v25, v29, v73
	v_fmac_f32_e32 v21, v33, v73
	v_fmac_f32_e32 v22, v58, v77
	v_fmac_f32_e32 v23, v59, v77
	v_fmac_f32_e32 v24, v60, v77
	v_fmac_f32_e32 v18, v54, v77
	v_fmac_f32_e32 v19, v55, v77
	v_fmac_f32_e32 v20, v56, v77
	v_fmac_f32_e32 v25, v37, v74
	v_fmac_f32_e32 v21, v41, v74
	v_cndmask_b32_e64 v5, v22, v18, s[10:11]
	v_cndmask_b32_e64 v7, v23, v19, s[10:11]
	v_cndmask_b32_e64 v9, v24, v20, s[10:11]
	s_waitcnt lgkmcnt(0)
	v_add_f32_e32 v2, v2, v3
	v_fmac_f32_e32 v25, v45, v75
	v_fmac_f32_e32 v21, v49, v75
	ds_bpermute_b32 v5, v84, v5
	ds_bpermute_b32 v7, v84, v7
	ds_bpermute_b32 v9, v84, v9
	s_nop 1
	v_mov_b32_dpp v3, v2 quad_perm:[1,0,3,2] row_mask:0xf bank_mask:0xf
	v_fmac_f32_e32 v25, v53, v76
	v_fmac_f32_e32 v21, v65, v76
	v_fmac_f32_e32 v25, v61, v77
	v_fmac_f32_e32 v21, v57, v77
	v_cndmask_b32_e64 v11, v25, v21, s[10:11]
	v_cndmask_b32_e64 v4, v18, v22, s[10:11]
	v_cndmask_b32_e64 v6, v19, v23, s[10:11]
	v_cndmask_b32_e64 v8, v20, v24, s[10:11]
	ds_bpermute_b32 v11, v84, v11
	s_waitcnt lgkmcnt(0)
	v_add_f32_e32 v4, v4, v5
	s_waitcnt lgkmcnt(0)
	v_add_f32_e32 v5, v6, v7
	s_waitcnt lgkmcnt(0)
	v_add_f32_e32 v6, v8, v9
	s_waitcnt lgkmcnt(0)
	v_add_f32_e32 v2, v2, v3
	v_cndmask_b32_e64 v8, v6, v4, s[2:3]
	v_cndmask_b32_e64 v4, v4, v6, s[2:3]
	v_fmamk_f32 v6, v2, 0xbb000000, v71
	v_fmamk_f32 v3, v2, 0xbb000000, v70
	v_mul_f32_e32 v6, v6, v6
	v_cndmask_b32_e64 v10, v21, v25, s[10:11]
	v_fmamk_f32 v9, v2, 0xbb000000, v72
	v_fmac_f32_e32 v6, v3, v3
	s_waitcnt lgkmcnt(0)
	v_add_f32_e32 v7, v10, v11
	v_fmamk_f32 v10, v2, 0xbb000000, v73
	v_fmac_f32_e32 v6, v9, v9
	v_fmamk_f32 v11, v2, 0xbb000000, v74
	v_fmac_f32_e32 v6, v10, v10
	v_fmamk_f32 v12, v2, 0xbb000000, v75
	v_fmac_f32_e32 v6, v11, v11
	v_fmamk_f32 v13, v2, 0xbb000000, v76
	v_fmac_f32_e32 v6, v12, v12
	v_fmamk_f32 v14, v2, 0xbb000000, v77
	v_fmac_f32_e32 v6, v13, v13
	v_fmac_f32_e32 v6, v14, v14
	ds_bpermute_b32 v3, v84, v6
	v_cndmask_b32_e64 v9, v5, v7, s[2:3]
	ds_bpermute_b32 v4, v81, v4
	ds_bpermute_b32 v9, v81, v9
	v_cndmask_b32_e64 v5, v7, v5, s[2:3]
	s_waitcnt lgkmcnt(0)
	v_add_f32_e32 v3, v6, v3
	ds_bpermute_b32 v6, v81, v3
	s_waitcnt lgkmcnt(0)
	v_add_f32_e32 v4, v8, v4
	s_waitcnt lgkmcnt(0)
	v_add_f32_e32 v5, v5, v9
	v_cndmask_b32_e64 v7, v4, v5, s[4:5]
	s_nop 1
	v_mov_b32_dpp v7, v7 row_ror:8 row_mask:0xf bank_mask:0xf
	s_waitcnt lgkmcnt(0)
	v_add_f32_e32 v3, v3, v6
	s_nop 1
	v_mov_b32_dpp v6, v3 row_ror:8 row_mask:0xf bank_mask:0xf
	v_cndmask_b32_e64 v4, v5, v4, s[4:5]
	s_waitcnt lgkmcnt(0)
	v_add_f32_e32 v4, v4, v7
	s_nop 1
	v_mov_b32_dpp v99, v4 row_half_mirror row_mask:0xf bank_mask:0xf
	s_nop 1
	v_mov_b32_dpp v5, v99 quad_perm:[3,2,1,0] row_mask:0xf bank_mask:0xf
	s_waitcnt lgkmcnt(0)
	v_add_f32_e32 v3, v3, v6
	s_nop 1
	v_mov_b32_dpp v99, v3 row_half_mirror row_mask:0xf bank_mask:0xf
	s_nop 1
	v_mov_b32_dpp v6, v99 quad_perm:[3,2,1,0] row_mask:0xf bank_mask:0xf
	s_waitcnt lgkmcnt(0)
	v_add_f32_e32 v4, v4, v5
	s_nop 1
	v_mov_b32_dpp v5, v4 quad_perm:[2,3,0,1] row_mask:0xf bank_mask:0xf
	s_waitcnt lgkmcnt(0)
	v_add_f32_e32 v3, v3, v6
	s_nop 1
	v_mov_b32_dpp v6, v3 quad_perm:[2,3,0,1] row_mask:0xf bank_mask:0xf
	s_waitcnt lgkmcnt(0)
	v_add_f32_e32 v5, v4, v5
	s_waitcnt lgkmcnt(0)
	v_add_f32_e32 v3, v3, v6
	s_nop 1
	v_mov_b32_dpp v4, v3 quad_perm:[1,0,3,2] row_mask:0xf bank_mask:0xf
	s_nop 1
	v_mov_b32_dpp v6, v5 quad_perm:[1,0,3,2] row_mask:0xf bank_mask:0xf
	s_and_saveexec_b64 s[2:3], s[6:7]
	s_cbranch_execz .LBB8_37
	s_waitcnt lgkmcnt(0)
	v_add_f32_e32 v5, v5, v6
	v_add_f32_e32 v5, v85, v5
	v_mad_u32_u24 v6, v68, 36, v86
	ds_write_b32 v6, v5
.LBB8_37:
	s_or_b64 exec, exec, s[2:3]
	s_and_saveexec_b64 s[4:5], s[8:9]
	s_cbranch_execz .LBB8_39
	s_waitcnt lgkmcnt(0)
	v_add_f32_e32 v3, v3, v4
	v_mov_b32_e32 v4, 0x3727c5ac
	v_fmac_f32_e32 v4, 0x3b000000, v3
	s_mov_b32 s2, 0xf800000
	v_mul_f32_e32 v3, 0x4f800000, v4
	v_cmp_gt_f32_e32 vcc, s2, v4
	v_mul_f32_e32 v2, 0x3b000000, v2
	s_nop 0
	v_cndmask_b32_e32 v3, v4, v3, vcc
	v_sqrt_f32_e32 v4, v3
	s_nop 0
	v_add_u32_e32 v5, -1, v4
	s_waitcnt lgkmcnt(0)
	v_fma_f32 v6, -v5, v4, v3
	v_cmp_ge_f32_e64 s[2:3], 0, v6
	v_add_u32_e32 v6, 1, v4
	s_nop 0
	v_cndmask_b32_e64 v5, v4, v5, s[2:3]
	v_fma_f32 v4, -v6, v4, v3
	v_cmp_lt_f32_e64 s[2:3], 0, v4
	s_nop 1
	v_cndmask_b32_e64 v4, v5, v6, s[2:3]
	v_mul_f32_e32 v5, 0x37800000, v4
	v_cndmask_b32_e32 v4, v4, v5, vcc
	v_mov_b32_e32 v5, 0x260
	v_cmp_class_f32_e32 vcc, v3, v5
	s_nop 1
	v_cndmask_b32_e32 v3, v4, v3, vcc
	v_div_scale_f32 v4, s[2:3], v3, v3, 1.0
	v_rcp_f32_e32 v5, v4
	s_nop 0
	v_fma_f32 v6, -v4, v5, 1.0
	v_fmac_f32_e32 v5, v6, v5
	v_div_scale_f32 v6, vcc, 1.0, v3, 1.0
	v_mul_f32_e32 v7, v6, v5
	v_fma_f32 v8, -v4, v7, v6
	v_fmac_f32_e32 v7, v8, v5
	v_fma_f32 v4, -v4, v7, v6
	v_div_fmas_f32 v4, v4, v5, v7
	v_div_fixup_f32 v3, v4, v3, 1.0
	v_lshlrev_b32_e32 v4, 1, v66
	v_ashrrev_i32_e32 v5, 31, v4
	v_lshl_add_u64 v[4:5], v[4:5], 2, s[14:15]
	global_store_dwordx2 v[4:5], v[2:3], off

	.amdhsa_kernel _Z18fused_router_wprepILb0EEvPKfS1_S1_PKiPfS4_PiS5_S5_S5_S4_S1_PDF16_S6_S1_S6_
		.amdhsa_group_segment_fixed_size 17792
		.amdhsa_private_segment_fixed_size 0
		.amdhsa_kernarg_size 128
		.amdhsa_user_sgpr_count 2
		.amdhsa_user_sgpr_dispatch_ptr 0
		.amdhsa_user_sgpr_queue_ptr 0
		.amdhsa_user_sgpr_kernarg_segment_ptr 1
		.amdhsa_user_sgpr_dispatch_id 0
		.amdhsa_user_sgpr_kernarg_preload_length 0
		.amdhsa_user_sgpr_kernarg_preload_offset 0
		.amdhsa_user_sgpr_private_segment_size 0
		.amdhsa_uses_dynamic_stack 0
		.amdhsa_enable_private_segment 0
		.amdhsa_system_sgpr_workgroup_id_x 1
		.amdhsa_system_sgpr_workgroup_id_y 0
		.amdhsa_system_sgpr_workgroup_id_z 0
		.amdhsa_system_sgpr_workgroup_info 0
		.amdhsa_system_vgpr_workitem_id 0
		.amdhsa_next_free_vgpr 100
		.amdhsa_next_free_sgpr 29
		.amdhsa_accum_offset 100
		.amdhsa_reserve_vcc 1
		.amdhsa_float_round_mode_32 0
		.amdhsa_float_round_mode_16_64 0
		.amdhsa_float_denorm_mode_32 3
		.amdhsa_float_denorm_mode_16_64 3
		.amdhsa_dx10_clamp 1
		.amdhsa_ieee_mode 1
		.amdhsa_fp16_overflow 0
		.amdhsa_tg_split 0
		.amdhsa_exception_fp_ieee_invalid_op 0
		.amdhsa_exception_fp_denorm_src 0
		.amdhsa_exception_fp_ieee_div_zero 0
		.amdhsa_exception_fp_ieee_overflow 0
		.amdhsa_exception_fp_ieee_underflow 0
		.amdhsa_exception_fp_ieee_inexact 0
		.amdhsa_exception_int_div_zero 0
	.end_amdhsa_kernel
